# LayerNorm and gMLP-LN wave reductions: serial ds_bpermute butterfly chains replaced by DPP and permlane-swap chains (bit-identical sums), on top of attention trims
# speedup vs baseline: 1.0229x; 1.0030x over previous
.LBB0_351:
	v_lshl_add_u64 v[6:7], v[46:47], 0, s[30:31]
	v_add_co_u32_e32 v2, vcc, 0x10a00000, v6
	s_nop 1
	v_addc_co_u32_e32 v3, vcc, 0, v7, vcc
	s_barrier
	global_load_dwordx4 v[2:5], v[2:3], off offset:512
	v_lshl_add_u64 v[6:7], v[6:7], 0, s[34:35]
	global_load_dwordx4 v[6:9], v[6:7], off offset:16
	v_add_u32_e32 v50, s30, v44
	v_ashrrev_i32_e32 v51, 31, v50
	s_waitcnt vmcnt(1)
	v_lshlrev_b32_e32 v10, 16, v2
	v_and_b32_e32 v2, 0xffff0000, v2
	v_add_f32_e32 v18, 0, v10
	v_lshlrev_b32_e32 v11, 16, v3
	v_add_f32_e32 v18, v18, v2
	v_and_b32_e32 v3, 0xffff0000, v3
	v_add_f32_e32 v18, v18, v11
	v_lshlrev_b32_e32 v12, 16, v4
	v_add_f32_e32 v18, v18, v3
	v_and_b32_e32 v4, 0xffff0000, v4
	v_add_f32_e32 v18, v18, v12
	v_lshlrev_b32_e32 v13, 16, v5
	v_add_f32_e32 v18, v18, v4
	v_and_b32_e32 v5, 0xffff0000, v5
	v_add_f32_e32 v18, v18, v13
	s_waitcnt vmcnt(0)
	v_lshlrev_b32_e32 v14, 16, v6
	v_add_f32_e32 v18, v18, v5
	v_and_b32_e32 v6, 0xffff0000, v6
	v_add_f32_e32 v18, v18, v14
	v_lshlrev_b32_e32 v15, 16, v7
	v_add_f32_e32 v18, v18, v6
	v_and_b32_e32 v7, 0xffff0000, v7
	v_add_f32_e32 v18, v18, v15
	v_lshlrev_b32_e32 v16, 16, v8
	v_add_f32_e32 v18, v18, v7
	v_and_b32_e32 v8, 0xffff0000, v8
	v_add_f32_e32 v18, v18, v16
	v_lshlrev_b32_e32 v17, 16, v9
	v_add_f32_e32 v18, v18, v8
	v_and_b32_e32 v9, 0xffff0000, v9
	v_add_f32_e32 v18, v18, v17
	v_add_f32_e32 v18, v18, v9
	s_waitcnt lgkmcnt(0)
	s_nop 1
	v_add_f32_dpp v18, v18, v18 quad_perm:[1,0,3,2] row_mask:0xf bank_mask:0xf
	s_nop 1
	v_add_f32_dpp v18, v18, v18 quad_perm:[2,3,0,1] row_mask:0xf bank_mask:0xf
	v_fmac_f32_e32 v2, 0xbc800000, v18
	v_fmac_f32_e32 v10, 0xbc800000, v18
	v_fmac_f32_e32 v11, 0xbc800000, v18
	v_fmac_f32_e32 v3, 0xbc800000, v18
	v_fmac_f32_e32 v12, 0xbc800000, v18
	v_fmac_f32_e32 v4, 0xbc800000, v18
	v_fmac_f32_e32 v13, 0xbc800000, v18
	v_fmac_f32_e32 v5, 0xbc800000, v18
	v_fmac_f32_e32 v14, 0xbc800000, v18
	v_fmac_f32_e32 v6, 0xbc800000, v18
	v_fmac_f32_e32 v15, 0xbc800000, v18
	v_fmac_f32_e32 v7, 0xbc800000, v18
	v_fmac_f32_e32 v16, 0xbc800000, v18
	v_fmac_f32_e32 v8, 0xbc800000, v18
	v_fmac_f32_e32 v17, 0xbc800000, v18
	v_fmac_f32_e32 v9, 0xbc800000, v18
	v_mul_f32_e32 v18, v2, v2
	v_fmac_f32_e32 v18, v10, v10
	v_fmac_f32_e32 v18, v11, v11
	v_fmac_f32_e32 v18, v3, v3
	v_fmac_f32_e32 v18, v12, v12
	v_fmac_f32_e32 v18, v4, v4
	v_fmac_f32_e32 v18, v13, v13
	v_fmac_f32_e32 v18, v5, v5
	v_fmac_f32_e32 v18, v14, v14
	v_fmac_f32_e32 v18, v6, v6
	v_fmac_f32_e32 v18, v15, v15
	v_fmac_f32_e32 v18, v7, v7
	v_fmac_f32_e32 v18, v16, v16
	v_fmac_f32_e32 v18, v8, v8
	v_fmac_f32_e32 v18, v17, v17
	v_fmac_f32_e32 v18, v9, v9
	s_waitcnt lgkmcnt(0)
	s_nop 1
	v_add_f32_dpp v18, v18, v18 quad_perm:[1,0,3,2] row_mask:0xf bank_mask:0xf
	s_nop 1
	v_add_f32_dpp v18, v18, v18 quad_perm:[2,3,0,1] row_mask:0xf bank_mask:0xf
	v_fmamk_f32 v18, v18, 0x3c800000, v39
	v_mul_f32_e32 v19, 0x4f800000, v18
	v_cmp_gt_f32_e32 vcc, s33, v18
	s_nop 1
	v_cndmask_b32_e32 v18, v18, v19, vcc
	v_sqrt_f32_e32 v19, v18
	s_nop 0
	v_add_u32_e32 v20, -1, v19
	v_add_u32_e32 v21, 1, v19
	v_fma_f32 v22, -v20, v19, v18
	v_fma_f32 v23, -v21, v19, v18
	v_cmp_ge_f32_e64 s[0:1], 0, v22
	s_nop 1
	v_cndmask_b32_e64 v19, v19, v20, s[0:1]
	v_cmp_lt_f32_e64 s[0:1], 0, v23
	s_nop 1
	v_cndmask_b32_e64 v19, v19, v21, s[0:1]
	v_mul_f32_e32 v20, 0x37800000, v19
	v_cndmask_b32_e32 v19, v19, v20, vcc
	v_cmp_class_f32_e32 vcc, v18, v54
	s_nop 1
	v_cndmask_b32_e32 v18, v19, v18, vcc
	v_div_scale_f32 v19, s[0:1], v18, v18, 1.0
	v_rcp_f32_e32 v20, v19
	v_div_scale_f32 v21, vcc, 1.0, v18, 1.0
	v_fma_f32 v22, -v19, v20, 1.0
	v_fmac_f32_e32 v20, v22, v20
	v_mul_f32_e32 v22, v21, v20
	v_fma_f32 v23, -v19, v22, v21
	v_fmac_f32_e32 v22, v23, v20
	v_fma_f32 v19, -v19, v22, v21
	v_div_fmas_f32 v19, v19, v20, v22
	v_div_fixup_f32 v18, v19, v18, 1.0
	v_mul_f32_e32 v10, v10, v18
	v_mul_f32_e32 v2, v2, v18
	v_mul_f32_e32 v11, v11, v18
	v_mul_f32_e32 v3, v3, v18
	v_mul_f32_e32 v12, v12, v18
	v_mul_f32_e32 v4, v4, v18
	v_mul_f32_e32 v13, v13, v18
	v_mul_f32_e32 v5, v5, v18
	v_mul_f32_e32 v14, v14, v18
	v_mul_f32_e32 v6, v6, v18
	v_mul_f32_e32 v15, v15, v18
	v_mul_f32_e32 v7, v7, v18
	v_mul_f32_e32 v16, v16, v18
	v_mul_f32_e32 v8, v8, v18
	v_bfe_u32 v19, v10, 16, 1
	v_bfe_u32 v20, v2, 16, 1
	v_mul_f32_e32 v17, v17, v18
	v_bfe_u32 v21, v11, 16, 1
	v_bfe_u32 v22, v3, 16, 1
	v_bfe_u32 v23, v12, 16, 1
	v_bfe_u32 v24, v4, 16, 1
	v_bfe_u32 v25, v13, 16, 1
	v_bfe_u32 v26, v5, 16, 1
	v_bfe_u32 v27, v14, 16, 1
	v_bfe_u32 v28, v6, 16, 1
	v_bfe_u32 v29, v15, 16, 1
	v_bfe_u32 v30, v7, 16, 1
	v_bfe_u32 v31, v16, 16, 1
	v_bfe_u32 v32, v8, 16, 1
	v_add3_u32 v10, v10, v19, s37
	v_add3_u32 v2, v2, v20, s37
	v_add3_u32 v11, v11, v21, s37
	v_add3_u32 v3, v3, v22, s37
	v_add3_u32 v12, v12, v23, s37
	v_add3_u32 v4, v4, v24, s37
	v_add3_u32 v13, v13, v25, s37
	v_add3_u32 v5, v5, v26, s37
	v_add3_u32 v14, v14, v27, s37
	v_add3_u32 v6, v6, v28, s37
	v_add3_u32 v15, v15, v29, s37
	v_add3_u32 v7, v7, v30, s37
	v_add3_u32 v16, v16, v31, s37
	v_add3_u32 v8, v8, v32, s37
	ds_write_b16_d16_hi v56, v10
	ds_write_b16_d16_hi v56, v2 offset:272
	ds_write_b16_d16_hi v56, v11 offset:544
	ds_write_b16_d16_hi v56, v3 offset:816
	ds_write_b16_d16_hi v56, v12 offset:1088
	ds_write_b16_d16_hi v56, v4 offset:1360
	ds_write_b16_d16_hi v56, v13 offset:1632
	ds_write_b16_d16_hi v56, v5 offset:1904
	ds_write_b16_d16_hi v56, v14 offset:2176
	ds_write_b16_d16_hi v56, v6 offset:2448
	ds_write_b16_d16_hi v56, v15 offset:2720
	ds_write_b16_d16_hi v56, v7 offset:2992
	ds_write_b16_d16_hi v56, v16 offset:3264
	ds_write_b16_d16_hi v56, v8 offset:3536
	v_bfe_u32 v2, v17, 16, 1
	v_add3_u32 v2, v17, v2, s37
	ds_write_b16_d16_hi v56, v2 offset:3808
	v_mul_f32_e32 v2, v9, v18
	v_bfe_u32 v3, v2, 16, 1
	v_add3_u32 v2, v2, v3, s37
	ds_write_b16_d16_hi v56, v2 offset:4080
	v_lshlrev_b64 v[2:3], 8, v[50:51]
	s_and_b64 vcc, exec, s[2:3]
	v_lshl_add_u64 v[2:3], v[42:43], 0, v[2:3]
	s_cbranch_vccnz .LBB0_356
	global_load_dwordx4 v[30:33], v[2:3], off
	v_cndmask_b32_e64 v4, 0, 1, s[24:25]
	v_cmp_ne_u32_e64 s[8:9], 1, v4
	s_andn2_b64 vcc, exec, s[24:25]
	s_cbranch_vccz .LBB0_357

.LBB0_617:
	s_waitcnt vmcnt(7)
	v_lshlrev_b32_e32 v87, 16, v59
	v_lshlrev_b32_e32 v86, 16, v58
	v_and_b32_e32 v59, 0xffff0000, v59
	v_and_b32_e32 v58, 0xffff0000, v58
	v_pk_add_f32 v[88:89], v[86:87], v[58:59]
	s_waitcnt vmcnt(6)
	v_lshlrev_b32_e32 v82, 16, v65
	v_and_b32_e32 v84, 0xffff0000, v65
	v_add_f32_e32 v65, v88, v89
	v_lshlrev_b32_e32 v89, 16, v61
	v_lshlrev_b32_e32 v88, 16, v60
	v_and_b32_e32 v61, 0xffff0000, v61
	v_and_b32_e32 v60, 0xffff0000, v60
	v_pk_add_f32 v[90:91], v[88:89], v[60:61]
	v_lshlrev_b32_e32 v72, 16, v62
	v_and_b32_e32 v73, 0xffff0000, v62
	v_lshlrev_b32_e32 v62, 16, v63
	v_and_b32_e32 v63, 0xffff0000, v63
	v_pk_add_f32 v[90:91], v[90:91], v[90:91] op_sel_hi:[0,1]
	v_lshlrev_b32_e32 v80, 16, v64
	v_and_b32_e32 v64, 0xffff0000, v64
	v_add_f32_e32 v85, 0, v65
	v_add_f32_e32 v81, v72, v73
	v_add_f32_e32 v65, v62, v63
	v_mov_b32_e32 v83, v91
	v_pk_add_f32 v[92:93], v[80:81], v[64:65]
	v_pk_add_f32 v[90:91], v[82:83], v[84:85]
	s_add_i32 s4, s4, 4
	v_pk_add_f32 v[90:91], v[92:93], v[90:91]
	s_cmp_lt_u32 s4, 12
	v_add_f32_e32 v65, v90, v91
	s_waitcnt lgkmcnt(0)
	s_nop 1
	v_add_f32_dpp v65, v65, v65 quad_perm:[1,0,3,2] row_mask:0xf bank_mask:0xf
	s_nop 1
	v_add_f32_dpp v65, v65, v65 quad_perm:[2,3,0,1] row_mask:0xf bank_mask:0xf
	s_nop 1
	v_add_f32_dpp v65, v65, v65 row_half_mirror row_mask:0xf bank_mask:0xf
	s_nop 1
	v_add_f32_dpp v65, v65, v65 row_mirror row_mask:0xf bank_mask:0xf
	v_mov_b32_e32 v81, v65
	s_nop 1
	v_permlane16_swap_b32_e32 v65, v81
	v_add_f32_e32 v65, v65, v81
	v_mov_b32_e32 v81, v65
	s_nop 1
	v_permlane32_swap_b32_e32 v65, v81
	v_add_f32_e32 v65, v65, v81
	v_fmac_f32_e32 v58, 0xba800000, v65
	v_fmac_f32_e32 v59, 0xba800000, v65
	v_fmac_f32_e32 v87, 0xba800000, v65
	v_fmac_f32_e32 v86, 0xba800000, v65
	v_mov_b32_e32 v90, v87
	v_mov_b32_e32 v91, v59
	v_mov_b32_e32 v87, v58
	v_pk_mul_f32 v[92:93], v[90:91], v[90:91]
	v_pk_mul_f32 v[58:59], v[86:87], v[86:87]
	v_fmac_f32_e32 v60, 0xba800000, v65
	v_pk_mov_b32 v[94:95], v[58:59], v[92:93] op_sel:[1,0]
	v_mov_b32_e32 v59, v93
	v_fmac_f32_e32 v61, 0xba800000, v65
	v_fmac_f32_e32 v89, 0xba800000, v65
	v_pk_add_f32 v[58:59], v[94:95], v[58:59]
	v_fmac_f32_e32 v88, 0xba800000, v65
	v_mov_b32_e32 v92, v89
	v_mov_b32_e32 v93, v61
	v_mov_b32_e32 v89, v60
	v_pk_add_f32 v[58:59], v[58:59], v[58:59] op_sel_hi:[0,1]
	v_pk_mul_f32 v[94:95], v[92:93], v[92:93]
	v_pk_mul_f32 v[60:61], v[88:89], v[88:89]
	v_fmac_f32_e32 v72, 0xba800000, v65
	v_pk_mov_b32 v[96:97], v[60:61], v[94:95] op_sel:[1,0]
	v_mov_b32_e32 v61, v95
	v_fmac_f32_e32 v73, 0xba800000, v65
	v_fmac_f32_e32 v62, 0xba800000, v65
	v_mul_f32_e32 v58, v72, v72
	v_pk_add_f32 v[60:61], v[96:97], v[60:61]
	v_fmac_f32_e32 v63, 0xba800000, v65
	v_pk_fma_f32 v[94:95], v[72:73], v[72:73], v[58:59] op_sel_hi:[1,1,0]
	v_mul_f32_e32 v58, v62, v62
	v_pk_add_f32 v[60:61], v[60:61], v[60:61] op_sel_hi:[0,1]
	v_pk_fma_f32 v[96:97], v[62:63], v[62:63], v[58:59] op_sel_hi:[1,1,0]
	v_fmac_f32_e32 v84, 0xba800000, v65
	v_fmac_f32_e32 v82, 0xba800000, v65
	v_fmac_f32_e32 v64, 0xba800000, v65
	v_fmac_f32_e32 v80, 0xba800000, v65
	v_mul_f32_e32 v94, v80, v80
	v_mul_f32_e32 v96, v64, v64
	v_mul_f32_e32 v58, v82, v82
	v_mul_f32_e32 v60, v84, v84
	v_pk_add_f32 v[94:95], v[94:95], v[96:97]
	v_pk_add_f32 v[58:59], v[58:59], v[60:61]
	v_mov_b32_e32 v83, v84
	v_pk_add_f32 v[58:59], v[94:95], v[58:59]
	s_nop 0
	v_add_f32_e32 v58, v58, v59
	s_waitcnt lgkmcnt(0)
	s_nop 1
	v_add_f32_dpp v58, v58, v58 quad_perm:[1,0,3,2] row_mask:0xf bank_mask:0xf
	s_nop 1
	v_add_f32_dpp v58, v58, v58 quad_perm:[2,3,0,1] row_mask:0xf bank_mask:0xf
	s_nop 1
	v_add_f32_dpp v58, v58, v58 row_half_mirror row_mask:0xf bank_mask:0xf
	s_nop 1
	v_add_f32_dpp v58, v58, v58 row_mirror row_mask:0xf bank_mask:0xf
	v_mov_b32_e32 v59, v58
	s_nop 1
	v_permlane16_swap_b32_e32 v58, v59
	v_add_f32_e32 v58, v58, v59
	v_mov_b32_e32 v59, v58
	s_nop 1
	v_permlane32_swap_b32_e32 v58, v59
	v_add_f32_e32 v58, v58, v59
	v_fmamk_f32 v58, v58, 0x3a800000, v78
	v_mul_f32_e32 v59, 0x4f800000, v58
	v_cmp_gt_f32_e32 vcc, s6, v58
	s_nop 1
	v_cndmask_b32_e32 v58, v58, v59, vcc
	v_sqrt_f32_e32 v59, v58
	s_nop 0
	v_add_u32_e32 v60, -1, v59
	v_fma_f32 v61, -v60, v59, v58
	v_cmp_ge_f32_e64 s[0:1], 0, v61
	v_add_u32_e32 v61, 1, v59
	s_nop 0
	v_cndmask_b32_e64 v60, v59, v60, s[0:1]
	v_fma_f32 v59, -v61, v59, v58
	v_cmp_lt_f32_e64 s[0:1], 0, v59
	s_nop 1
	v_cndmask_b32_e64 v59, v60, v61, s[0:1]
	v_mul_f32_e32 v60, 0x37800000, v59
	v_cndmask_b32_e32 v59, v59, v60, vcc
	v_cmp_class_f32_e32 vcc, v58, v79
	s_nop 1
	v_cndmask_b32_e32 v58, v59, v58, vcc
	v_div_scale_f32 v59, s[0:1], v58, v58, 1.0
	v_rcp_f32_e32 v60, v59
	s_nop 0
	v_fma_f32 v61, -v59, v60, 1.0
	v_fmac_f32_e32 v60, v61, v60
	v_div_scale_f32 v61, vcc, 1.0, v58, 1.0
	v_mul_f32_e32 v65, v61, v60
	v_fma_f32 v81, -v59, v65, v61
	v_fmac_f32_e32 v65, v81, v60
	v_fma_f32 v59, -v59, v65, v61
	v_div_fmas_f32 v59, v59, v60, v65
	v_div_fixup_f32 v58, v59, v58, 1.0
	v_pk_mul_f32 v[60:61], v[86:87], v[58:59] op_sel_hi:[1,0]
	v_mov_b32_e32 v81, v64
	v_pk_mul_f32 v[86:87], v[90:91], v[58:59] op_sel_hi:[1,0]
	v_pk_fma_f32 v[60:61], v[10:11], v[60:61], v[14:15]
	v_pk_mul_f32 v[88:89], v[88:89], v[58:59] op_sel_hi:[1,0]
	v_pk_mul_f32 v[90:91], v[92:93], v[58:59] op_sel_hi:[1,0]
	v_pk_mul_f32 v[72:73], v[72:73], v[58:59] op_sel_hi:[1,0]
	v_pk_mul_f32 v[62:63], v[62:63], v[58:59] op_sel_hi:[1,0]
	v_pk_mul_f32 v[64:65], v[80:81], v[58:59] op_sel_hi:[1,0]
	v_pk_mul_f32 v[58:59], v[82:83], v[58:59] op_sel_hi:[1,0]
	v_pk_fma_f32 v[86:87], v[12:13], v[86:87], v[16:17]
	v_pk_fma_f32 v[80:81], v[20:21], v[58:59], v[24:25]
	v_bfe_u32 v58, v60, 16, 1
	v_add3_u32 v58, v60, v58, s7
	v_bfe_u32 v59, v61, 16, 1
	v_lshrrev_b32_e32 v58, 16, v58
	v_add3_u32 v59, v61, v59, s7
	v_and_or_b32 v58, v59, s5, v58
	v_bfe_u32 v59, v86, 16, 1
	v_add3_u32 v59, v86, v59, s7
	v_bfe_u32 v60, v87, 16, 1
	v_pk_fma_f32 v[88:89], v[2:3], v[88:89], v[6:7]
	v_lshrrev_b32_e32 v59, 16, v59
	v_add3_u32 v60, v87, v60, s7
	v_and_or_b32 v59, v60, s5, v59
	v_bfe_u32 v60, v88, 16, 1
	v_add3_u32 v60, v88, v60, s7
	v_bfe_u32 v61, v89, 16, 1
	v_pk_fma_f32 v[90:91], v[4:5], v[90:91], v[8:9]
	v_lshrrev_b32_e32 v60, 16, v60
	v_add3_u32 v61, v89, v61, s7
	v_and_or_b32 v60, v61, s5, v60
	v_bfe_u32 v61, v90, 16, 1
	v_add3_u32 v61, v90, v61, s7
	v_bfe_u32 v82, v91, 16, 1
	v_lshrrev_b32_e32 v61, 16, v61
	v_add3_u32 v82, v91, v82, s7
	v_pk_fma_f32 v[72:73], v[26:27], v[72:73], v[30:31]
	v_and_or_b32 v61, v82, s5, v61
	global_store_dwordx4 v[70:71], v[58:61], off offset:-1024
	v_pk_fma_f32 v[62:63], v[28:29], v[62:63], v[32:33]
	v_pk_fma_f32 v[64:65], v[18:19], v[64:65], v[22:23]
	v_bfe_u32 v58, v72, 16, 1
	v_add3_u32 v58, v72, v58, s7
	v_bfe_u32 v59, v73, 16, 1
	v_lshrrev_b32_e32 v58, 16, v58
	v_add3_u32 v59, v73, v59, s7
	v_and_or_b32 v58, v59, s5, v58
	v_bfe_u32 v59, v62, 16, 1
	v_add3_u32 v59, v62, v59, s7
	v_bfe_u32 v60, v63, 16, 1
	v_lshrrev_b32_e32 v59, 16, v59
	v_add3_u32 v60, v63, v60, s7
	v_and_or_b32 v59, v60, s5, v59
	v_bfe_u32 v60, v64, 16, 1
	v_add3_u32 v60, v64, v60, s7
	v_bfe_u32 v61, v65, 16, 1
	v_lshrrev_b32_e32 v60, 16, v60
	v_add3_u32 v61, v65, v61, s7
	v_and_or_b32 v60, v61, s5, v60
	v_bfe_u32 v61, v80, 16, 1
	v_add3_u32 v61, v80, v61, s7
	v_bfe_u32 v62, v81, 16, 1
	v_lshrrev_b32_e32 v61, 16, v61
	v_add3_u32 v62, v81, v62, s7
	v_and_or_b32 v61, v62, s5, v61
	global_store_dwordx4 v[70:71], v[58:61], off
	v_lshl_add_u64 v[70:71], v[70:71], 0, s[2:3]
	s_cbranch_scc0 .LBB0_624
.LBB0_618:
	s_waitcnt vmcnt(5)
	v_lshlrev_b32_e32 v91, 16, v35
	v_lshlrev_b32_e32 v90, 16, v34
	v_and_b32_e32 v59, 0xffff0000, v35
	v_and_b32_e32 v58, 0xffff0000, v34
	v_pk_add_f32 v[60:61], v[90:91], v[58:59]
	v_lshlrev_b32_e32 v93, 16, v37
	v_add_f32_e32 v60, v60, v61
	v_add_f32_e32 v89, 0, v60
	v_lshlrev_b32_e32 v92, 16, v36
	v_and_b32_e32 v61, 0xffff0000, v37
	v_and_b32_e32 v60, 0xffff0000, v36
	v_pk_add_f32 v[62:63], v[92:93], v[60:61]
	s_waitcnt vmcnt(4)
	v_lshlrev_b32_e32 v72, 16, v38
	v_and_b32_e32 v73, 0xffff0000, v38
	v_lshlrev_b32_e32 v80, 16, v39
	v_and_b32_e32 v81, 0xffff0000, v39
	v_pk_add_f32 v[62:63], v[62:63], v[62:63] op_sel_hi:[0,1]
	v_lshlrev_b32_e32 v82, 16, v40
	v_and_b32_e32 v84, 0xffff0000, v40
	v_lshlrev_b32_e32 v86, 16, v41
	v_and_b32_e32 v88, 0xffff0000, v41
	v_add_f32_e32 v83, v72, v73
	v_add_f32_e32 v85, v80, v81
	v_mov_b32_e32 v87, v63
	v_pk_add_f32 v[64:65], v[82:83], v[84:85]
	v_pk_add_f32 v[62:63], v[86:87], v[88:89]
	s_nop 0
	v_pk_add_f32 v[62:63], v[64:65], v[62:63]
	s_nop 0
	v_add_f32_e32 v62, v62, v63
	s_waitcnt lgkmcnt(0)
	s_nop 1
	v_add_f32_dpp v62, v62, v62 quad_perm:[1,0,3,2] row_mask:0xf bank_mask:0xf
	s_nop 1
	v_add_f32_dpp v62, v62, v62 quad_perm:[2,3,0,1] row_mask:0xf bank_mask:0xf
	s_nop 1
	v_add_f32_dpp v62, v62, v62 row_half_mirror row_mask:0xf bank_mask:0xf
	s_nop 1
	v_add_f32_dpp v62, v62, v62 row_mirror row_mask:0xf bank_mask:0xf
	v_mov_b32_e32 v63, v62
	s_nop 1
	v_permlane16_swap_b32_e32 v62, v63
	v_add_f32_e32 v62, v62, v63
	v_mov_b32_e32 v63, v62
	s_nop 1
	v_permlane32_swap_b32_e32 v62, v63
	v_add_f32_e32 v83, v62, v63
	v_fmac_f32_e32 v58, 0xba800000, v83
	v_fmac_f32_e32 v59, 0xba800000, v83
	v_fmac_f32_e32 v91, 0xba800000, v83
	v_fmac_f32_e32 v90, 0xba800000, v83
	v_mov_b32_e32 v94, v91
	v_mov_b32_e32 v95, v59
	v_mov_b32_e32 v91, v58
	v_pk_mul_f32 v[62:63], v[94:95], v[94:95]
	v_pk_mul_f32 v[58:59], v[90:91], v[90:91]
	v_fmac_f32_e32 v60, 0xba800000, v83
	v_pk_mov_b32 v[64:65], v[58:59], v[62:63] op_sel:[1,0]
	v_mov_b32_e32 v59, v63
	v_fmac_f32_e32 v61, 0xba800000, v83
	v_fmac_f32_e32 v93, 0xba800000, v83
	v_pk_add_f32 v[58:59], v[64:65], v[58:59]
	v_fmac_f32_e32 v92, 0xba800000, v83
	v_mov_b32_e32 v96, v93
	v_mov_b32_e32 v97, v61
	v_mov_b32_e32 v93, v60
	v_pk_add_f32 v[58:59], v[58:59], v[58:59] op_sel_hi:[0,1]
	v_pk_mul_f32 v[62:63], v[96:97], v[96:97]
	v_pk_mul_f32 v[60:61], v[92:93], v[92:93]
	v_fmac_f32_e32 v72, 0xba800000, v83
	v_pk_mov_b32 v[64:65], v[60:61], v[62:63] op_sel:[1,0]
	v_mov_b32_e32 v61, v63
	v_fmac_f32_e32 v73, 0xba800000, v83
	v_fmac_f32_e32 v80, 0xba800000, v83
	v_mul_f32_e32 v58, v72, v72
	v_pk_add_f32 v[60:61], v[64:65], v[60:61]
	v_fmac_f32_e32 v81, 0xba800000, v83
	v_pk_fma_f32 v[62:63], v[72:73], v[72:73], v[58:59] op_sel_hi:[1,1,0]
	v_mul_f32_e32 v58, v80, v80
	v_pk_add_f32 v[60:61], v[60:61], v[60:61] op_sel_hi:[0,1]
	v_pk_fma_f32 v[64:65], v[80:81], v[80:81], v[58:59] op_sel_hi:[1,1,0]
	v_fmac_f32_e32 v88, 0xba800000, v83
	v_fmac_f32_e32 v86, 0xba800000, v83
	v_fmac_f32_e32 v84, 0xba800000, v83
	v_fmac_f32_e32 v82, 0xba800000, v83
	v_mul_f32_e32 v62, v82, v82
	v_mul_f32_e32 v64, v84, v84
	v_mul_f32_e32 v58, v86, v86
	v_mul_f32_e32 v60, v88, v88
	v_pk_add_f32 v[62:63], v[62:63], v[64:65]
	v_pk_add_f32 v[58:59], v[58:59], v[60:61]
	s_nop 0
	v_pk_add_f32 v[58:59], v[62:63], v[58:59]
	s_nop 0
	v_add_f32_e32 v58, v58, v59
	s_waitcnt lgkmcnt(0)
	s_nop 1
	v_add_f32_dpp v58, v58, v58 quad_perm:[1,0,3,2] row_mask:0xf bank_mask:0xf
	s_nop 1
	v_add_f32_dpp v58, v58, v58 quad_perm:[2,3,0,1] row_mask:0xf bank_mask:0xf
	s_nop 1
	v_add_f32_dpp v58, v58, v58 row_half_mirror row_mask:0xf bank_mask:0xf
	s_nop 1
	v_add_f32_dpp v58, v58, v58 row_mirror row_mask:0xf bank_mask:0xf
	v_mov_b32_e32 v59, v58
	s_nop 1
	v_permlane16_swap_b32_e32 v58, v59
	v_add_f32_e32 v58, v58, v59
	v_mov_b32_e32 v59, v58
	s_nop 1
	v_permlane32_swap_b32_e32 v58, v59
	v_add_f32_e32 v58, v58, v59
	v_fmamk_f32 v58, v58, 0x3a800000, v78
	v_mul_f32_e32 v59, 0x4f800000, v58
	v_cmp_gt_f32_e32 vcc, s6, v58
	s_nop 1
	v_cndmask_b32_e32 v58, v58, v59, vcc
	v_sqrt_f32_e32 v59, v58
	s_nop 0
	v_add_u32_e32 v60, -1, v59
	v_fma_f32 v61, -v60, v59, v58
	v_cmp_ge_f32_e64 s[0:1], 0, v61
	v_add_u32_e32 v61, 1, v59
	s_nop 0
	v_cndmask_b32_e64 v60, v59, v60, s[0:1]
	v_fma_f32 v59, -v61, v59, v58
	v_cmp_lt_f32_e64 s[0:1], 0, v59
	s_nop 1
	v_cndmask_b32_e64 v59, v60, v61, s[0:1]
	v_mul_f32_e32 v60, 0x37800000, v59
	v_cndmask_b32_e32 v59, v59, v60, vcc
	v_cmp_class_f32_e32 vcc, v58, v79
	s_nop 1
	v_cndmask_b32_e32 v83, v59, v58, vcc
	global_load_dwordx4 v[58:61], v[70:71], off offset:-1024
	global_load_dwordx4 v[62:65], v[70:71], off
	v_div_scale_f32 v85, s[0:1], v83, v83, 1.0
	v_rcp_f32_e32 v87, v85
	s_add_i32 s0, s4, 5
	s_cmp_gt_u32 s0, 12
	v_fma_f32 v89, -v85, v87, 1.0
	v_fmac_f32_e32 v87, v89, v87
	v_div_scale_f32 v89, vcc, 1.0, v83, 1.0
	v_mul_f32_e32 v98, v89, v87
	v_fma_f32 v99, -v85, v98, v89
	v_fmac_f32_e32 v98, v99, v87
	v_fma_f32 v85, -v85, v98, v89
	v_div_fmas_f32 v85, v85, v87, v98
	v_div_fixup_f32 v98, v85, v83, 1.0
	v_pk_mul_f32 v[90:91], v[90:91], v[98:99] op_sel_hi:[1,0]
	v_pk_mul_f32 v[72:73], v[72:73], v[98:99] op_sel_hi:[1,0]
	v_mov_b32_e32 v83, v84
	v_pk_fma_f32 v[90:91], v[10:11], v[90:91], v[14:15]
	v_pk_mul_f32 v[80:81], v[80:81], v[98:99] op_sel_hi:[1,0]
	v_pk_fma_f32 v[102:103], v[26:27], v[72:73], v[30:31]
	v_pk_mul_f32 v[72:73], v[82:83], v[98:99] op_sel_hi:[1,0]
	v_mov_b32_e32 v87, v88
	v_pk_fma_f32 v[100:101], v[28:29], v[80:81], v[32:33]
	v_pk_mul_f32 v[80:81], v[86:87], v[98:99] op_sel_hi:[1,0]
	v_pk_fma_f32 v[86:87], v[18:19], v[72:73], v[22:23]
	v_bfe_u32 v72, v90, 16, 1
	v_pk_mul_f32 v[94:95], v[94:95], v[98:99] op_sel_hi:[1,0]
	v_add3_u32 v72, v90, v72, s7
	v_bfe_u32 v73, v91, 16, 1
	v_pk_fma_f32 v[94:95], v[12:13], v[94:95], v[16:17]
	v_lshrrev_b32_e32 v72, 16, v72
	v_add3_u32 v73, v91, v73, s7
	v_pk_fma_f32 v[84:85], v[20:21], v[80:81], v[24:25]
	v_and_or_b32 v80, v73, s5, v72
	v_bfe_u32 v72, v94, 16, 1
	v_pk_mul_f32 v[92:93], v[92:93], v[98:99] op_sel_hi:[1,0]
	v_add3_u32 v72, v94, v72, s7
	v_bfe_u32 v73, v95, 16, 1
	v_pk_fma_f32 v[92:93], v[2:3], v[92:93], v[6:7]
	v_lshrrev_b32_e32 v72, 16, v72
	v_add3_u32 v73, v95, v73, s7
	v_and_or_b32 v81, v73, s5, v72
	v_bfe_u32 v72, v92, 16, 1
	v_pk_mul_f32 v[96:97], v[96:97], v[98:99] op_sel_hi:[1,0]
	v_add3_u32 v72, v92, v72, s7
	v_bfe_u32 v73, v93, 16, 1
	v_pk_fma_f32 v[96:97], v[4:5], v[96:97], v[8:9]
	v_lshrrev_b32_e32 v72, 16, v72
	v_add3_u32 v73, v93, v73, s7
	v_and_or_b32 v82, v73, s5, v72
	v_bfe_u32 v72, v96, 16, 1
	v_add3_u32 v72, v96, v72, s7
	v_bfe_u32 v73, v97, 16, 1
	v_lshrrev_b32_e32 v72, 16, v72
	v_add3_u32 v73, v97, v73, s7
	v_and_or_b32 v83, v73, s5, v72
	v_add_co_u32_e32 v72, vcc, s8, v70
	s_nop 1
	v_addc_co_u32_e32 v73, vcc, -1, v71, vcc
	global_store_dwordx4 v[72:73], v[80:83], off offset:-3072
	s_nop 1
	v_bfe_u32 v80, v102, 16, 1
	v_add3_u32 v80, v102, v80, s7
	v_bfe_u32 v81, v103, 16, 1
	v_lshrrev_b32_e32 v80, 16, v80
	v_add3_u32 v81, v103, v81, s7
	v_and_or_b32 v80, v81, s5, v80
	v_bfe_u32 v81, v100, 16, 1
	v_add3_u32 v81, v100, v81, s7
	v_bfe_u32 v82, v101, 16, 1
	v_lshrrev_b32_e32 v81, 16, v81
	v_add3_u32 v82, v101, v82, s7
	v_and_or_b32 v81, v82, s5, v81
	v_bfe_u32 v82, v86, 16, 1
	v_add3_u32 v82, v86, v82, s7
	v_bfe_u32 v83, v87, 16, 1
	v_lshrrev_b32_e32 v82, 16, v82
	v_add3_u32 v83, v87, v83, s7
	v_and_or_b32 v82, v83, s5, v82
	v_bfe_u32 v83, v84, 16, 1
	v_add3_u32 v83, v84, v83, s7
	v_bfe_u32 v84, v85, 16, 1
	v_lshrrev_b32_e32 v83, 16, v83
	v_add3_u32 v84, v85, v84, s7
	v_and_or_b32 v83, v84, s5, v83
	global_store_dwordx4 v[72:73], v[80:83], off offset:-2048
	s_cbranch_scc1 .LBB0_620
	v_add3_u32 v34, v66, s4, 8
	v_ashrrev_i32_e32 v35, 31, v34
	v_lshlrev_b64 v[34:35], 11, v[34:35]
	v_lshl_add_u64 v[38:39], v[68:69], 0, v[34:35]
	global_load_dwordx4 v[34:37], v[38:39], off
	s_nop 0
	global_load_dwordx4 v[38:41], v[38:39], off offset:1024
.LBB0_620:
	s_waitcnt vmcnt(7)
	v_lshlrev_b32_e32 v93, 16, v43
	v_lshlrev_b32_e32 v92, 16, v42
	v_and_b32_e32 v95, 0xffff0000, v43
	v_and_b32_e32 v94, 0xffff0000, v42
	v_pk_add_f32 v[96:97], v[92:93], v[94:95]
	v_and_b32_e32 v99, 0xffff0000, v45
	v_add_f32_e32 v85, v96, v97
	v_lshlrev_b32_e32 v97, 16, v45
	v_lshlrev_b32_e32 v96, 16, v44
	v_and_b32_e32 v98, 0xffff0000, v44
	v_pk_add_f32 v[100:101], v[96:97], v[98:99]
	s_waitcnt vmcnt(6)
	v_lshlrev_b32_e32 v80, 16, v46
	v_and_b32_e32 v81, 0xffff0000, v46
	v_lshlrev_b32_e32 v82, 16, v47
	v_and_b32_e32 v83, 0xffff0000, v47
	v_pk_add_f32 v[100:101], v[100:101], v[100:101] op_sel_hi:[0,1]
	v_lshlrev_b32_e32 v84, 16, v48
	v_and_b32_e32 v86, 0xffff0000, v48
	v_lshlrev_b32_e32 v88, 16, v49
	v_and_b32_e32 v90, 0xffff0000, v49
	v_add_f32_e32 v91, 0, v85
	v_add_f32_e32 v85, v80, v81
	v_add_f32_e32 v87, v82, v83
	v_mov_b32_e32 v89, v101
	v_pk_add_f32 v[102:103], v[84:85], v[86:87]
	v_pk_add_f32 v[100:101], v[88:89], v[90:91]
	s_nop 0
	v_pk_add_f32 v[100:101], v[102:103], v[100:101]
	s_nop 0
	v_add_f32_e32 v85, v100, v101
	s_waitcnt lgkmcnt(0)
	s_nop 1
	v_add_f32_dpp v85, v85, v85 quad_perm:[1,0,3,2] row_mask:0xf bank_mask:0xf
	s_nop 1
	v_add_f32_dpp v85, v85, v85 quad_perm:[2,3,0,1] row_mask:0xf bank_mask:0xf
	s_nop 1
	v_add_f32_dpp v85, v85, v85 row_half_mirror row_mask:0xf bank_mask:0xf
	s_nop 1
	v_add_f32_dpp v85, v85, v85 row_mirror row_mask:0xf bank_mask:0xf
	v_mov_b32_e32 v87, v85
	s_nop 1
	v_permlane16_swap_b32_e32 v85, v87
	v_add_f32_e32 v85, v85, v87
	v_mov_b32_e32 v87, v85
	s_nop 1
	v_permlane32_swap_b32_e32 v85, v87
	v_add_f32_e32 v85, v85, v87
	v_fmac_f32_e32 v94, 0xba800000, v85
	v_fmac_f32_e32 v95, 0xba800000, v85
	v_fmac_f32_e32 v93, 0xba800000, v85
	v_fmac_f32_e32 v92, 0xba800000, v85
	v_mov_b32_e32 v100, v93
	v_mov_b32_e32 v101, v95
	v_mov_b32_e32 v93, v94
	v_pk_mul_f32 v[102:103], v[100:101], v[100:101]
	v_pk_mul_f32 v[94:95], v[92:93], v[92:93]
	v_fmac_f32_e32 v98, 0xba800000, v85
	v_pk_mov_b32 v[104:105], v[94:95], v[102:103] op_sel:[1,0]
	v_mov_b32_e32 v95, v103
	v_fmac_f32_e32 v99, 0xba800000, v85
	v_fmac_f32_e32 v97, 0xba800000, v85
	v_pk_add_f32 v[94:95], v[104:105], v[94:95]
	v_fmac_f32_e32 v96, 0xba800000, v85
	v_mov_b32_e32 v102, v97
	v_mov_b32_e32 v103, v99
	v_mov_b32_e32 v97, v98
	v_pk_add_f32 v[94:95], v[94:95], v[94:95] op_sel_hi:[0,1]
	v_pk_mul_f32 v[104:105], v[102:103], v[102:103]
	v_pk_mul_f32 v[98:99], v[96:97], v[96:97]
	v_fmac_f32_e32 v80, 0xba800000, v85
	v_pk_mov_b32 v[106:107], v[98:99], v[104:105] op_sel:[1,0]
	v_mov_b32_e32 v99, v105
	v_fmac_f32_e32 v81, 0xba800000, v85
	v_fmac_f32_e32 v82, 0xba800000, v85
	v_mul_f32_e32 v94, v80, v80
	v_pk_add_f32 v[98:99], v[106:107], v[98:99]
	v_fmac_f32_e32 v83, 0xba800000, v85
	v_pk_fma_f32 v[104:105], v[80:81], v[80:81], v[94:95] op_sel_hi:[1,1,0]
	v_mul_f32_e32 v94, v82, v82
	v_pk_add_f32 v[98:99], v[98:99], v[98:99] op_sel_hi:[0,1]
	v_pk_fma_f32 v[106:107], v[82:83], v[82:83], v[94:95] op_sel_hi:[1,1,0]
	v_fmac_f32_e32 v90, 0xba800000, v85
	v_fmac_f32_e32 v88, 0xba800000, v85
	v_fmac_f32_e32 v86, 0xba800000, v85
	v_fmac_f32_e32 v84, 0xba800000, v85
	v_mul_f32_e32 v104, v84, v84
	v_mul_f32_e32 v106, v86, v86
	v_mul_f32_e32 v94, v88, v88
	v_mul_f32_e32 v98, v90, v90
	v_pk_add_f32 v[104:105], v[104:105], v[106:107]
	v_pk_add_f32 v[94:95], v[94:95], v[98:99]
	s_nop 0
	v_pk_add_f32 v[94:95], v[104:105], v[94:95]
	s_nop 0
	v_add_f32_e32 v85, v94, v95
	s_waitcnt lgkmcnt(0)
	s_nop 1
	v_add_f32_dpp v85, v85, v85 quad_perm:[1,0,3,2] row_mask:0xf bank_mask:0xf
	s_nop 1
	v_add_f32_dpp v85, v85, v85 quad_perm:[2,3,0,1] row_mask:0xf bank_mask:0xf
	s_nop 1
	v_add_f32_dpp v85, v85, v85 row_half_mirror row_mask:0xf bank_mask:0xf
	s_nop 1
	v_add_f32_dpp v85, v85, v85 row_mirror row_mask:0xf bank_mask:0xf
	v_mov_b32_e32 v87, v85
	s_nop 1
	v_permlane16_swap_b32_e32 v85, v87
	v_add_f32_e32 v85, v85, v87
	v_mov_b32_e32 v87, v85
	s_nop 1
	v_permlane32_swap_b32_e32 v85, v87
	v_add_f32_e32 v85, v85, v87
	v_fmamk_f32 v85, v85, 0x3a800000, v78
	v_mul_f32_e32 v87, 0x4f800000, v85
	v_cmp_gt_f32_e32 vcc, s6, v85
	s_nop 1
	v_cndmask_b32_e32 v85, v85, v87, vcc
	v_sqrt_f32_e32 v87, v85
	s_nop 0
	v_add_u32_e32 v89, -1, v87
	v_fma_f32 v91, -v89, v87, v85
	v_cmp_ge_f32_e64 s[0:1], 0, v91
	v_add_u32_e32 v91, 1, v87
	s_nop 0
	v_cndmask_b32_e64 v89, v87, v89, s[0:1]
	v_fma_f32 v87, -v91, v87, v85
	v_cmp_lt_f32_e64 s[0:1], 0, v87
	s_nop 1
	v_cndmask_b32_e64 v87, v89, v91, s[0:1]
	v_mul_f32_e32 v89, 0x37800000, v87
	v_cndmask_b32_e32 v87, v87, v89, vcc
	v_cmp_class_f32_e32 vcc, v85, v79
	s_nop 1
	v_cndmask_b32_e32 v85, v87, v85, vcc
	v_div_scale_f32 v87, s[0:1], v85, v85, 1.0
	v_rcp_f32_e32 v89, v87
	s_add_i32 s0, s4, 6
	s_cmp_gt_u32 s0, 12
	v_fma_f32 v91, -v87, v89, 1.0
	v_fmac_f32_e32 v89, v91, v89
	v_div_scale_f32 v91, vcc, 1.0, v85, 1.0
	v_mul_f32_e32 v94, v91, v89
	v_fma_f32 v95, -v87, v94, v91
	v_fmac_f32_e32 v94, v95, v89
	v_fma_f32 v87, -v87, v94, v91
	v_div_fmas_f32 v87, v87, v89, v94
	v_div_fixup_f32 v94, v87, v85, 1.0
	v_pk_mul_f32 v[92:93], v[92:93], v[94:95] op_sel_hi:[1,0]
	v_pk_mul_f32 v[80:81], v[80:81], v[94:95] op_sel_hi:[1,0]
	v_mov_b32_e32 v85, v86
	v_pk_fma_f32 v[92:93], v[10:11], v[92:93], v[14:15]
	v_pk_fma_f32 v[104:105], v[26:27], v[80:81], v[30:31]
	v_pk_mul_f32 v[80:81], v[84:85], v[94:95] op_sel_hi:[1,0]
	v_pk_mul_f32 v[98:99], v[100:101], v[94:95] op_sel_hi:[1,0]
	v_pk_fma_f32 v[86:87], v[18:19], v[80:81], v[22:23]
	v_bfe_u32 v80, v92, 16, 1
	v_add3_u32 v80, v92, v80, s7
	v_bfe_u32 v81, v93, 16, 1
	v_pk_fma_f32 v[98:99], v[12:13], v[98:99], v[16:17]
	v_pk_mul_f32 v[82:83], v[82:83], v[94:95] op_sel_hi:[1,0]
	v_mov_b32_e32 v89, v90
	v_lshrrev_b32_e32 v80, 16, v80
	v_add3_u32 v81, v93, v81, s7
	v_pk_mul_f32 v[100:101], v[102:103], v[94:95] op_sel_hi:[1,0]
	v_pk_fma_f32 v[102:103], v[28:29], v[82:83], v[32:33]
	v_pk_mul_f32 v[82:83], v[88:89], v[94:95] op_sel_hi:[1,0]
	v_and_or_b32 v80, v81, s5, v80
	v_bfe_u32 v81, v98, 16, 1
	v_pk_mul_f32 v[96:97], v[96:97], v[94:95] op_sel_hi:[1,0]
	v_pk_fma_f32 v[84:85], v[20:21], v[82:83], v[24:25]
	v_add3_u32 v81, v98, v81, s7
	v_bfe_u32 v82, v99, 16, 1
	v_pk_fma_f32 v[96:97], v[2:3], v[96:97], v[6:7]
	v_lshrrev_b32_e32 v81, 16, v81
	v_add3_u32 v82, v99, v82, s7
	v_and_or_b32 v81, v82, s5, v81
	v_bfe_u32 v82, v96, 16, 1
	v_add3_u32 v82, v96, v82, s7
	v_bfe_u32 v83, v97, 16, 1
	v_pk_fma_f32 v[100:101], v[4:5], v[100:101], v[8:9]
	v_lshrrev_b32_e32 v82, 16, v82
	v_add3_u32 v83, v97, v83, s7
	v_and_or_b32 v82, v83, s5, v82
	v_bfe_u32 v83, v100, 16, 1
	v_add3_u32 v83, v100, v83, s7
	v_bfe_u32 v88, v101, 16, 1
	v_lshrrev_b32_e32 v83, 16, v83
	v_add3_u32 v88, v101, v88, s7
	v_and_or_b32 v83, v88, s5, v83
	global_store_dwordx4 v[72:73], v[80:83], off offset:-1024
	v_bfe_u32 v72, v104, 16, 1
	v_add3_u32 v72, v104, v72, s7
	v_bfe_u32 v73, v105, 16, 1
	v_lshrrev_b32_e32 v72, 16, v72
	v_add3_u32 v73, v105, v73, s7
	v_and_or_b32 v80, v73, s5, v72
	v_bfe_u32 v72, v102, 16, 1
	v_add3_u32 v72, v102, v72, s7
	v_bfe_u32 v73, v103, 16, 1
	v_lshrrev_b32_e32 v72, 16, v72
	v_add3_u32 v73, v103, v73, s7
	v_and_or_b32 v81, v73, s5, v72
	v_bfe_u32 v72, v86, 16, 1
	v_add3_u32 v72, v86, v72, s7
	v_bfe_u32 v73, v87, 16, 1
	v_lshrrev_b32_e32 v72, 16, v72
	v_add3_u32 v73, v87, v73, s7
	v_and_or_b32 v82, v73, s5, v72
	v_bfe_u32 v72, v84, 16, 1
	v_add3_u32 v72, v84, v72, s7
	v_bfe_u32 v73, v85, 16, 1
	v_lshrrev_b32_e32 v72, 16, v72
	v_add3_u32 v73, v85, v73, s7
	v_and_or_b32 v83, v73, s5, v72
	global_store_dwordx4 v[70:71], v[80:83], off offset:-4096
	s_cbranch_scc1 .LBB0_622
	v_add3_u32 v42, v66, s4, 9
	v_ashrrev_i32_e32 v43, 31, v42
	v_lshlrev_b64 v[42:43], 11, v[42:43]
	v_lshl_add_u64 v[46:47], v[68:69], 0, v[42:43]
	global_load_dwordx4 v[42:45], v[46:47], off
	s_nop 0
	global_load_dwordx4 v[46:49], v[46:47], off offset:1024
.LBB0_622:
	s_waitcnt vmcnt(7)
	v_lshlrev_b32_e32 v91, 16, v51
	v_lshlrev_b32_e32 v90, 16, v50
	v_and_b32_e32 v93, 0xffff0000, v51
	v_and_b32_e32 v92, 0xffff0000, v50
	v_pk_add_f32 v[94:95], v[90:91], v[92:93]
	v_and_b32_e32 v97, 0xffff0000, v53
	v_add_f32_e32 v83, v94, v95
	v_lshlrev_b32_e32 v95, 16, v53
	v_lshlrev_b32_e32 v94, 16, v52
	v_and_b32_e32 v96, 0xffff0000, v52
	v_pk_add_f32 v[98:99], v[94:95], v[96:97]
	s_waitcnt vmcnt(6)
	v_lshlrev_b32_e32 v72, 16, v54
	v_and_b32_e32 v73, 0xffff0000, v54
	v_lshlrev_b32_e32 v80, 16, v55
	v_and_b32_e32 v81, 0xffff0000, v55
	v_pk_add_f32 v[98:99], v[98:99], v[98:99] op_sel_hi:[0,1]
	v_lshlrev_b32_e32 v82, 16, v56
	v_and_b32_e32 v84, 0xffff0000, v56
	v_lshlrev_b32_e32 v86, 16, v57
	v_and_b32_e32 v88, 0xffff0000, v57
	v_add_f32_e32 v89, 0, v83
	v_add_f32_e32 v83, v72, v73
	v_add_f32_e32 v85, v80, v81
	v_mov_b32_e32 v87, v99
	v_pk_add_f32 v[100:101], v[82:83], v[84:85]
	v_pk_add_f32 v[98:99], v[86:87], v[88:89]
	s_nop 0
	v_pk_add_f32 v[98:99], v[100:101], v[98:99]
	s_nop 0
	v_add_f32_e32 v83, v98, v99
	s_waitcnt lgkmcnt(0)
	s_nop 1
	v_add_f32_dpp v83, v83, v83 quad_perm:[1,0,3,2] row_mask:0xf bank_mask:0xf
	s_nop 1
	v_add_f32_dpp v83, v83, v83 quad_perm:[2,3,0,1] row_mask:0xf bank_mask:0xf
	s_nop 1
	v_add_f32_dpp v83, v83, v83 row_half_mirror row_mask:0xf bank_mask:0xf
	s_nop 1
	v_add_f32_dpp v83, v83, v83 row_mirror row_mask:0xf bank_mask:0xf
	v_mov_b32_e32 v85, v83
	s_nop 1
	v_permlane16_swap_b32_e32 v83, v85
	v_add_f32_e32 v83, v83, v85
	v_mov_b32_e32 v85, v83
	s_nop 1
	v_permlane32_swap_b32_e32 v83, v85
	v_add_f32_e32 v83, v83, v85
	v_fmac_f32_e32 v92, 0xba800000, v83
	v_fmac_f32_e32 v93, 0xba800000, v83
	v_fmac_f32_e32 v91, 0xba800000, v83
	v_fmac_f32_e32 v90, 0xba800000, v83
	v_mov_b32_e32 v98, v91
	v_mov_b32_e32 v99, v93
	v_mov_b32_e32 v91, v92
	v_pk_mul_f32 v[100:101], v[98:99], v[98:99]
	v_pk_mul_f32 v[92:93], v[90:91], v[90:91]
	v_fmac_f32_e32 v96, 0xba800000, v83
	v_pk_mov_b32 v[102:103], v[92:93], v[100:101] op_sel:[1,0]
	v_mov_b32_e32 v93, v101
	v_fmac_f32_e32 v97, 0xba800000, v83
	v_fmac_f32_e32 v95, 0xba800000, v83
	v_pk_add_f32 v[92:93], v[102:103], v[92:93]
	v_fmac_f32_e32 v94, 0xba800000, v83
	v_mov_b32_e32 v100, v95
	v_mov_b32_e32 v101, v97
	v_mov_b32_e32 v95, v96
	v_pk_add_f32 v[92:93], v[92:93], v[92:93] op_sel_hi:[0,1]
	v_pk_mul_f32 v[102:103], v[100:101], v[100:101]
	v_pk_mul_f32 v[96:97], v[94:95], v[94:95]
	v_fmac_f32_e32 v72, 0xba800000, v83
	v_pk_mov_b32 v[104:105], v[96:97], v[102:103] op_sel:[1,0]
	v_mov_b32_e32 v97, v103
	v_fmac_f32_e32 v73, 0xba800000, v83
	v_fmac_f32_e32 v80, 0xba800000, v83
	v_mul_f32_e32 v92, v72, v72
	v_pk_add_f32 v[96:97], v[104:105], v[96:97]
	v_fmac_f32_e32 v81, 0xba800000, v83
	v_pk_fma_f32 v[102:103], v[72:73], v[72:73], v[92:93] op_sel_hi:[1,1,0]
	v_mul_f32_e32 v92, v80, v80
	v_pk_add_f32 v[96:97], v[96:97], v[96:97] op_sel_hi:[0,1]
	v_pk_fma_f32 v[104:105], v[80:81], v[80:81], v[92:93] op_sel_hi:[1,1,0]
	v_fmac_f32_e32 v88, 0xba800000, v83
	v_fmac_f32_e32 v86, 0xba800000, v83
	v_fmac_f32_e32 v84, 0xba800000, v83
	v_fmac_f32_e32 v82, 0xba800000, v83
	v_mul_f32_e32 v102, v82, v82
	v_mul_f32_e32 v104, v84, v84
	v_mul_f32_e32 v92, v86, v86
	v_mul_f32_e32 v96, v88, v88
	v_pk_add_f32 v[102:103], v[102:103], v[104:105]
	v_pk_add_f32 v[92:93], v[92:93], v[96:97]
	s_nop 0
	v_pk_add_f32 v[92:93], v[102:103], v[92:93]
	s_nop 0
	v_add_f32_e32 v83, v92, v93
	s_waitcnt lgkmcnt(0)
	s_nop 1
	v_add_f32_dpp v83, v83, v83 quad_perm:[1,0,3,2] row_mask:0xf bank_mask:0xf
	s_nop 1
	v_add_f32_dpp v83, v83, v83 quad_perm:[2,3,0,1] row_mask:0xf bank_mask:0xf
	s_nop 1
	v_add_f32_dpp v83, v83, v83 row_half_mirror row_mask:0xf bank_mask:0xf
	s_nop 1
	v_add_f32_dpp v83, v83, v83 row_mirror row_mask:0xf bank_mask:0xf
	v_mov_b32_e32 v85, v83
	s_nop 1
	v_permlane16_swap_b32_e32 v83, v85
	v_add_f32_e32 v83, v83, v85
	v_mov_b32_e32 v85, v83
	s_nop 1
	v_permlane32_swap_b32_e32 v83, v85
	v_add_f32_e32 v83, v83, v85
	v_fmamk_f32 v83, v83, 0x3a800000, v78
	v_mul_f32_e32 v85, 0x4f800000, v83
	v_cmp_gt_f32_e32 vcc, s6, v83
	s_nop 1
	v_cndmask_b32_e32 v83, v83, v85, vcc
	v_sqrt_f32_e32 v85, v83
	s_nop 0
	v_add_u32_e32 v87, -1, v85
	v_fma_f32 v89, -v87, v85, v83
	v_cmp_ge_f32_e64 s[0:1], 0, v89
	v_add_u32_e32 v89, 1, v85
	s_nop 0
	v_cndmask_b32_e64 v87, v85, v87, s[0:1]
	v_fma_f32 v85, -v89, v85, v83
	v_cmp_lt_f32_e64 s[0:1], 0, v85
	s_nop 1
	v_cndmask_b32_e64 v85, v87, v89, s[0:1]
	v_mul_f32_e32 v87, 0x37800000, v85
	v_cndmask_b32_e32 v85, v85, v87, vcc
	v_cmp_class_f32_e32 vcc, v83, v79
	s_nop 1
	v_cndmask_b32_e32 v83, v85, v83, vcc
	v_div_scale_f32 v85, s[0:1], v83, v83, 1.0
	v_rcp_f32_e32 v87, v85
	s_add_i32 s0, s4, 7
	s_cmp_gt_u32 s0, 12
	v_fma_f32 v89, -v85, v87, 1.0
	v_fmac_f32_e32 v87, v89, v87
	v_div_scale_f32 v89, vcc, 1.0, v83, 1.0
	v_mul_f32_e32 v92, v89, v87
	v_fma_f32 v93, -v85, v92, v89
	v_fmac_f32_e32 v92, v93, v87
	v_fma_f32 v85, -v85, v92, v89
	v_div_fmas_f32 v85, v85, v87, v92
	v_div_fixup_f32 v92, v85, v83, 1.0
	v_pk_mul_f32 v[90:91], v[90:91], v[92:93] op_sel_hi:[1,0]
	v_pk_mul_f32 v[80:81], v[80:81], v[92:93] op_sel_hi:[1,0]
	v_mov_b32_e32 v83, v84
	v_pk_mul_f32 v[96:97], v[98:99], v[92:93] op_sel_hi:[1,0]
	v_pk_fma_f32 v[90:91], v[10:11], v[90:91], v[14:15]
	v_pk_mul_f32 v[98:99], v[100:101], v[92:93] op_sel_hi:[1,0]
	v_pk_fma_f32 v[100:101], v[28:29], v[80:81], v[32:33]
	v_pk_mul_f32 v[80:81], v[82:83], v[92:93] op_sel_hi:[1,0]
	v_mov_b32_e32 v87, v88
	v_pk_mul_f32 v[82:83], v[86:87], v[92:93] op_sel_hi:[1,0]
	v_pk_fma_f32 v[86:87], v[18:19], v[80:81], v[22:23]
	v_bfe_u32 v80, v90, 16, 1
	v_add3_u32 v80, v90, v80, s7
	v_bfe_u32 v81, v91, 16, 1
	v_pk_fma_f32 v[96:97], v[12:13], v[96:97], v[16:17]
	v_lshrrev_b32_e32 v80, 16, v80
	v_add3_u32 v81, v91, v81, s7
	v_and_or_b32 v80, v81, s5, v80
	v_bfe_u32 v81, v96, 16, 1
	v_pk_mul_f32 v[94:95], v[94:95], v[92:93] op_sel_hi:[1,0]
	v_pk_fma_f32 v[84:85], v[20:21], v[82:83], v[24:25]
	v_add3_u32 v81, v96, v81, s7
	v_bfe_u32 v82, v97, 16, 1
	v_pk_fma_f32 v[94:95], v[2:3], v[94:95], v[6:7]
	v_lshrrev_b32_e32 v81, 16, v81
	v_add3_u32 v82, v97, v82, s7
	v_and_or_b32 v81, v82, s5, v81
	v_bfe_u32 v82, v94, 16, 1
	v_add3_u32 v82, v94, v82, s7
	v_bfe_u32 v83, v95, 16, 1
	v_pk_fma_f32 v[98:99], v[4:5], v[98:99], v[8:9]
	v_lshrrev_b32_e32 v82, 16, v82
	v_add3_u32 v83, v95, v83, s7
	v_and_or_b32 v82, v83, s5, v82
	v_bfe_u32 v83, v98, 16, 1
	v_add3_u32 v83, v98, v83, s7
	v_bfe_u32 v88, v99, 16, 1
	v_pk_mul_f32 v[72:73], v[72:73], v[92:93] op_sel_hi:[1,0]
	v_lshrrev_b32_e32 v83, 16, v83
	v_add3_u32 v88, v99, v88, s7
	v_pk_fma_f32 v[72:73], v[26:27], v[72:73], v[30:31]
	v_and_or_b32 v83, v88, s5, v83
	global_store_dwordx4 v[70:71], v[80:83], off offset:-3072
	s_nop 1
	v_bfe_u32 v80, v72, 16, 1
	v_add3_u32 v72, v72, v80, s7
	v_bfe_u32 v80, v73, 16, 1
	v_lshrrev_b32_e32 v72, 16, v72
	v_add3_u32 v73, v73, v80, s7
	v_and_or_b32 v80, v73, s5, v72
	v_bfe_u32 v72, v100, 16, 1
	v_add3_u32 v72, v100, v72, s7
	v_bfe_u32 v73, v101, 16, 1
	v_lshrrev_b32_e32 v72, 16, v72
	v_add3_u32 v73, v101, v73, s7
	v_and_or_b32 v81, v73, s5, v72
	v_bfe_u32 v72, v86, 16, 1
	v_add3_u32 v72, v86, v72, s7
	v_bfe_u32 v73, v87, 16, 1
	v_lshrrev_b32_e32 v72, 16, v72
	v_add3_u32 v73, v87, v73, s7
	v_and_or_b32 v82, v73, s5, v72
	v_bfe_u32 v72, v84, 16, 1
	v_add3_u32 v72, v84, v72, s7
	v_bfe_u32 v73, v85, 16, 1
	v_lshrrev_b32_e32 v72, 16, v72
	v_add3_u32 v73, v85, v73, s7
	v_and_or_b32 v83, v73, s5, v72
	global_store_dwordx4 v[70:71], v[80:83], off offset:-2048
	s_cbranch_scc1 .LBB0_617
	v_add3_u32 v50, v66, s4, 10
	v_ashrrev_i32_e32 v51, 31, v50
	v_lshlrev_b64 v[50:51], 11, v[50:51]
	v_lshl_add_u64 v[54:55], v[68:69], 0, v[50:51]
	global_load_dwordx4 v[50:53], v[54:55], off
	s_nop 0
	global_load_dwordx4 v[54:57], v[54:55], off offset:1024
	s_branch .LBB0_617

.LBB0_721:
	s_waitcnt vmcnt(7)
	v_lshlrev_b32_e32 v87, 16, v59
	v_lshlrev_b32_e32 v86, 16, v58
	v_and_b32_e32 v59, 0xffff0000, v59
	v_and_b32_e32 v58, 0xffff0000, v58
	v_pk_add_f32 v[88:89], v[86:87], v[58:59]
	s_waitcnt vmcnt(6)
	v_lshlrev_b32_e32 v82, 16, v65
	v_and_b32_e32 v84, 0xffff0000, v65
	v_add_f32_e32 v65, v88, v89
	v_lshlrev_b32_e32 v89, 16, v61
	v_lshlrev_b32_e32 v88, 16, v60
	v_and_b32_e32 v61, 0xffff0000, v61
	v_and_b32_e32 v60, 0xffff0000, v60
	v_pk_add_f32 v[90:91], v[88:89], v[60:61]
	v_lshlrev_b32_e32 v72, 16, v62
	v_and_b32_e32 v73, 0xffff0000, v62
	v_lshlrev_b32_e32 v62, 16, v63
	v_and_b32_e32 v63, 0xffff0000, v63
	v_pk_add_f32 v[90:91], v[90:91], v[90:91] op_sel_hi:[0,1]
	v_lshlrev_b32_e32 v80, 16, v64
	v_and_b32_e32 v64, 0xffff0000, v64
	v_add_f32_e32 v85, 0, v65
	v_add_f32_e32 v81, v72, v73
	v_add_f32_e32 v65, v62, v63
	v_mov_b32_e32 v83, v91
	v_pk_add_f32 v[92:93], v[80:81], v[64:65]
	v_pk_add_f32 v[90:91], v[82:83], v[84:85]
	s_add_i32 s4, s4, 4
	v_pk_add_f32 v[90:91], v[92:93], v[90:91]
	s_cmp_gt_u32 s4, 11
	v_add_f32_e32 v65, v90, v91
	s_waitcnt lgkmcnt(0)
	s_nop 1
	v_add_f32_dpp v65, v65, v65 quad_perm:[1,0,3,2] row_mask:0xf bank_mask:0xf
	s_nop 1
	v_add_f32_dpp v65, v65, v65 quad_perm:[2,3,0,1] row_mask:0xf bank_mask:0xf
	s_nop 1
	v_add_f32_dpp v65, v65, v65 row_half_mirror row_mask:0xf bank_mask:0xf
	s_nop 1
	v_add_f32_dpp v65, v65, v65 row_mirror row_mask:0xf bank_mask:0xf
	v_mov_b32_e32 v81, v65
	s_nop 1
	v_permlane16_swap_b32_e32 v65, v81
	v_add_f32_e32 v65, v65, v81
	v_mov_b32_e32 v81, v65
	s_nop 1
	v_permlane32_swap_b32_e32 v65, v81
	v_add_f32_e32 v65, v65, v81
	v_fmac_f32_e32 v58, 0xba800000, v65
	v_fmac_f32_e32 v59, 0xba800000, v65
	v_fmac_f32_e32 v87, 0xba800000, v65
	v_fmac_f32_e32 v86, 0xba800000, v65
	v_mov_b32_e32 v90, v87
	v_mov_b32_e32 v91, v59
	v_mov_b32_e32 v87, v58
	v_pk_mul_f32 v[92:93], v[90:91], v[90:91]
	v_pk_mul_f32 v[58:59], v[86:87], v[86:87]
	v_fmac_f32_e32 v60, 0xba800000, v65
	v_pk_mov_b32 v[94:95], v[58:59], v[92:93] op_sel:[1,0]
	v_mov_b32_e32 v59, v93
	v_fmac_f32_e32 v61, 0xba800000, v65
	v_fmac_f32_e32 v89, 0xba800000, v65
	v_pk_add_f32 v[58:59], v[94:95], v[58:59]
	v_fmac_f32_e32 v88, 0xba800000, v65
	v_mov_b32_e32 v92, v89
	v_mov_b32_e32 v93, v61
	v_mov_b32_e32 v89, v60
	v_pk_add_f32 v[58:59], v[58:59], v[58:59] op_sel_hi:[0,1]
	v_pk_mul_f32 v[94:95], v[92:93], v[92:93]
	v_pk_mul_f32 v[60:61], v[88:89], v[88:89]
	v_fmac_f32_e32 v72, 0xba800000, v65
	v_pk_mov_b32 v[96:97], v[60:61], v[94:95] op_sel:[1,0]
	v_mov_b32_e32 v61, v95
	v_fmac_f32_e32 v73, 0xba800000, v65
	v_fmac_f32_e32 v62, 0xba800000, v65
	v_mul_f32_e32 v58, v72, v72
	v_pk_add_f32 v[60:61], v[96:97], v[60:61]
	v_fmac_f32_e32 v63, 0xba800000, v65
	v_pk_fma_f32 v[94:95], v[72:73], v[72:73], v[58:59] op_sel_hi:[1,1,0]
	v_mul_f32_e32 v58, v62, v62
	v_pk_add_f32 v[60:61], v[60:61], v[60:61] op_sel_hi:[0,1]
	v_pk_fma_f32 v[96:97], v[62:63], v[62:63], v[58:59] op_sel_hi:[1,1,0]
	v_fmac_f32_e32 v84, 0xba800000, v65
	v_fmac_f32_e32 v82, 0xba800000, v65
	v_fmac_f32_e32 v64, 0xba800000, v65
	v_fmac_f32_e32 v80, 0xba800000, v65
	v_mul_f32_e32 v94, v80, v80
	v_mul_f32_e32 v96, v64, v64
	v_mul_f32_e32 v58, v82, v82
	v_mul_f32_e32 v60, v84, v84
	v_pk_add_f32 v[94:95], v[94:95], v[96:97]
	v_pk_add_f32 v[58:59], v[58:59], v[60:61]
	v_mov_b32_e32 v83, v84
	v_pk_add_f32 v[58:59], v[94:95], v[58:59]
	s_nop 0
	v_add_f32_e32 v58, v58, v59
	s_waitcnt lgkmcnt(0)
	s_nop 1
	v_add_f32_dpp v58, v58, v58 quad_perm:[1,0,3,2] row_mask:0xf bank_mask:0xf
	s_nop 1
	v_add_f32_dpp v58, v58, v58 quad_perm:[2,3,0,1] row_mask:0xf bank_mask:0xf
	s_nop 1
	v_add_f32_dpp v58, v58, v58 row_half_mirror row_mask:0xf bank_mask:0xf
	s_nop 1
	v_add_f32_dpp v58, v58, v58 row_mirror row_mask:0xf bank_mask:0xf
	v_mov_b32_e32 v59, v58
	s_nop 1
	v_permlane16_swap_b32_e32 v58, v59
	v_add_f32_e32 v58, v58, v59
	v_mov_b32_e32 v59, v58
	s_nop 1
	v_permlane32_swap_b32_e32 v58, v59
	v_add_f32_e32 v58, v58, v59
	v_fmamk_f32 v58, v58, 0x3a800000, v78
	v_mul_f32_e32 v59, 0x4f800000, v58
	v_cmp_gt_f32_e32 vcc, s6, v58
	s_nop 1
	v_cndmask_b32_e32 v58, v58, v59, vcc
	v_sqrt_f32_e32 v59, v58
	s_nop 0
	v_add_u32_e32 v60, -1, v59
	v_fma_f32 v61, -v60, v59, v58
	v_cmp_ge_f32_e64 s[0:1], 0, v61
	v_add_u32_e32 v61, 1, v59
	s_nop 0
	v_cndmask_b32_e64 v60, v59, v60, s[0:1]
	v_fma_f32 v59, -v61, v59, v58
	v_cmp_lt_f32_e64 s[0:1], 0, v59
	s_nop 1
	v_cndmask_b32_e64 v59, v60, v61, s[0:1]
	v_mul_f32_e32 v60, 0x37800000, v59
	v_cndmask_b32_e32 v59, v59, v60, vcc
	v_cmp_class_f32_e32 vcc, v58, v79
	s_nop 1
	v_cndmask_b32_e32 v58, v59, v58, vcc
	v_div_scale_f32 v59, s[0:1], v58, v58, 1.0
	v_rcp_f32_e32 v60, v59
	s_nop 0
	v_fma_f32 v61, -v59, v60, 1.0
	v_fmac_f32_e32 v60, v61, v60
	v_div_scale_f32 v61, vcc, 1.0, v58, 1.0
	v_mul_f32_e32 v65, v61, v60
	v_fma_f32 v81, -v59, v65, v61
	v_fmac_f32_e32 v65, v81, v60
	v_fma_f32 v59, -v59, v65, v61
	v_div_fmas_f32 v59, v59, v60, v65
	v_div_fixup_f32 v58, v59, v58, 1.0
	v_pk_mul_f32 v[60:61], v[86:87], v[58:59] op_sel_hi:[1,0]
	v_mov_b32_e32 v81, v64
	v_pk_mul_f32 v[86:87], v[90:91], v[58:59] op_sel_hi:[1,0]
	v_pk_fma_f32 v[60:61], v[6:7], v[60:61], v[14:15]
	v_pk_mul_f32 v[88:89], v[88:89], v[58:59] op_sel_hi:[1,0]
	v_pk_mul_f32 v[90:91], v[92:93], v[58:59] op_sel_hi:[1,0]
	v_pk_mul_f32 v[72:73], v[72:73], v[58:59] op_sel_hi:[1,0]
	v_pk_mul_f32 v[62:63], v[62:63], v[58:59] op_sel_hi:[1,0]
	v_pk_mul_f32 v[64:65], v[80:81], v[58:59] op_sel_hi:[1,0]
	v_pk_mul_f32 v[58:59], v[82:83], v[58:59] op_sel_hi:[1,0]
	v_pk_fma_f32 v[86:87], v[8:9], v[86:87], v[16:17]
	v_pk_fma_f32 v[80:81], v[20:21], v[58:59], v[28:29]
	v_bfe_u32 v58, v60, 16, 1
	v_add3_u32 v58, v60, v58, s7
	v_bfe_u32 v59, v61, 16, 1
	v_lshrrev_b32_e32 v58, 16, v58
	v_add3_u32 v59, v61, v59, s7
	v_and_or_b32 v58, v59, s5, v58
	v_bfe_u32 v59, v86, 16, 1
	v_add3_u32 v59, v86, v59, s7
	v_bfe_u32 v60, v87, 16, 1
	v_pk_fma_f32 v[88:89], v[2:3], v[88:89], v[10:11]
	v_lshrrev_b32_e32 v59, 16, v59
	v_add3_u32 v60, v87, v60, s7
	v_and_or_b32 v59, v60, s5, v59
	v_bfe_u32 v60, v88, 16, 1
	v_add3_u32 v60, v88, v60, s7
	v_bfe_u32 v61, v89, 16, 1
	v_pk_fma_f32 v[90:91], v[4:5], v[90:91], v[12:13]
	v_lshrrev_b32_e32 v60, 16, v60
	v_add3_u32 v61, v89, v61, s7
	v_and_or_b32 v60, v61, s5, v60
	v_bfe_u32 v61, v90, 16, 1
	v_add3_u32 v61, v90, v61, s7
	v_bfe_u32 v82, v91, 16, 1
	v_lshrrev_b32_e32 v61, 16, v61
	v_add3_u32 v82, v91, v82, s7
	v_pk_fma_f32 v[72:73], v[22:23], v[72:73], v[30:31]
	v_and_or_b32 v61, v82, s5, v61
	global_store_dwordx4 v[70:71], v[58:61], off offset:-1024
	v_pk_fma_f32 v[62:63], v[24:25], v[62:63], v[32:33]
	v_pk_fma_f32 v[64:65], v[18:19], v[64:65], v[26:27]
	v_bfe_u32 v58, v72, 16, 1
	v_add3_u32 v58, v72, v58, s7
	v_bfe_u32 v59, v73, 16, 1
	v_lshrrev_b32_e32 v58, 16, v58
	v_add3_u32 v59, v73, v59, s7
	v_and_or_b32 v58, v59, s5, v58
	v_bfe_u32 v59, v62, 16, 1
	v_add3_u32 v59, v62, v59, s7
	v_bfe_u32 v60, v63, 16, 1
	v_lshrrev_b32_e32 v59, 16, v59
	v_add3_u32 v60, v63, v60, s7
	v_and_or_b32 v59, v60, s5, v59
	v_bfe_u32 v60, v64, 16, 1
	v_add3_u32 v60, v64, v60, s7
	v_bfe_u32 v61, v65, 16, 1
	v_lshrrev_b32_e32 v60, 16, v60
	v_add3_u32 v61, v65, v61, s7
	v_and_or_b32 v60, v61, s5, v60
	v_bfe_u32 v61, v80, 16, 1
	v_add3_u32 v61, v80, v61, s7
	v_bfe_u32 v62, v81, 16, 1
	v_lshrrev_b32_e32 v61, 16, v61
	v_add3_u32 v62, v81, v62, s7
	v_and_or_b32 v61, v62, s5, v61
	global_store_dwordx4 v[70:71], v[58:61], off
	v_lshl_add_u64 v[70:71], v[70:71], 0, s[2:3]
	s_cbranch_scc1 .LBB0_728
.LBB0_722:
	s_waitcnt vmcnt(5)
	v_lshlrev_b32_e32 v91, 16, v35
	v_lshlrev_b32_e32 v90, 16, v34
	v_and_b32_e32 v59, 0xffff0000, v35
	v_and_b32_e32 v58, 0xffff0000, v34
	v_pk_add_f32 v[60:61], v[90:91], v[58:59]
	v_lshlrev_b32_e32 v93, 16, v37
	v_add_f32_e32 v60, v60, v61
	v_add_f32_e32 v89, 0, v60
	v_lshlrev_b32_e32 v92, 16, v36
	v_and_b32_e32 v61, 0xffff0000, v37
	v_and_b32_e32 v60, 0xffff0000, v36
	v_pk_add_f32 v[62:63], v[92:93], v[60:61]
	s_waitcnt vmcnt(4)
	v_lshlrev_b32_e32 v72, 16, v38
	v_and_b32_e32 v73, 0xffff0000, v38
	v_lshlrev_b32_e32 v80, 16, v39
	v_and_b32_e32 v81, 0xffff0000, v39
	v_pk_add_f32 v[62:63], v[62:63], v[62:63] op_sel_hi:[0,1]
	v_lshlrev_b32_e32 v82, 16, v40
	v_and_b32_e32 v84, 0xffff0000, v40
	v_lshlrev_b32_e32 v86, 16, v41
	v_and_b32_e32 v88, 0xffff0000, v41
	v_add_f32_e32 v83, v72, v73
	v_add_f32_e32 v85, v80, v81
	v_mov_b32_e32 v87, v63
	v_pk_add_f32 v[64:65], v[82:83], v[84:85]
	v_pk_add_f32 v[62:63], v[86:87], v[88:89]
	s_nop 0
	v_pk_add_f32 v[62:63], v[64:65], v[62:63]
	s_nop 0
	v_add_f32_e32 v62, v62, v63
	s_waitcnt lgkmcnt(0)
	s_nop 1
	v_add_f32_dpp v62, v62, v62 quad_perm:[1,0,3,2] row_mask:0xf bank_mask:0xf
	s_nop 1
	v_add_f32_dpp v62, v62, v62 quad_perm:[2,3,0,1] row_mask:0xf bank_mask:0xf
	s_nop 1
	v_add_f32_dpp v62, v62, v62 row_half_mirror row_mask:0xf bank_mask:0xf
	s_nop 1
	v_add_f32_dpp v62, v62, v62 row_mirror row_mask:0xf bank_mask:0xf
	v_mov_b32_e32 v63, v62
	s_nop 1
	v_permlane16_swap_b32_e32 v62, v63
	v_add_f32_e32 v62, v62, v63
	v_mov_b32_e32 v63, v62
	s_nop 1
	v_permlane32_swap_b32_e32 v62, v63
	v_add_f32_e32 v83, v62, v63
	v_fmac_f32_e32 v58, 0xba800000, v83
	v_fmac_f32_e32 v59, 0xba800000, v83
	v_fmac_f32_e32 v91, 0xba800000, v83
	v_fmac_f32_e32 v90, 0xba800000, v83
	v_mov_b32_e32 v94, v91
	v_mov_b32_e32 v95, v59
	v_mov_b32_e32 v91, v58
	v_pk_mul_f32 v[62:63], v[94:95], v[94:95]
	v_pk_mul_f32 v[58:59], v[90:91], v[90:91]
	v_fmac_f32_e32 v60, 0xba800000, v83
	v_pk_mov_b32 v[64:65], v[58:59], v[62:63] op_sel:[1,0]
	v_mov_b32_e32 v59, v63
	v_fmac_f32_e32 v61, 0xba800000, v83
	v_fmac_f32_e32 v93, 0xba800000, v83
	v_pk_add_f32 v[58:59], v[64:65], v[58:59]
	v_fmac_f32_e32 v92, 0xba800000, v83
	v_mov_b32_e32 v96, v93
	v_mov_b32_e32 v97, v61
	v_mov_b32_e32 v93, v60
	v_pk_add_f32 v[58:59], v[58:59], v[58:59] op_sel_hi:[0,1]
	v_pk_mul_f32 v[62:63], v[96:97], v[96:97]
	v_pk_mul_f32 v[60:61], v[92:93], v[92:93]
	v_fmac_f32_e32 v72, 0xba800000, v83
	v_pk_mov_b32 v[64:65], v[60:61], v[62:63] op_sel:[1,0]
	v_mov_b32_e32 v61, v63
	v_fmac_f32_e32 v73, 0xba800000, v83
	v_fmac_f32_e32 v80, 0xba800000, v83
	v_mul_f32_e32 v58, v72, v72
	v_pk_add_f32 v[60:61], v[64:65], v[60:61]
	v_fmac_f32_e32 v81, 0xba800000, v83
	v_pk_fma_f32 v[62:63], v[72:73], v[72:73], v[58:59] op_sel_hi:[1,1,0]
	v_mul_f32_e32 v58, v80, v80
	v_pk_add_f32 v[60:61], v[60:61], v[60:61] op_sel_hi:[0,1]
	v_pk_fma_f32 v[64:65], v[80:81], v[80:81], v[58:59] op_sel_hi:[1,1,0]
	v_fmac_f32_e32 v88, 0xba800000, v83
	v_fmac_f32_e32 v86, 0xba800000, v83
	v_fmac_f32_e32 v84, 0xba800000, v83
	v_fmac_f32_e32 v82, 0xba800000, v83
	v_mul_f32_e32 v62, v82, v82
	v_mul_f32_e32 v64, v84, v84
	v_mul_f32_e32 v58, v86, v86
	v_mul_f32_e32 v60, v88, v88
	v_pk_add_f32 v[62:63], v[62:63], v[64:65]
	v_pk_add_f32 v[58:59], v[58:59], v[60:61]
	s_nop 0
	v_pk_add_f32 v[58:59], v[62:63], v[58:59]
	s_nop 0
	v_add_f32_e32 v58, v58, v59
	s_waitcnt lgkmcnt(0)
	s_nop 1
	v_add_f32_dpp v58, v58, v58 quad_perm:[1,0,3,2] row_mask:0xf bank_mask:0xf
	s_nop 1
	v_add_f32_dpp v58, v58, v58 quad_perm:[2,3,0,1] row_mask:0xf bank_mask:0xf
	s_nop 1
	v_add_f32_dpp v58, v58, v58 row_half_mirror row_mask:0xf bank_mask:0xf
	s_nop 1
	v_add_f32_dpp v58, v58, v58 row_mirror row_mask:0xf bank_mask:0xf
	v_mov_b32_e32 v59, v58
	s_nop 1
	v_permlane16_swap_b32_e32 v58, v59
	v_add_f32_e32 v58, v58, v59
	v_mov_b32_e32 v59, v58
	s_nop 1
	v_permlane32_swap_b32_e32 v58, v59
	v_add_f32_e32 v58, v58, v59
	v_fmamk_f32 v58, v58, 0x3a800000, v78
	v_mul_f32_e32 v59, 0x4f800000, v58
	v_cmp_gt_f32_e32 vcc, s6, v58
	s_nop 1
	v_cndmask_b32_e32 v58, v58, v59, vcc
	v_sqrt_f32_e32 v59, v58
	s_nop 0
	v_add_u32_e32 v60, -1, v59
	v_fma_f32 v61, -v60, v59, v58
	v_cmp_ge_f32_e64 s[0:1], 0, v61
	v_add_u32_e32 v61, 1, v59
	s_nop 0
	v_cndmask_b32_e64 v60, v59, v60, s[0:1]
	v_fma_f32 v59, -v61, v59, v58
	v_cmp_lt_f32_e64 s[0:1], 0, v59
	s_nop 1
	v_cndmask_b32_e64 v59, v60, v61, s[0:1]
	v_mul_f32_e32 v60, 0x37800000, v59
	v_cndmask_b32_e32 v59, v59, v60, vcc
	v_cmp_class_f32_e32 vcc, v58, v79
	s_nop 1
	v_cndmask_b32_e32 v83, v59, v58, vcc
	global_load_dwordx4 v[58:61], v[70:71], off offset:-1024
	global_load_dwordx4 v[62:65], v[70:71], off
	v_div_scale_f32 v85, s[0:1], v83, v83, 1.0
	v_rcp_f32_e32 v87, v85
	s_add_i32 s0, s4, 5
	s_cmp_gt_u32 s0, 12
	v_fma_f32 v89, -v85, v87, 1.0
	v_fmac_f32_e32 v87, v89, v87
	v_div_scale_f32 v89, vcc, 1.0, v83, 1.0
	v_mul_f32_e32 v98, v89, v87
	v_fma_f32 v99, -v85, v98, v89
	v_fmac_f32_e32 v98, v99, v87
	v_fma_f32 v85, -v85, v98, v89
	v_div_fmas_f32 v85, v85, v87, v98
	v_div_fixup_f32 v98, v85, v83, 1.0
	v_pk_mul_f32 v[90:91], v[90:91], v[98:99] op_sel_hi:[1,0]
	v_pk_mul_f32 v[72:73], v[72:73], v[98:99] op_sel_hi:[1,0]
	v_mov_b32_e32 v83, v84
	v_pk_fma_f32 v[90:91], v[6:7], v[90:91], v[14:15]
	v_pk_mul_f32 v[80:81], v[80:81], v[98:99] op_sel_hi:[1,0]
	v_pk_fma_f32 v[102:103], v[22:23], v[72:73], v[30:31]
	v_pk_mul_f32 v[72:73], v[82:83], v[98:99] op_sel_hi:[1,0]
	v_mov_b32_e32 v87, v88
	v_pk_fma_f32 v[100:101], v[24:25], v[80:81], v[32:33]
	v_pk_mul_f32 v[80:81], v[86:87], v[98:99] op_sel_hi:[1,0]
	v_pk_fma_f32 v[86:87], v[18:19], v[72:73], v[26:27]
	v_bfe_u32 v72, v90, 16, 1
	v_pk_mul_f32 v[94:95], v[94:95], v[98:99] op_sel_hi:[1,0]
	v_add3_u32 v72, v90, v72, s7
	v_bfe_u32 v73, v91, 16, 1
	v_pk_fma_f32 v[94:95], v[8:9], v[94:95], v[16:17]
	v_lshrrev_b32_e32 v72, 16, v72
	v_add3_u32 v73, v91, v73, s7
	v_pk_fma_f32 v[84:85], v[20:21], v[80:81], v[28:29]
	v_and_or_b32 v80, v73, s5, v72
	v_bfe_u32 v72, v94, 16, 1
	v_pk_mul_f32 v[92:93], v[92:93], v[98:99] op_sel_hi:[1,0]
	v_add3_u32 v72, v94, v72, s7
	v_bfe_u32 v73, v95, 16, 1
	v_pk_fma_f32 v[92:93], v[2:3], v[92:93], v[10:11]
	v_lshrrev_b32_e32 v72, 16, v72
	v_add3_u32 v73, v95, v73, s7
	v_and_or_b32 v81, v73, s5, v72
	v_bfe_u32 v72, v92, 16, 1
	v_pk_mul_f32 v[96:97], v[96:97], v[98:99] op_sel_hi:[1,0]
	v_add3_u32 v72, v92, v72, s7
	v_bfe_u32 v73, v93, 16, 1
	v_pk_fma_f32 v[96:97], v[4:5], v[96:97], v[12:13]
	v_lshrrev_b32_e32 v72, 16, v72
	v_add3_u32 v73, v93, v73, s7
	v_and_or_b32 v82, v73, s5, v72
	v_bfe_u32 v72, v96, 16, 1
	v_add3_u32 v72, v96, v72, s7
	v_bfe_u32 v73, v97, 16, 1
	v_lshrrev_b32_e32 v72, 16, v72
	v_add3_u32 v73, v97, v73, s7
	v_and_or_b32 v83, v73, s5, v72
	v_add_co_u32_e32 v72, vcc, s8, v70
	s_nop 1
	v_addc_co_u32_e32 v73, vcc, -1, v71, vcc
	global_store_dwordx4 v[72:73], v[80:83], off offset:-3072
	s_nop 1
	v_bfe_u32 v80, v102, 16, 1
	v_add3_u32 v80, v102, v80, s7
	v_bfe_u32 v81, v103, 16, 1
	v_lshrrev_b32_e32 v80, 16, v80
	v_add3_u32 v81, v103, v81, s7
	v_and_or_b32 v80, v81, s5, v80
	v_bfe_u32 v81, v100, 16, 1
	v_add3_u32 v81, v100, v81, s7
	v_bfe_u32 v82, v101, 16, 1
	v_lshrrev_b32_e32 v81, 16, v81
	v_add3_u32 v82, v101, v82, s7
	v_and_or_b32 v81, v82, s5, v81
	v_bfe_u32 v82, v86, 16, 1
	v_add3_u32 v82, v86, v82, s7
	v_bfe_u32 v83, v87, 16, 1
	v_lshrrev_b32_e32 v82, 16, v82
	v_add3_u32 v83, v87, v83, s7
	v_and_or_b32 v82, v83, s5, v82
	v_bfe_u32 v83, v84, 16, 1
	v_add3_u32 v83, v84, v83, s7
	v_bfe_u32 v84, v85, 16, 1
	v_lshrrev_b32_e32 v83, 16, v83
	v_add3_u32 v84, v85, v84, s7
	v_and_or_b32 v83, v84, s5, v83
	global_store_dwordx4 v[72:73], v[80:83], off offset:-2048
	s_cbranch_scc1 .LBB0_724
	v_add3_u32 v34, v66, s4, 8
	v_ashrrev_i32_e32 v35, 31, v34
	v_lshlrev_b64 v[34:35], 11, v[34:35]
	v_lshl_add_u64 v[38:39], v[68:69], 0, v[34:35]
	global_load_dwordx4 v[34:37], v[38:39], off
	s_nop 0
	global_load_dwordx4 v[38:41], v[38:39], off offset:1024
.LBB0_724:
	s_waitcnt vmcnt(7)
	v_lshlrev_b32_e32 v93, 16, v43
	v_lshlrev_b32_e32 v92, 16, v42
	v_and_b32_e32 v95, 0xffff0000, v43
	v_and_b32_e32 v94, 0xffff0000, v42
	v_pk_add_f32 v[96:97], v[92:93], v[94:95]
	v_and_b32_e32 v99, 0xffff0000, v45
	v_add_f32_e32 v85, v96, v97
	v_lshlrev_b32_e32 v97, 16, v45
	v_lshlrev_b32_e32 v96, 16, v44
	v_and_b32_e32 v98, 0xffff0000, v44
	v_pk_add_f32 v[100:101], v[96:97], v[98:99]
	s_waitcnt vmcnt(6)
	v_lshlrev_b32_e32 v80, 16, v46
	v_and_b32_e32 v81, 0xffff0000, v46
	v_lshlrev_b32_e32 v82, 16, v47
	v_and_b32_e32 v83, 0xffff0000, v47
	v_pk_add_f32 v[100:101], v[100:101], v[100:101] op_sel_hi:[0,1]
	v_lshlrev_b32_e32 v84, 16, v48
	v_and_b32_e32 v86, 0xffff0000, v48
	v_lshlrev_b32_e32 v88, 16, v49
	v_and_b32_e32 v90, 0xffff0000, v49
	v_add_f32_e32 v91, 0, v85
	v_add_f32_e32 v85, v80, v81
	v_add_f32_e32 v87, v82, v83
	v_mov_b32_e32 v89, v101
	v_pk_add_f32 v[102:103], v[84:85], v[86:87]
	v_pk_add_f32 v[100:101], v[88:89], v[90:91]
	s_nop 0
	v_pk_add_f32 v[100:101], v[102:103], v[100:101]
	s_nop 0
	v_add_f32_e32 v85, v100, v101
	s_waitcnt lgkmcnt(0)
	s_nop 1
	v_add_f32_dpp v85, v85, v85 quad_perm:[1,0,3,2] row_mask:0xf bank_mask:0xf
	s_nop 1
	v_add_f32_dpp v85, v85, v85 quad_perm:[2,3,0,1] row_mask:0xf bank_mask:0xf
	s_nop 1
	v_add_f32_dpp v85, v85, v85 row_half_mirror row_mask:0xf bank_mask:0xf
	s_nop 1
	v_add_f32_dpp v85, v85, v85 row_mirror row_mask:0xf bank_mask:0xf
	v_mov_b32_e32 v87, v85
	s_nop 1
	v_permlane16_swap_b32_e32 v85, v87
	v_add_f32_e32 v85, v85, v87
	v_mov_b32_e32 v87, v85
	s_nop 1
	v_permlane32_swap_b32_e32 v85, v87
	v_add_f32_e32 v85, v85, v87
	v_fmac_f32_e32 v94, 0xba800000, v85
	v_fmac_f32_e32 v95, 0xba800000, v85
	v_fmac_f32_e32 v93, 0xba800000, v85
	v_fmac_f32_e32 v92, 0xba800000, v85
	v_mov_b32_e32 v100, v93
	v_mov_b32_e32 v101, v95
	v_mov_b32_e32 v93, v94
	v_pk_mul_f32 v[102:103], v[100:101], v[100:101]
	v_pk_mul_f32 v[94:95], v[92:93], v[92:93]
	v_fmac_f32_e32 v98, 0xba800000, v85
	v_pk_mov_b32 v[104:105], v[94:95], v[102:103] op_sel:[1,0]
	v_mov_b32_e32 v95, v103
	v_fmac_f32_e32 v99, 0xba800000, v85
	v_fmac_f32_e32 v97, 0xba800000, v85
	v_pk_add_f32 v[94:95], v[104:105], v[94:95]
	v_fmac_f32_e32 v96, 0xba800000, v85
	v_mov_b32_e32 v102, v97
	v_mov_b32_e32 v103, v99
	v_mov_b32_e32 v97, v98
	v_pk_add_f32 v[94:95], v[94:95], v[94:95] op_sel_hi:[0,1]
	v_pk_mul_f32 v[104:105], v[102:103], v[102:103]
	v_pk_mul_f32 v[98:99], v[96:97], v[96:97]
	v_fmac_f32_e32 v80, 0xba800000, v85
	v_pk_mov_b32 v[106:107], v[98:99], v[104:105] op_sel:[1,0]
	v_mov_b32_e32 v99, v105
	v_fmac_f32_e32 v81, 0xba800000, v85
	v_fmac_f32_e32 v82, 0xba800000, v85
	v_mul_f32_e32 v94, v80, v80
	v_pk_add_f32 v[98:99], v[106:107], v[98:99]
	v_fmac_f32_e32 v83, 0xba800000, v85
	v_pk_fma_f32 v[104:105], v[80:81], v[80:81], v[94:95] op_sel_hi:[1,1,0]
	v_mul_f32_e32 v94, v82, v82
	v_pk_add_f32 v[98:99], v[98:99], v[98:99] op_sel_hi:[0,1]
	v_pk_fma_f32 v[106:107], v[82:83], v[82:83], v[94:95] op_sel_hi:[1,1,0]
	v_fmac_f32_e32 v90, 0xba800000, v85
	v_fmac_f32_e32 v88, 0xba800000, v85
	v_fmac_f32_e32 v86, 0xba800000, v85
	v_fmac_f32_e32 v84, 0xba800000, v85
	v_mul_f32_e32 v104, v84, v84
	v_mul_f32_e32 v106, v86, v86
	v_mul_f32_e32 v94, v88, v88
	v_mul_f32_e32 v98, v90, v90
	v_pk_add_f32 v[104:105], v[104:105], v[106:107]
	v_pk_add_f32 v[94:95], v[94:95], v[98:99]
	s_nop 0
	v_pk_add_f32 v[94:95], v[104:105], v[94:95]
	s_nop 0
	v_add_f32_e32 v85, v94, v95
	s_waitcnt lgkmcnt(0)
	s_nop 1
	v_add_f32_dpp v85, v85, v85 quad_perm:[1,0,3,2] row_mask:0xf bank_mask:0xf
	s_nop 1
	v_add_f32_dpp v85, v85, v85 quad_perm:[2,3,0,1] row_mask:0xf bank_mask:0xf
	s_nop 1
	v_add_f32_dpp v85, v85, v85 row_half_mirror row_mask:0xf bank_mask:0xf
	s_nop 1
	v_add_f32_dpp v85, v85, v85 row_mirror row_mask:0xf bank_mask:0xf
	v_mov_b32_e32 v87, v85
	s_nop 1
	v_permlane16_swap_b32_e32 v85, v87
	v_add_f32_e32 v85, v85, v87
	v_mov_b32_e32 v87, v85
	s_nop 1
	v_permlane32_swap_b32_e32 v85, v87
	v_add_f32_e32 v85, v85, v87
	v_fmamk_f32 v85, v85, 0x3a800000, v78
	v_mul_f32_e32 v87, 0x4f800000, v85
	v_cmp_gt_f32_e32 vcc, s6, v85
	s_nop 1
	v_cndmask_b32_e32 v85, v85, v87, vcc
	v_sqrt_f32_e32 v87, v85
	s_nop 0
	v_add_u32_e32 v89, -1, v87
	v_fma_f32 v91, -v89, v87, v85
	v_cmp_ge_f32_e64 s[0:1], 0, v91
	v_add_u32_e32 v91, 1, v87
	s_nop 0
	v_cndmask_b32_e64 v89, v87, v89, s[0:1]
	v_fma_f32 v87, -v91, v87, v85
	v_cmp_lt_f32_e64 s[0:1], 0, v87
	s_nop 1
	v_cndmask_b32_e64 v87, v89, v91, s[0:1]
	v_mul_f32_e32 v89, 0x37800000, v87
	v_cndmask_b32_e32 v87, v87, v89, vcc
	v_cmp_class_f32_e32 vcc, v85, v79
	s_nop 1
	v_cndmask_b32_e32 v85, v87, v85, vcc
	v_div_scale_f32 v87, s[0:1], v85, v85, 1.0
	v_rcp_f32_e32 v89, v87
	s_add_i32 s0, s4, 6
	s_cmp_gt_u32 s0, 12
	v_fma_f32 v91, -v87, v89, 1.0
	v_fmac_f32_e32 v89, v91, v89
	v_div_scale_f32 v91, vcc, 1.0, v85, 1.0
	v_mul_f32_e32 v94, v91, v89
	v_fma_f32 v95, -v87, v94, v91
	v_fmac_f32_e32 v94, v95, v89
	v_fma_f32 v87, -v87, v94, v91
	v_div_fmas_f32 v87, v87, v89, v94
	v_div_fixup_f32 v94, v87, v85, 1.0
	v_pk_mul_f32 v[92:93], v[92:93], v[94:95] op_sel_hi:[1,0]
	v_pk_mul_f32 v[80:81], v[80:81], v[94:95] op_sel_hi:[1,0]
	v_mov_b32_e32 v85, v86
	v_pk_fma_f32 v[92:93], v[6:7], v[92:93], v[14:15]
	v_pk_fma_f32 v[104:105], v[22:23], v[80:81], v[30:31]
	v_pk_mul_f32 v[80:81], v[84:85], v[94:95] op_sel_hi:[1,0]
	v_pk_mul_f32 v[98:99], v[100:101], v[94:95] op_sel_hi:[1,0]
	v_pk_fma_f32 v[86:87], v[18:19], v[80:81], v[26:27]
	v_bfe_u32 v80, v92, 16, 1
	v_add3_u32 v80, v92, v80, s7
	v_bfe_u32 v81, v93, 16, 1
	v_pk_fma_f32 v[98:99], v[8:9], v[98:99], v[16:17]
	v_pk_mul_f32 v[82:83], v[82:83], v[94:95] op_sel_hi:[1,0]
	v_mov_b32_e32 v89, v90
	v_lshrrev_b32_e32 v80, 16, v80
	v_add3_u32 v81, v93, v81, s7
	v_pk_mul_f32 v[100:101], v[102:103], v[94:95] op_sel_hi:[1,0]
	v_pk_fma_f32 v[102:103], v[24:25], v[82:83], v[32:33]
	v_pk_mul_f32 v[82:83], v[88:89], v[94:95] op_sel_hi:[1,0]
	v_and_or_b32 v80, v81, s5, v80
	v_bfe_u32 v81, v98, 16, 1
	v_pk_mul_f32 v[96:97], v[96:97], v[94:95] op_sel_hi:[1,0]
	v_pk_fma_f32 v[84:85], v[20:21], v[82:83], v[28:29]
	v_add3_u32 v81, v98, v81, s7
	v_bfe_u32 v82, v99, 16, 1
	v_pk_fma_f32 v[96:97], v[2:3], v[96:97], v[10:11]
	v_lshrrev_b32_e32 v81, 16, v81
	v_add3_u32 v82, v99, v82, s7
	v_and_or_b32 v81, v82, s5, v81
	v_bfe_u32 v82, v96, 16, 1
	v_add3_u32 v82, v96, v82, s7
	v_bfe_u32 v83, v97, 16, 1
	v_pk_fma_f32 v[100:101], v[4:5], v[100:101], v[12:13]
	v_lshrrev_b32_e32 v82, 16, v82
	v_add3_u32 v83, v97, v83, s7
	v_and_or_b32 v82, v83, s5, v82
	v_bfe_u32 v83, v100, 16, 1
	v_add3_u32 v83, v100, v83, s7
	v_bfe_u32 v88, v101, 16, 1
	v_lshrrev_b32_e32 v83, 16, v83
	v_add3_u32 v88, v101, v88, s7
	v_and_or_b32 v83, v88, s5, v83
	global_store_dwordx4 v[72:73], v[80:83], off offset:-1024
	v_bfe_u32 v72, v104, 16, 1
	v_add3_u32 v72, v104, v72, s7
	v_bfe_u32 v73, v105, 16, 1
	v_lshrrev_b32_e32 v72, 16, v72
	v_add3_u32 v73, v105, v73, s7
	v_and_or_b32 v80, v73, s5, v72
	v_bfe_u32 v72, v102, 16, 1
	v_add3_u32 v72, v102, v72, s7
	v_bfe_u32 v73, v103, 16, 1
	v_lshrrev_b32_e32 v72, 16, v72
	v_add3_u32 v73, v103, v73, s7
	v_and_or_b32 v81, v73, s5, v72
	v_bfe_u32 v72, v86, 16, 1
	v_add3_u32 v72, v86, v72, s7
	v_bfe_u32 v73, v87, 16, 1
	v_lshrrev_b32_e32 v72, 16, v72
	v_add3_u32 v73, v87, v73, s7
	v_and_or_b32 v82, v73, s5, v72
	v_bfe_u32 v72, v84, 16, 1
	v_add3_u32 v72, v84, v72, s7
	v_bfe_u32 v73, v85, 16, 1
	v_lshrrev_b32_e32 v72, 16, v72
	v_add3_u32 v73, v85, v73, s7
	v_and_or_b32 v83, v73, s5, v72
	global_store_dwordx4 v[70:71], v[80:83], off offset:-4096
	s_cbranch_scc1 .LBB0_726
	v_add3_u32 v42, v66, s4, 9
	v_ashrrev_i32_e32 v43, 31, v42
	v_lshlrev_b64 v[42:43], 11, v[42:43]
	v_lshl_add_u64 v[46:47], v[68:69], 0, v[42:43]
	global_load_dwordx4 v[42:45], v[46:47], off
	s_nop 0
	global_load_dwordx4 v[46:49], v[46:47], off offset:1024
.LBB0_726:
	s_waitcnt vmcnt(7)
	v_lshlrev_b32_e32 v91, 16, v51
	v_lshlrev_b32_e32 v90, 16, v50
	v_and_b32_e32 v93, 0xffff0000, v51
	v_and_b32_e32 v92, 0xffff0000, v50
	v_pk_add_f32 v[94:95], v[90:91], v[92:93]
	v_and_b32_e32 v97, 0xffff0000, v53
	v_add_f32_e32 v83, v94, v95
	v_lshlrev_b32_e32 v95, 16, v53
	v_lshlrev_b32_e32 v94, 16, v52
	v_and_b32_e32 v96, 0xffff0000, v52
	v_pk_add_f32 v[98:99], v[94:95], v[96:97]
	s_waitcnt vmcnt(6)
	v_lshlrev_b32_e32 v72, 16, v54
	v_and_b32_e32 v73, 0xffff0000, v54
	v_lshlrev_b32_e32 v80, 16, v55
	v_and_b32_e32 v81, 0xffff0000, v55
	v_pk_add_f32 v[98:99], v[98:99], v[98:99] op_sel_hi:[0,1]
	v_lshlrev_b32_e32 v82, 16, v56
	v_and_b32_e32 v84, 0xffff0000, v56
	v_lshlrev_b32_e32 v86, 16, v57
	v_and_b32_e32 v88, 0xffff0000, v57
	v_add_f32_e32 v89, 0, v83
	v_add_f32_e32 v83, v72, v73
	v_add_f32_e32 v85, v80, v81
	v_mov_b32_e32 v87, v99
	v_pk_add_f32 v[100:101], v[82:83], v[84:85]
	v_pk_add_f32 v[98:99], v[86:87], v[88:89]
	s_nop 0
	v_pk_add_f32 v[98:99], v[100:101], v[98:99]
	s_nop 0
	v_add_f32_e32 v83, v98, v99
	s_waitcnt lgkmcnt(0)
	s_nop 1
	v_add_f32_dpp v83, v83, v83 quad_perm:[1,0,3,2] row_mask:0xf bank_mask:0xf
	s_nop 1
	v_add_f32_dpp v83, v83, v83 quad_perm:[2,3,0,1] row_mask:0xf bank_mask:0xf
	s_nop 1
	v_add_f32_dpp v83, v83, v83 row_half_mirror row_mask:0xf bank_mask:0xf
	s_nop 1
	v_add_f32_dpp v83, v83, v83 row_mirror row_mask:0xf bank_mask:0xf
	v_mov_b32_e32 v85, v83
	s_nop 1
	v_permlane16_swap_b32_e32 v83, v85
	v_add_f32_e32 v83, v83, v85
	v_mov_b32_e32 v85, v83
	s_nop 1
	v_permlane32_swap_b32_e32 v83, v85
	v_add_f32_e32 v83, v83, v85
	v_fmac_f32_e32 v92, 0xba800000, v83
	v_fmac_f32_e32 v93, 0xba800000, v83
	v_fmac_f32_e32 v91, 0xba800000, v83
	v_fmac_f32_e32 v90, 0xba800000, v83
	v_mov_b32_e32 v98, v91
	v_mov_b32_e32 v99, v93
	v_mov_b32_e32 v91, v92
	v_pk_mul_f32 v[100:101], v[98:99], v[98:99]
	v_pk_mul_f32 v[92:93], v[90:91], v[90:91]
	v_fmac_f32_e32 v96, 0xba800000, v83
	v_pk_mov_b32 v[102:103], v[92:93], v[100:101] op_sel:[1,0]
	v_mov_b32_e32 v93, v101
	v_fmac_f32_e32 v97, 0xba800000, v83
	v_fmac_f32_e32 v95, 0xba800000, v83
	v_pk_add_f32 v[92:93], v[102:103], v[92:93]
	v_fmac_f32_e32 v94, 0xba800000, v83
	v_mov_b32_e32 v100, v95
	v_mov_b32_e32 v101, v97
	v_mov_b32_e32 v95, v96
	v_pk_add_f32 v[92:93], v[92:93], v[92:93] op_sel_hi:[0,1]
	v_pk_mul_f32 v[102:103], v[100:101], v[100:101]
	v_pk_mul_f32 v[96:97], v[94:95], v[94:95]
	v_fmac_f32_e32 v72, 0xba800000, v83
	v_pk_mov_b32 v[104:105], v[96:97], v[102:103] op_sel:[1,0]
	v_mov_b32_e32 v97, v103
	v_fmac_f32_e32 v73, 0xba800000, v83
	v_fmac_f32_e32 v80, 0xba800000, v83
	v_mul_f32_e32 v92, v72, v72
	v_pk_add_f32 v[96:97], v[104:105], v[96:97]
	v_fmac_f32_e32 v81, 0xba800000, v83
	v_pk_fma_f32 v[102:103], v[72:73], v[72:73], v[92:93] op_sel_hi:[1,1,0]
	v_mul_f32_e32 v92, v80, v80
	v_pk_add_f32 v[96:97], v[96:97], v[96:97] op_sel_hi:[0,1]
	v_pk_fma_f32 v[104:105], v[80:81], v[80:81], v[92:93] op_sel_hi:[1,1,0]
	v_fmac_f32_e32 v88, 0xba800000, v83
	v_fmac_f32_e32 v86, 0xba800000, v83
	v_fmac_f32_e32 v84, 0xba800000, v83
	v_fmac_f32_e32 v82, 0xba800000, v83
	v_mul_f32_e32 v102, v82, v82
	v_mul_f32_e32 v104, v84, v84
	v_mul_f32_e32 v92, v86, v86
	v_mul_f32_e32 v96, v88, v88
	v_pk_add_f32 v[102:103], v[102:103], v[104:105]
	v_pk_add_f32 v[92:93], v[92:93], v[96:97]
	s_nop 0
	v_pk_add_f32 v[92:93], v[102:103], v[92:93]
	s_nop 0
	v_add_f32_e32 v83, v92, v93
	s_waitcnt lgkmcnt(0)
	s_nop 1
	v_add_f32_dpp v83, v83, v83 quad_perm:[1,0,3,2] row_mask:0xf bank_mask:0xf
	s_nop 1
	v_add_f32_dpp v83, v83, v83 quad_perm:[2,3,0,1] row_mask:0xf bank_mask:0xf
	s_nop 1
	v_add_f32_dpp v83, v83, v83 row_half_mirror row_mask:0xf bank_mask:0xf
	s_nop 1
	v_add_f32_dpp v83, v83, v83 row_mirror row_mask:0xf bank_mask:0xf
	v_mov_b32_e32 v85, v83
	s_nop 1
	v_permlane16_swap_b32_e32 v83, v85
	v_add_f32_e32 v83, v83, v85
	v_mov_b32_e32 v85, v83
	s_nop 1
	v_permlane32_swap_b32_e32 v83, v85
	v_add_f32_e32 v83, v83, v85
	v_fmamk_f32 v83, v83, 0x3a800000, v78
	v_mul_f32_e32 v85, 0x4f800000, v83
	v_cmp_gt_f32_e32 vcc, s6, v83
	s_nop 1
	v_cndmask_b32_e32 v83, v83, v85, vcc
	v_sqrt_f32_e32 v85, v83
	s_nop 0
	v_add_u32_e32 v87, -1, v85
	v_fma_f32 v89, -v87, v85, v83
	v_cmp_ge_f32_e64 s[0:1], 0, v89
	v_add_u32_e32 v89, 1, v85
	s_nop 0
	v_cndmask_b32_e64 v87, v85, v87, s[0:1]
	v_fma_f32 v85, -v89, v85, v83
	v_cmp_lt_f32_e64 s[0:1], 0, v85
	s_nop 1
	v_cndmask_b32_e64 v85, v87, v89, s[0:1]
	v_mul_f32_e32 v87, 0x37800000, v85
	v_cndmask_b32_e32 v85, v85, v87, vcc
	v_cmp_class_f32_e32 vcc, v83, v79
	s_nop 1
	v_cndmask_b32_e32 v83, v85, v83, vcc
	v_div_scale_f32 v85, s[0:1], v83, v83, 1.0
	v_rcp_f32_e32 v87, v85
	s_add_i32 s0, s4, 7
	s_cmp_gt_u32 s0, 12
	v_fma_f32 v89, -v85, v87, 1.0
	v_fmac_f32_e32 v87, v89, v87
	v_div_scale_f32 v89, vcc, 1.0, v83, 1.0
	v_mul_f32_e32 v92, v89, v87
	v_fma_f32 v93, -v85, v92, v89
	v_fmac_f32_e32 v92, v93, v87
	v_fma_f32 v85, -v85, v92, v89
	v_div_fmas_f32 v85, v85, v87, v92
	v_div_fixup_f32 v92, v85, v83, 1.0
	v_pk_mul_f32 v[90:91], v[90:91], v[92:93] op_sel_hi:[1,0]
	v_pk_mul_f32 v[80:81], v[80:81], v[92:93] op_sel_hi:[1,0]
	v_mov_b32_e32 v83, v84
	v_pk_mul_f32 v[96:97], v[98:99], v[92:93] op_sel_hi:[1,0]
	v_pk_fma_f32 v[90:91], v[6:7], v[90:91], v[14:15]
	v_pk_mul_f32 v[98:99], v[100:101], v[92:93] op_sel_hi:[1,0]
	v_pk_fma_f32 v[100:101], v[24:25], v[80:81], v[32:33]
	v_pk_mul_f32 v[80:81], v[82:83], v[92:93] op_sel_hi:[1,0]
	v_mov_b32_e32 v87, v88
	v_pk_mul_f32 v[82:83], v[86:87], v[92:93] op_sel_hi:[1,0]
	v_pk_fma_f32 v[86:87], v[18:19], v[80:81], v[26:27]
	v_bfe_u32 v80, v90, 16, 1
	v_add3_u32 v80, v90, v80, s7
	v_bfe_u32 v81, v91, 16, 1
	v_pk_fma_f32 v[96:97], v[8:9], v[96:97], v[16:17]
	v_lshrrev_b32_e32 v80, 16, v80
	v_add3_u32 v81, v91, v81, s7
	v_and_or_b32 v80, v81, s5, v80
	v_bfe_u32 v81, v96, 16, 1
	v_pk_mul_f32 v[94:95], v[94:95], v[92:93] op_sel_hi:[1,0]
	v_pk_fma_f32 v[84:85], v[20:21], v[82:83], v[28:29]
	v_add3_u32 v81, v96, v81, s7
	v_bfe_u32 v82, v97, 16, 1
	v_pk_fma_f32 v[94:95], v[2:3], v[94:95], v[10:11]
	v_lshrrev_b32_e32 v81, 16, v81
	v_add3_u32 v82, v97, v82, s7
	v_and_or_b32 v81, v82, s5, v81
	v_bfe_u32 v82, v94, 16, 1
	v_add3_u32 v82, v94, v82, s7
	v_bfe_u32 v83, v95, 16, 1
	v_pk_fma_f32 v[98:99], v[4:5], v[98:99], v[12:13]
	v_lshrrev_b32_e32 v82, 16, v82
	v_add3_u32 v83, v95, v83, s7
	v_and_or_b32 v82, v83, s5, v82
	v_bfe_u32 v83, v98, 16, 1
	v_add3_u32 v83, v98, v83, s7
	v_bfe_u32 v88, v99, 16, 1
	v_pk_mul_f32 v[72:73], v[72:73], v[92:93] op_sel_hi:[1,0]
	v_lshrrev_b32_e32 v83, 16, v83
	v_add3_u32 v88, v99, v88, s7
	v_pk_fma_f32 v[72:73], v[22:23], v[72:73], v[30:31]
	v_and_or_b32 v83, v88, s5, v83
	global_store_dwordx4 v[70:71], v[80:83], off offset:-3072
	s_nop 1
	v_bfe_u32 v80, v72, 16, 1
	v_add3_u32 v72, v72, v80, s7
	v_bfe_u32 v80, v73, 16, 1
	v_lshrrev_b32_e32 v72, 16, v72
	v_add3_u32 v73, v73, v80, s7
	v_and_or_b32 v80, v73, s5, v72
	v_bfe_u32 v72, v100, 16, 1
	v_add3_u32 v72, v100, v72, s7
	v_bfe_u32 v73, v101, 16, 1
	v_lshrrev_b32_e32 v72, 16, v72
	v_add3_u32 v73, v101, v73, s7
	v_and_or_b32 v81, v73, s5, v72
	v_bfe_u32 v72, v86, 16, 1
	v_add3_u32 v72, v86, v72, s7
	v_bfe_u32 v73, v87, 16, 1
	v_lshrrev_b32_e32 v72, 16, v72
	v_add3_u32 v73, v87, v73, s7
	v_and_or_b32 v82, v73, s5, v72
	v_bfe_u32 v72, v84, 16, 1
	v_add3_u32 v72, v84, v72, s7
	v_bfe_u32 v73, v85, 16, 1
	v_lshrrev_b32_e32 v72, 16, v72
	v_add3_u32 v73, v85, v73, s7
	v_and_or_b32 v83, v73, s5, v72
	global_store_dwordx4 v[70:71], v[80:83], off offset:-2048
	s_cbranch_scc1 .LBB0_721
	v_add3_u32 v50, v66, s4, 10
	v_ashrrev_i32_e32 v51, 31, v50
	v_lshlrev_b64 v[50:51], 11, v[50:51]
	v_lshl_add_u64 v[54:55], v[68:69], 0, v[50:51]
	global_load_dwordx4 v[50:53], v[54:55], off
	s_nop 0
	global_load_dwordx4 v[54:57], v[54:55], off offset:1024
	s_branch .LBB0_721

.LBB0_964:
	v_lshl_add_u64 v[6:7], v[46:47], 0, s[24:25]
	v_add_co_u32_e32 v2, vcc, 0x10a00000, v6
	s_nop 1
	v_addc_co_u32_e32 v3, vcc, 0, v7, vcc
	s_barrier
	global_load_dwordx4 v[2:5], v[2:3], off offset:512
	v_lshl_add_u64 v[6:7], v[6:7], 0, s[26:27]
	global_load_dwordx4 v[6:9], v[6:7], off offset:16
	v_add_u32_e32 v50, s24, v44
	v_ashrrev_i32_e32 v51, 31, v50
	s_waitcnt vmcnt(1)
	v_lshlrev_b32_e32 v10, 16, v2
	v_and_b32_e32 v2, 0xffff0000, v2
	v_add_f32_e32 v18, 0, v10
	v_lshlrev_b32_e32 v11, 16, v3
	v_add_f32_e32 v18, v18, v2
	v_and_b32_e32 v3, 0xffff0000, v3
	v_add_f32_e32 v18, v18, v11
	v_lshlrev_b32_e32 v12, 16, v4
	v_add_f32_e32 v18, v18, v3
	v_and_b32_e32 v4, 0xffff0000, v4
	v_add_f32_e32 v18, v18, v12
	v_lshlrev_b32_e32 v13, 16, v5
	v_add_f32_e32 v18, v18, v4
	v_and_b32_e32 v5, 0xffff0000, v5
	v_add_f32_e32 v18, v18, v13
	s_waitcnt vmcnt(0)
	v_lshlrev_b32_e32 v14, 16, v6
	v_add_f32_e32 v18, v18, v5
	v_and_b32_e32 v6, 0xffff0000, v6
	v_add_f32_e32 v18, v18, v14
	v_lshlrev_b32_e32 v15, 16, v7
	v_add_f32_e32 v18, v18, v6
	v_and_b32_e32 v7, 0xffff0000, v7
	v_add_f32_e32 v18, v18, v15
	v_lshlrev_b32_e32 v16, 16, v8
	v_add_f32_e32 v18, v18, v7
	v_and_b32_e32 v8, 0xffff0000, v8
	v_add_f32_e32 v18, v18, v16
	v_lshlrev_b32_e32 v17, 16, v9
	v_add_f32_e32 v18, v18, v8
	v_and_b32_e32 v9, 0xffff0000, v9
	v_add_f32_e32 v18, v18, v17
	v_add_f32_e32 v18, v18, v9
	s_waitcnt lgkmcnt(0)
	s_nop 1
	v_add_f32_dpp v18, v18, v18 quad_perm:[1,0,3,2] row_mask:0xf bank_mask:0xf
	s_nop 1
	v_add_f32_dpp v18, v18, v18 quad_perm:[2,3,0,1] row_mask:0xf bank_mask:0xf
	v_fmac_f32_e32 v2, 0xbc800000, v18
	v_fmac_f32_e32 v10, 0xbc800000, v18
	v_fmac_f32_e32 v11, 0xbc800000, v18
	v_fmac_f32_e32 v3, 0xbc800000, v18
	v_fmac_f32_e32 v12, 0xbc800000, v18
	v_fmac_f32_e32 v4, 0xbc800000, v18
	v_fmac_f32_e32 v13, 0xbc800000, v18
	v_fmac_f32_e32 v5, 0xbc800000, v18
	v_fmac_f32_e32 v14, 0xbc800000, v18
	v_fmac_f32_e32 v6, 0xbc800000, v18
	v_fmac_f32_e32 v15, 0xbc800000, v18
	v_fmac_f32_e32 v7, 0xbc800000, v18
	v_fmac_f32_e32 v16, 0xbc800000, v18
	v_fmac_f32_e32 v8, 0xbc800000, v18
	v_fmac_f32_e32 v17, 0xbc800000, v18
	v_fmac_f32_e32 v9, 0xbc800000, v18
	v_mul_f32_e32 v18, v2, v2
	v_fmac_f32_e32 v18, v10, v10
	v_fmac_f32_e32 v18, v11, v11
	v_fmac_f32_e32 v18, v3, v3
	v_fmac_f32_e32 v18, v12, v12
	v_fmac_f32_e32 v18, v4, v4
	v_fmac_f32_e32 v18, v13, v13
	v_fmac_f32_e32 v18, v5, v5
	v_fmac_f32_e32 v18, v14, v14
	v_fmac_f32_e32 v18, v6, v6
	v_fmac_f32_e32 v18, v15, v15
	v_fmac_f32_e32 v18, v7, v7
	v_fmac_f32_e32 v18, v16, v16
	v_fmac_f32_e32 v18, v8, v8
	v_fmac_f32_e32 v18, v17, v17
	v_fmac_f32_e32 v18, v9, v9
	s_waitcnt lgkmcnt(0)
	s_nop 1
	v_add_f32_dpp v18, v18, v18 quad_perm:[1,0,3,2] row_mask:0xf bank_mask:0xf
	s_nop 1
	v_add_f32_dpp v18, v18, v18 quad_perm:[2,3,0,1] row_mask:0xf bank_mask:0xf
	v_fmamk_f32 v18, v18, 0x3c800000, v39
	v_mul_f32_e32 v19, 0x4f800000, v18
	v_cmp_gt_f32_e32 vcc, s28, v18
	s_nop 1
	v_cndmask_b32_e32 v18, v18, v19, vcc
	v_sqrt_f32_e32 v19, v18
	s_nop 0
	v_add_u32_e32 v20, -1, v19
	v_add_u32_e32 v21, 1, v19
	v_fma_f32 v22, -v20, v19, v18
	v_fma_f32 v23, -v21, v19, v18
	v_cmp_ge_f32_e64 s[0:1], 0, v22
	s_nop 1
	v_cndmask_b32_e64 v19, v19, v20, s[0:1]
	v_cmp_lt_f32_e64 s[0:1], 0, v23
	s_nop 1
	v_cndmask_b32_e64 v19, v19, v21, s[0:1]
	v_mul_f32_e32 v20, 0x37800000, v19
	v_cndmask_b32_e32 v19, v19, v20, vcc
	v_cmp_class_f32_e32 vcc, v18, v54
	s_nop 1
	v_cndmask_b32_e32 v18, v19, v18, vcc
	v_div_scale_f32 v19, s[0:1], v18, v18, 1.0
	v_rcp_f32_e32 v20, v19
	v_div_scale_f32 v21, vcc, 1.0, v18, 1.0
	v_fma_f32 v22, -v19, v20, 1.0
	v_fmac_f32_e32 v20, v22, v20
	v_mul_f32_e32 v22, v21, v20
	v_fma_f32 v23, -v19, v22, v21
	v_fmac_f32_e32 v22, v23, v20
	v_fma_f32 v19, -v19, v22, v21
	v_div_fmas_f32 v19, v19, v20, v22
	v_div_fixup_f32 v18, v19, v18, 1.0
	v_mul_f32_e32 v10, v10, v18
	v_mul_f32_e32 v2, v2, v18
	v_mul_f32_e32 v11, v11, v18
	v_mul_f32_e32 v3, v3, v18
	v_mul_f32_e32 v12, v12, v18
	v_mul_f32_e32 v4, v4, v18
	v_mul_f32_e32 v13, v13, v18
	v_mul_f32_e32 v5, v5, v18
	v_mul_f32_e32 v14, v14, v18
	v_mul_f32_e32 v6, v6, v18
	v_mul_f32_e32 v15, v15, v18
	v_mul_f32_e32 v7, v7, v18
	v_mul_f32_e32 v16, v16, v18
	v_mul_f32_e32 v8, v8, v18
	v_bfe_u32 v19, v10, 16, 1
	v_bfe_u32 v20, v2, 16, 1
	v_mul_f32_e32 v17, v17, v18
	v_bfe_u32 v21, v11, 16, 1
	v_bfe_u32 v22, v3, 16, 1
	v_bfe_u32 v23, v12, 16, 1
	v_bfe_u32 v24, v4, 16, 1
	v_bfe_u32 v25, v13, 16, 1
	v_bfe_u32 v26, v5, 16, 1
	v_bfe_u32 v27, v14, 16, 1
	v_bfe_u32 v28, v6, 16, 1
	v_bfe_u32 v29, v15, 16, 1
	v_bfe_u32 v30, v7, 16, 1
	v_bfe_u32 v31, v16, 16, 1
	v_bfe_u32 v32, v8, 16, 1
	v_add3_u32 v10, v10, v19, s30
	v_add3_u32 v2, v2, v20, s30
	v_add3_u32 v11, v11, v21, s30
	v_add3_u32 v3, v3, v22, s30
	v_add3_u32 v12, v12, v23, s30
	v_add3_u32 v4, v4, v24, s30
	v_add3_u32 v13, v13, v25, s30
	v_add3_u32 v5, v5, v26, s30
	v_add3_u32 v14, v14, v27, s30
	v_add3_u32 v6, v6, v28, s30
	v_add3_u32 v15, v15, v29, s30
	v_add3_u32 v7, v7, v30, s30
	v_add3_u32 v16, v16, v31, s30
	v_add3_u32 v8, v8, v32, s30
	ds_write_b16_d16_hi v56, v10
	ds_write_b16_d16_hi v56, v2 offset:272
	ds_write_b16_d16_hi v56, v11 offset:544
	ds_write_b16_d16_hi v56, v3 offset:816
	ds_write_b16_d16_hi v56, v12 offset:1088
	ds_write_b16_d16_hi v56, v4 offset:1360
	ds_write_b16_d16_hi v56, v13 offset:1632
	ds_write_b16_d16_hi v56, v5 offset:1904
	ds_write_b16_d16_hi v56, v14 offset:2176
	ds_write_b16_d16_hi v56, v6 offset:2448
	ds_write_b16_d16_hi v56, v15 offset:2720
	ds_write_b16_d16_hi v56, v7 offset:2992
	ds_write_b16_d16_hi v56, v16 offset:3264
	ds_write_b16_d16_hi v56, v8 offset:3536
	v_bfe_u32 v2, v17, 16, 1
	v_add3_u32 v2, v17, v2, s30
	ds_write_b16_d16_hi v56, v2 offset:3808
	v_mul_f32_e32 v2, v9, v18
	v_bfe_u32 v3, v2, 16, 1
	v_add3_u32 v2, v2, v3, s30
	ds_write_b16_d16_hi v56, v2 offset:4080
	v_lshlrev_b64 v[2:3], 8, v[50:51]
	s_and_b64 vcc, exec, s[2:3]
	v_lshl_add_u64 v[2:3], v[42:43], 0, v[2:3]
	s_cbranch_vccnz .LBB0_969
	global_load_dwordx4 v[30:33], v[2:3], off
	v_cndmask_b32_e64 v4, 0, 1, s[16:17]
	v_cmp_ne_u32_e64 s[8:9], 1, v4
	s_andn2_b64 vcc, exec, s[16:17]
	s_cbranch_vccz .LBB0_970

.LBB0_1233:
	s_waitcnt vmcnt(5)
	v_lshlrev_b32_e32 v217, 16, v163
	s_waitcnt lgkmcnt(2)
	v_lshlrev_b32_e32 v216, 16, v162
	v_and_b32_e32 v187, 0xffff0000, v163
	v_and_b32_e32 v186, 0xffff0000, v162
	v_pk_add_f32 v[188:189], v[216:217], v[186:187]
	v_lshlrev_b32_e32 v235, 16, v165
	v_add_f32_e32 v188, v188, v189
	v_add_f32_e32 v233, 0, v188
	v_lshlrev_b32_e32 v234, 16, v164
	v_and_b32_e32 v189, 0xffff0000, v165
	v_and_b32_e32 v188, 0xffff0000, v164
	v_pk_add_f32 v[190:191], v[234:235], v[188:189]
	s_waitcnt vmcnt(4)
	v_lshlrev_b32_e32 v194, 16, v166
	v_and_b32_e32 v195, 0xffff0000, v166
	v_lshlrev_b32_e32 v196, 16, v167
	v_and_b32_e32 v197, 0xffff0000, v167
	v_pk_add_f32 v[190:191], v[190:191], v[190:191] op_sel_hi:[0,1]
	v_lshlrev_b32_e32 v212, 16, v168
	v_and_b32_e32 v214, 0xffff0000, v168
	s_waitcnt lgkmcnt(1)
	v_lshlrev_b32_e32 v218, 16, v169
	s_waitcnt lgkmcnt(0)
	v_and_b32_e32 v232, 0xffff0000, v169
	v_add_f32_e32 v213, v194, v195
	v_add_f32_e32 v215, v196, v197
	v_mov_b32_e32 v219, v191
	v_pk_add_f32 v[192:193], v[212:213], v[214:215]
	v_pk_add_f32 v[190:191], v[218:219], v[232:233]
	s_nop 0
	v_pk_add_f32 v[190:191], v[192:193], v[190:191]
	s_nop 0
	v_add_f32_e32 v190, v190, v191
	s_waitcnt lgkmcnt(0)
	s_nop 1
	v_add_f32_dpp v190, v190, v190 quad_perm:[1,0,3,2] row_mask:0xf bank_mask:0xf
	s_nop 1
	v_add_f32_dpp v190, v190, v190 quad_perm:[2,3,0,1] row_mask:0xf bank_mask:0xf
	s_nop 1
	v_add_f32_dpp v190, v190, v190 row_half_mirror row_mask:0xf bank_mask:0xf
	s_nop 1
	v_add_f32_dpp v190, v190, v190 row_mirror row_mask:0xf bank_mask:0xf
	v_mov_b32_e32 v191, v190
	s_nop 1
	v_permlane16_swap_b32_e32 v190, v191
	v_add_f32_e32 v190, v190, v191
	v_mov_b32_e32 v191, v190
	s_nop 1
	v_permlane32_swap_b32_e32 v190, v191
	v_add_f32_e32 v210, v190, v191
	v_fmac_f32_e32 v186, 0xba800000, v210
	v_fmac_f32_e32 v187, 0xba800000, v210
	v_fmac_f32_e32 v217, 0xba800000, v210
	v_fmac_f32_e32 v216, 0xba800000, v210
	v_mov_b32_e32 v236, v217
	v_mov_b32_e32 v237, v187
	v_mov_b32_e32 v217, v186
	v_pk_mul_f32 v[190:191], v[236:237], v[236:237]
	v_pk_mul_f32 v[186:187], v[216:217], v[216:217]
	v_fmac_f32_e32 v188, 0xba800000, v210
	v_pk_mov_b32 v[192:193], v[186:187], v[190:191] op_sel:[1,0]
	v_mov_b32_e32 v187, v191
	v_fmac_f32_e32 v189, 0xba800000, v210
	v_fmac_f32_e32 v235, 0xba800000, v210
	v_pk_add_f32 v[186:187], v[192:193], v[186:187]
	v_fmac_f32_e32 v234, 0xba800000, v210
	v_mov_b32_e32 v238, v235
	v_mov_b32_e32 v239, v189
	v_mov_b32_e32 v235, v188
	v_pk_add_f32 v[186:187], v[186:187], v[186:187] op_sel_hi:[0,1]
	v_pk_mul_f32 v[190:191], v[238:239], v[238:239]
	v_pk_mul_f32 v[188:189], v[234:235], v[234:235]
	v_fmac_f32_e32 v194, 0xba800000, v210
	v_pk_mov_b32 v[192:193], v[188:189], v[190:191] op_sel:[1,0]
	v_mov_b32_e32 v189, v191
	v_fmac_f32_e32 v195, 0xba800000, v210
	v_fmac_f32_e32 v196, 0xba800000, v210
	v_mul_f32_e32 v186, v194, v194
	v_pk_add_f32 v[188:189], v[192:193], v[188:189]
	v_fmac_f32_e32 v197, 0xba800000, v210
	v_pk_fma_f32 v[190:191], v[194:195], v[194:195], v[186:187] op_sel_hi:[1,1,0]
	v_mul_f32_e32 v186, v196, v196
	v_pk_add_f32 v[188:189], v[188:189], v[188:189] op_sel_hi:[0,1]
	v_pk_fma_f32 v[192:193], v[196:197], v[196:197], v[186:187] op_sel_hi:[1,1,0]
	v_fmac_f32_e32 v232, 0xba800000, v210
	v_fmac_f32_e32 v218, 0xba800000, v210
	v_fmac_f32_e32 v214, 0xba800000, v210
	v_fmac_f32_e32 v212, 0xba800000, v210
	v_mul_f32_e32 v190, v212, v212
	v_mul_f32_e32 v192, v214, v214
	v_mul_f32_e32 v186, v218, v218
	v_mul_f32_e32 v188, v232, v232
	v_pk_add_f32 v[190:191], v[190:191], v[192:193]
	v_pk_add_f32 v[186:187], v[186:187], v[188:189]
	v_lshl_add_u64 v[210:211], s[94:95], 0, v[208:209]
	v_pk_add_f32 v[186:187], v[190:191], v[186:187]
	v_add_co_u32_e32 v190, vcc, 0xca01000, v210
	v_add_f32_e32 v186, v186, v187
	ds_bpermute_b32 v187, v220, v186
	v_addc_co_u32_e32 v191, vcc, 0, v211, vcc
	s_waitcnt lgkmcnt(0)
	v_add_f32_e32 v186, v186, v187
	ds_bpermute_b32 v187, v221, v186
	s_waitcnt lgkmcnt(0)
	v_add_f32_e32 v186, v186, v187
	ds_bpermute_b32 v187, v222, v186
	s_waitcnt lgkmcnt(0)
	v_add_f32_e32 v186, v186, v187
	ds_bpermute_b32 v187, v223, v186
	s_waitcnt lgkmcnt(0)
	v_add_f32_e32 v186, v186, v187
	ds_bpermute_b32 v187, v224, v186
	s_waitcnt lgkmcnt(0)
	v_add_f32_e32 v186, v186, v187
	ds_bpermute_b32 v187, v225, v186
	s_waitcnt lgkmcnt(0)
	v_add_f32_e32 v186, v186, v187
	v_fmamk_f32 v186, v186, 0x3a800000, v228
	v_mul_f32_e32 v187, 0x4f800000, v186
	v_cmp_gt_f32_e64 s[0:1], s30, v186
	s_nop 1
	v_cndmask_b32_e64 v186, v186, v187, s[0:1]
	v_sqrt_f32_e32 v187, v186
	s_nop 0
	v_add_u32_e32 v188, -1, v187
	v_fma_f32 v189, -v188, v187, v186
	v_cmp_ge_f32_e64 s[4:5], 0, v189
	v_add_u32_e32 v189, 1, v187
	s_nop 0
	v_cndmask_b32_e64 v188, v187, v188, s[4:5]
	v_fma_f32 v187, -v189, v187, v186
	v_cmp_lt_f32_e64 s[4:5], 0, v187
	s_nop 1
	v_cndmask_b32_e64 v187, v188, v189, s[4:5]
	v_mul_f32_e32 v188, 0x37800000, v187
	v_cndmask_b32_e64 v187, v187, v188, s[0:1]
	v_cmp_class_f32_e64 s[0:1], v186, v229
	s_nop 1
	v_cndmask_b32_e64 v213, v187, v186, s[0:1]
	v_div_scale_f32 v215, s[0:1], v213, v213, 1.0
	v_rcp_f32_e32 v219, v215
	global_load_dwordx4 v[186:189], v[190:191], off offset:2048
	s_nop 0
	global_load_dwordx4 v[190:193], v[190:191], off offset:3072
	v_fma_f32 v233, -v215, v219, 1.0
	v_fmac_f32_e32 v219, v233, v219
	v_div_scale_f32 v233, vcc, 1.0, v213, 1.0
	v_mul_f32_e32 v240, v233, v219
	v_fma_f32 v241, -v215, v240, v233
	v_fmac_f32_e32 v240, v241, v219
	v_fma_f32 v215, -v215, v240, v233
	v_div_fmas_f32 v215, v215, v219, v240
	v_div_fixup_f32 v240, v215, v213, 1.0
	v_pk_mul_f32 v[216:217], v[216:217], v[240:241] op_sel_hi:[1,0]
	v_pk_mul_f32 v[194:195], v[194:195], v[240:241] op_sel_hi:[1,0]
	v_mov_b32_e32 v213, v214
	v_pk_fma_f32 v[242:243], v[2:3], v[216:217], v[6:7]
	v_pk_mul_f32 v[216:217], v[234:235], v[240:241] op_sel_hi:[1,0]
	v_pk_mul_f32 v[196:197], v[196:197], v[240:241] op_sel_hi:[1,0]
	v_pk_fma_f32 v[244:245], v[18:19], v[194:195], v[30:31]
	v_pk_mul_f32 v[194:195], v[212:213], v[240:241] op_sel_hi:[1,0]
	v_mov_b32_e32 v219, v232
	v_pk_mul_f32 v[234:235], v[238:239], v[240:241] op_sel_hi:[1,0]
	v_pk_fma_f32 v[238:239], v[14:15], v[216:217], v[26:27]
	v_pk_fma_f32 v[216:217], v[20:21], v[196:197], v[32:33]
	v_pk_mul_f32 v[196:197], v[218:219], v[240:241] op_sel_hi:[1,0]
	v_pk_fma_f32 v[218:219], v[10:11], v[194:195], v[22:23]
	v_bfe_u32 v194, v242, 16, 1
	v_pk_mul_f32 v[236:237], v[236:237], v[240:241] op_sel_hi:[1,0]
	v_add3_u32 v194, v242, v194, s31
	v_bfe_u32 v195, v243, 16, 1
	v_pk_fma_f32 v[236:237], v[4:5], v[236:237], v[8:9]
	v_lshrrev_b32_e32 v194, 16, v194
	v_add3_u32 v195, v243, v195, s31
	v_and_or_b32 v194, v195, s29, v194
	v_bfe_u32 v195, v236, 16, 1
	v_pk_fma_f32 v[214:215], v[12:13], v[196:197], v[24:25]
	v_add3_u32 v195, v236, v195, s31
	v_bfe_u32 v196, v237, 16, 1
	v_lshrrev_b32_e32 v195, 16, v195
	v_add3_u32 v196, v237, v196, s31
	v_and_or_b32 v195, v196, s29, v195
	v_bfe_u32 v196, v238, 16, 1
	v_add3_u32 v196, v238, v196, s31
	v_bfe_u32 v197, v239, 16, 1
	v_fma_f32 v240, v36, v242, 0
	v_fma_f32 v241, v37, v242, 0
	v_fma_f32 v246, v38, v242, 0
	v_fma_f32 v247, v39, v242, 0
	v_fma_f32 v248, v40, v242, 0
	v_fma_f32 v249, v41, v242, 0
	v_pk_fma_f32 v[232:233], v[34:35], v[242:243], 0 op_sel_hi:[1,0,0]
	v_pk_fma_f32 v[234:235], v[16:17], v[234:235], v[28:29]
	v_lshrrev_b32_e32 v196, 16, v196
	v_add3_u32 v197, v239, v197, s31
	v_fmac_f32_e32 v240, v44, v243
	v_fmac_f32_e32 v241, v45, v243
	v_fmac_f32_e32 v246, v46, v243
	v_fmac_f32_e32 v247, v47, v243
	v_fmac_f32_e32 v248, v48, v243
	v_fmac_f32_e32 v249, v49, v243
	v_pk_fma_f32 v[232:233], v[42:43], v[242:243], v[232:233] op_sel:[0,1,0]
	v_and_or_b32 v196, v197, s29, v196
	v_bfe_u32 v197, v234, 16, 1
	v_fmac_f32_e32 v240, v52, v236
	v_fmac_f32_e32 v241, v53, v236
	v_fmac_f32_e32 v246, v54, v236
	v_fmac_f32_e32 v247, v55, v236
	v_fmac_f32_e32 v248, v56, v236
	v_fmac_f32_e32 v249, v57, v236
	v_pk_fma_f32 v[232:233], v[50:51], v[236:237], v[232:233] op_sel_hi:[1,0,1]
	v_add3_u32 v197, v234, v197, s31
	v_bfe_u32 v212, v235, 16, 1
	v_fmac_f32_e32 v240, v60, v237
	v_fmac_f32_e32 v241, v61, v237
	v_fmac_f32_e32 v246, v62, v237
	v_fmac_f32_e32 v247, v63, v237
	v_fmac_f32_e32 v248, v64, v237
	v_fmac_f32_e32 v249, v65, v237
	v_pk_fma_f32 v[232:233], v[58:59], v[236:237], v[232:233] op_sel:[0,1,0]
	v_lshrrev_b32_e32 v197, 16, v197
	v_add3_u32 v212, v235, v212, s31
	v_fmac_f32_e32 v240, v68, v238
	v_fmac_f32_e32 v241, v69, v238
	v_fmac_f32_e32 v246, v70, v238
	v_fmac_f32_e32 v247, v71, v238
	v_fmac_f32_e32 v248, v72, v238
	v_fmac_f32_e32 v249, v73, v238
	v_pk_fma_f32 v[232:233], v[66:67], v[238:239], v[232:233] op_sel_hi:[1,0,1]
	v_and_or_b32 v197, v212, s29, v197
	v_add_co_u32_e32 v212, vcc, s33, v210
	v_fmac_f32_e32 v240, v76, v239
	v_fmac_f32_e32 v241, v77, v239
	v_fmac_f32_e32 v246, v78, v239
	v_fmac_f32_e32 v247, v79, v239
	v_fmac_f32_e32 v248, v80, v239
	v_fmac_f32_e32 v249, v81, v239
	v_pk_fma_f32 v[232:233], v[74:75], v[238:239], v[232:233] op_sel:[0,1,0]
	v_addc_co_u32_e32 v213, vcc, 0, v211, vcc
	v_fmac_f32_e32 v240, v84, v234
	v_fmac_f32_e32 v241, v85, v234
	v_fmac_f32_e32 v246, v86, v234
	v_fmac_f32_e32 v247, v87, v234
	v_fmac_f32_e32 v248, v88, v234
	v_fmac_f32_e32 v249, v89, v234
	v_pk_fma_f32 v[232:233], v[82:83], v[234:235], v[232:233] op_sel_hi:[1,0,1]
	global_store_dwordx4 v[212:213], v[194:197], off
	v_fmac_f32_e32 v240, v92, v235
	v_fmac_f32_e32 v241, v93, v235
	v_bfe_u32 v194, v244, 16, 1
	v_fmac_f32_e32 v246, v94, v235
	v_fmac_f32_e32 v247, v95, v235
	v_fmac_f32_e32 v248, v96, v235
	v_fmac_f32_e32 v249, v97, v235
	v_pk_fma_f32 v[232:233], v[90:91], v[234:235], v[232:233] op_sel:[0,1,0]
	v_add3_u32 v194, v244, v194, s31
	v_bfe_u32 v195, v245, 16, 1
	v_fmac_f32_e32 v240, v108, v244
	v_fmac_f32_e32 v241, v109, v244
	v_fmac_f32_e32 v246, v98, v244
	v_fmac_f32_e32 v247, v99, v244
	v_fmac_f32_e32 v248, v100, v244
	v_fmac_f32_e32 v249, v101, v244
	v_pk_fma_f32 v[232:233], v[106:107], v[244:245], v[232:233] op_sel_hi:[1,0,1]
	v_lshrrev_b32_e32 v194, 16, v194
	v_add3_u32 v195, v245, v195, s31
	v_pk_fma_f32 v[232:233], v[102:103], v[244:245], v[232:233] op_sel:[0,1,0]
	v_fmac_f32_e32 v240, v104, v245
	v_fmac_f32_e32 v241, v105, v245
	v_fmac_f32_e32 v246, v110, v245
	v_fmac_f32_e32 v247, v111, v245
	v_fmac_f32_e32 v248, v112, v245
	v_fmac_f32_e32 v249, v113, v245
	v_and_or_b32 v194, v195, s29, v194
	v_bfe_u32 v195, v216, 16, 1
	v_bfe_u32 v196, v217, 16, 1
	v_fmac_f32_e32 v240, v124, v216
	v_fmac_f32_e32 v241, v125, v216
	v_fmac_f32_e32 v246, v138, v216
	v_fmac_f32_e32 v247, v139, v216
	v_fmac_f32_e32 v248, v140, v216
	v_fmac_f32_e32 v249, v141, v216
	v_pk_fma_f32 v[232:233], v[122:123], v[216:217], v[232:233] op_sel_hi:[1,0,1]
	v_add3_u32 v195, v216, v195, s31
	v_add3_u32 v196, v217, v196, s31
	v_fmac_f32_e32 v240, v116, v217
	v_fmac_f32_e32 v241, v117, v217
	v_fmac_f32_e32 v246, v118, v217
	v_fmac_f32_e32 v247, v119, v217
	v_fmac_f32_e32 v248, v120, v217
	v_fmac_f32_e32 v249, v121, v217
	v_pk_fma_f32 v[216:217], v[114:115], v[216:217], v[232:233] op_sel:[0,1,0]
	v_lshrrev_b32_e32 v195, 16, v195
	v_pk_fma_f32 v[216:217], v[126:127], v[218:219], v[216:217] op_sel_hi:[1,0,1]
	v_and_or_b32 v195, v196, s29, v195
	v_pk_fma_f32 v[216:217], v[134:135], v[218:219], v[216:217] op_sel:[0,1,0]
	v_bfe_u32 v196, v218, 16, 1
	v_pk_fma_f32 v[216:217], v[142:143], v[214:215], v[216:217] op_sel_hi:[1,0,1]
	v_bfe_u32 v197, v219, 16, 1
	v_pk_fma_f32 v[216:217], v[154:155], v[214:215], v[216:217] op_sel:[0,1,0]
	ds_bpermute_b32 v232, v220, v216
	ds_bpermute_b32 v233, v220, v217
	v_fmac_f32_e32 v240, v128, v218
	v_fmac_f32_e32 v241, v129, v218
	v_fmac_f32_e32 v246, v130, v218
	v_fmac_f32_e32 v247, v131, v218
	v_fmac_f32_e32 v248, v132, v218
	v_fmac_f32_e32 v249, v133, v218
	s_waitcnt lgkmcnt(0)
	v_pk_add_f32 v[216:217], v[216:217], v[232:233]
	v_add3_u32 v196, v218, v196, s31
	v_add3_u32 v197, v219, v197, s31
	v_fmac_f32_e32 v240, v136, v219
	v_fmac_f32_e32 v241, v137, v219
	v_fmac_f32_e32 v246, v146, v219
	v_fmac_f32_e32 v247, v147, v219
	v_fmac_f32_e32 v248, v148, v219
	v_fmac_f32_e32 v249, v149, v219
	ds_bpermute_b32 v218, v221, v216
	ds_bpermute_b32 v219, v221, v217
	v_lshrrev_b32_e32 v196, 16, v196
	v_fmac_f32_e32 v240, v144, v214
	v_and_or_b32 v196, v197, s29, v196
	v_bfe_u32 v197, v214, 16, 1
	s_waitcnt lgkmcnt(0)
	v_pk_add_f32 v[216:217], v[216:217], v[218:219]
	v_fmac_f32_e32 v240, v156, v215
	v_add3_u32 v197, v214, v197, s31
	v_fmac_f32_e32 v241, v145, v214
	v_fmac_f32_e32 v246, v150, v214
	v_fmac_f32_e32 v247, v151, v214
	v_fmac_f32_e32 v248, v152, v214
	v_fmac_f32_e32 v249, v153, v214
	ds_bpermute_b32 v218, v222, v216
	ds_bpermute_b32 v219, v222, v217
	ds_bpermute_b32 v214, v220, v240
	v_fmac_f32_e32 v241, v157, v215
	v_fmac_f32_e32 v246, v158, v215
	ds_bpermute_b32 v233, v220, v241
	s_waitcnt lgkmcnt(2)
	v_pk_add_f32 v[216:217], v[216:217], v[218:219]
	s_waitcnt lgkmcnt(1)
	v_add_f32_e32 v214, v240, v214
	ds_bpermute_b32 v218, v223, v216
	ds_bpermute_b32 v219, v223, v217
	ds_bpermute_b32 v232, v221, v214
	ds_bpermute_b32 v234, v220, v246
	v_fmac_f32_e32 v247, v159, v215
	v_fmac_f32_e32 v248, v160, v215
	s_waitcnt lgkmcnt(2)
	v_pk_add_f32 v[216:217], v[216:217], v[218:219]
	s_waitcnt lgkmcnt(1)
	v_add_f32_e32 v214, v214, v232
	ds_bpermute_b32 v218, v224, v216
	ds_bpermute_b32 v219, v224, v217
	ds_bpermute_b32 v232, v222, v214
	v_fmac_f32_e32 v249, v161, v215
	ds_bpermute_b32 v238, v220, v247
	ds_bpermute_b32 v239, v220, v249
	s_waitcnt lgkmcnt(3)
	v_pk_add_f32 v[216:217], v[216:217], v[218:219]
	v_add_f32_e32 v218, v241, v233
	s_waitcnt lgkmcnt(2)
	v_add_f32_e32 v214, v214, v232
	v_add_f32_e32 v232, v246, v234
	ds_bpermute_b32 v219, v221, v218
	ds_bpermute_b32 v233, v221, v232
	ds_bpermute_b32 v234, v223, v214
	s_waitcnt lgkmcnt(4)
	v_add_f32_e32 v238, v247, v238
	s_waitcnt lgkmcnt(3)
	v_add_f32_e32 v239, v249, v239
	s_waitcnt lgkmcnt(2)
	v_add_f32_e32 v219, v218, v219
	s_waitcnt lgkmcnt(1)
	v_add_f32_e32 v232, v232, v233
	ds_bpermute_b32 v235, v222, v219
	ds_bpermute_b32 v233, v222, v232
	s_waitcnt lgkmcnt(2)
	v_add_f32_e32 v214, v214, v234
	ds_bpermute_b32 v236, v224, v214
	ds_bpermute_b32 v240, v221, v238
	s_waitcnt lgkmcnt(3)
	v_add_f32_e32 v234, v219, v235
	s_waitcnt lgkmcnt(2)
	v_add_f32_e32 v232, v232, v233
	ds_bpermute_b32 v235, v223, v234
	ds_bpermute_b32 v233, v223, v232
	s_waitcnt lgkmcnt(3)
	v_add_f32_e32 v214, v214, v236
	ds_bpermute_b32 v242, v221, v239
	s_waitcnt lgkmcnt(3)
	v_add_f32_e32 v238, v238, v240
	s_waitcnt lgkmcnt(2)
	v_add_f32_e32 v234, v234, v235
	s_waitcnt lgkmcnt(1)
	v_add_f32_e32 v236, v232, v233
	ds_bpermute_b32 v235, v224, v234
	ds_bpermute_b32 v237, v224, v236
	s_waitcnt lgkmcnt(2)
	v_add_f32_e32 v239, v239, v242
	ds_bpermute_b32 v240, v222, v238
	ds_bpermute_b32 v242, v222, v239
	s_waitcnt lgkmcnt(3)
	v_add_f32_e32 v233, v234, v235
	s_waitcnt lgkmcnt(2)
	v_add_f32_e32 v235, v236, v237
	ds_bpermute_b32 v237, v220, v248
	s_waitcnt lgkmcnt(2)
	v_add_f32_e32 v238, v238, v240
	s_waitcnt lgkmcnt(1)
	v_add_f32_e32 v239, v239, v242
	ds_bpermute_b32 v240, v223, v238
	ds_bpermute_b32 v242, v223, v239
	s_waitcnt lgkmcnt(2)
	v_add_f32_e32 v237, v248, v237
	ds_bpermute_b32 v241, v221, v237
	ds_bpermute_b32 v218, v225, v216
	s_waitcnt lgkmcnt(3)
	v_add_f32_e32 v238, v238, v240
	s_waitcnt lgkmcnt(2)
	v_add_f32_e32 v242, v239, v242
	ds_bpermute_b32 v240, v224, v238
	s_waitcnt lgkmcnt(2)
	v_add_f32_e32 v237, v237, v241
	ds_bpermute_b32 v241, v222, v237
	ds_bpermute_b32 v244, v224, v242
	ds_bpermute_b32 v219, v225, v217
	ds_bpermute_b32 v232, v225, v214
	ds_bpermute_b32 v234, v225, v233
	s_waitcnt lgkmcnt(4)
	v_add_f32_e32 v237, v237, v241
	ds_bpermute_b32 v241, v223, v237
	ds_bpermute_b32 v236, v225, v235
	v_lshrrev_b32_e32 v197, 16, v197
	s_waitcnt lgkmcnt(1)
	v_add_f32_e32 v241, v237, v241
	ds_bpermute_b32 v243, v224, v241
	v_add_f32_e32 v237, v238, v240
	ds_bpermute_b32 v238, v225, v237
	s_waitcnt lgkmcnt(1)
	v_add_f32_e32 v239, v241, v243
	v_add_f32_e32 v241, v242, v244
	ds_bpermute_b32 v240, v225, v239
	ds_bpermute_b32 v242, v225, v241
	v_bfe_u32 v243, v215, 16, 1
	v_add3_u32 v215, v215, v243, s31
	v_and_or_b32 v197, v215, s29, v197
	global_store_dwordx4 v[212:213], v[194:197], off offset:1024
	s_and_saveexec_b64 s[24:25], s[2:3]
	s_cbranch_execz .LBB0_1235
	v_pk_add_f32 v[196:197], v[216:217], v[218:219]
	v_add_f32_e32 v214, v214, v232
	v_cmp_gt_f32_e32 vcc, v197, v196
	v_add_f32_e32 v233, v233, v234
	v_add_f32_e32 v235, v235, v236
	v_cndmask_b32_e32 v194, v196, v197, vcc
	v_cmp_gt_f32_e64 s[0:1], v214, v194
	s_waitcnt lgkmcnt(2)
	v_add_f32_e32 v237, v237, v238
	s_waitcnt lgkmcnt(1)
	v_add_f32_e32 v215, v239, v240
	v_cndmask_b32_e64 v194, v194, v214, s[0:1]
	v_cmp_gt_f32_e64 s[4:5], v233, v194
	s_waitcnt lgkmcnt(0)
	v_add_f32_e32 v195, v241, v242
	v_cmp_nlg_f32_e64 s[14:15], s34, v196
	v_cndmask_b32_e64 v194, v194, v233, s[4:5]
	v_cmp_gt_f32_e64 s[6:7], v235, v194
	s_nop 1
	v_cndmask_b32_e64 v194, v194, v235, s[6:7]
	v_cmp_gt_f32_e64 s[8:9], v237, v194
	s_nop 1
	v_cndmask_b32_e64 v194, v194, v237, s[8:9]
	v_cmp_gt_f32_e64 s[10:11], v215, v194
	s_nop 1
	v_cndmask_b32_e64 v216, v194, v215, s[10:11]
	v_cndmask_b32_e64 v194, 0, 1, vcc
	v_cndmask_b32_e64 v194, v194, 2, s[0:1]
	v_cndmask_b32_e64 v194, v194, 3, s[4:5]
	v_cndmask_b32_e64 v194, v194, 4, s[6:7]
	v_cndmask_b32_e64 v194, v194, 5, s[8:9]
	v_cndmask_b32_e64 v194, v194, 6, s[10:11]
	v_cmp_ngt_f32_e32 vcc, v195, v216
	s_and_b64 s[16:17], s[10:11], vcc
	s_nop 0
	v_cndmask_b32_e32 v194, 7, v194, vcc
	v_cmp_eq_u32_e64 s[12:13], 0, v194
	s_or_b64 s[12:13], s[12:13], s[14:15]
	v_cmp_ne_u32_e64 s[10:11], 1, v194
	v_cndmask_b32_e64 v196, v196, v231, s[12:13]
	v_cmp_gt_f32_e64 s[14:15], v197, v196
	s_and_b64 s[10:11], s[10:11], s[14:15]
	v_cndmask_b32_e64 v196, v196, v197, s[10:11]
	v_cmp_ne_u32_e64 s[8:9], 2, v194
	v_cmp_gt_f32_e64 s[14:15], v214, v196
	s_and_b64 s[8:9], s[8:9], s[14:15]
	v_cndmask_b32_e64 v196, v196, v214, s[8:9]
	v_cmp_ne_u32_e64 s[6:7], 3, v194
	v_cmp_gt_f32_e64 s[14:15], v233, v196
	s_and_b64 s[6:7], s[6:7], s[14:15]
	v_cndmask_b32_e64 v196, v196, v233, s[6:7]
	v_cmp_ne_u32_e64 s[4:5], 4, v194
	v_cmp_gt_f32_e64 s[14:15], v235, v196
	s_and_b64 s[4:5], s[4:5], s[14:15]
	v_cndmask_b32_e64 v196, v196, v235, s[4:5]
	v_cmp_ne_u32_e64 s[0:1], 5, v194
	v_cmp_gt_f32_e64 s[14:15], v237, v196
	s_and_b64 s[0:1], s[0:1], s[14:15]
	v_cndmask_b32_e64 v196, v196, v237, s[0:1]
	v_cmp_ngt_f32_e64 s[14:15], v215, v196
	s_or_b64 s[14:15], s[16:17], s[14:15]
	v_cndmask_b32_e64 v197, 0, -1, s[12:13]
	v_cndmask_b32_e64 v196, v215, v196, s[14:15]
	v_cmp_gt_f32_e64 s[16:17], v195, v196
	s_and_b64 s[16:17], vcc, s[16:17]
	v_cndmask_b32_e64 v197, v197, 1, s[10:11]
	v_cndmask_b32_e64 v196, v196, v195, s[16:17]
	v_cndmask_b32_e32 v195, v195, v216, vcc
	v_sub_f32_e32 v195, v196, v195
	v_mul_f32_e32 v195, 0x3fb8aa3b, v195
	v_exp_f32_e32 v215, v195
	v_cndmask_b32_e64 v195, v197, 2, s[8:9]
	v_cndmask_b32_e64 v195, v195, 3, s[6:7]
	v_cndmask_b32_e64 v195, v195, 4, s[4:5]
	v_add_f32_e32 v214, 1.0, v215
	v_div_scale_f32 v196, s[4:5], v214, v214, 1.0
	v_rcp_f32_e32 v216, v196
	v_cndmask_b32_e64 v195, v195, 5, s[0:1]
	v_cndmask_b32_e64 v195, 6, v195, s[14:15]
	v_cndmask_b32_e64 v195, v195, 7, s[16:17]
	v_fma_f32 v197, -v196, v216, 1.0
	v_fmac_f32_e32 v216, v197, v216
	v_div_scale_f32 v197, vcc, 1.0, v214, 1.0
	v_mul_f32_e32 v217, v197, v216
	v_fma_f32 v218, -v196, v217, v197
	v_fmac_f32_e32 v217, v218, v216
	v_fma_f32 v218, -v196, v217, v197
	v_lshl_add_u32 v196, v194, 2, 0
	ds_add_rtn_u32 v196, v196, v230
	v_lshl_add_u32 v197, v195, 2, 0
	ds_add_rtn_u32 v197, v197, v230
	v_div_fmas_f32 v216, v218, v216, v217
	v_div_fixup_f32 v214, v216, v214, 1.0
	v_mul_f32_e32 v215, v215, v214
	s_waitcnt lgkmcnt(0)
	ds_write_b128 v226, v[194:197]
	v_lshl_add_u64 v[194:195], s[94:95], 0, v[206:207]
	v_add_co_u32_e32 v194, vcc, 0x280000, v194
	s_nop 1
	v_addc_co_u32_e32 v195, vcc, 0, v195, vcc
	global_store_dwordx2 v[194:195], v[214:215], off

.LBB0_1237:
	s_waitcnt vmcnt(7)
	v_lshlrev_b32_e32 v217, 16, v171
	v_lshlrev_b32_e32 v216, 16, v170
	v_and_b32_e32 v237, 0xffff0000, v171
	v_and_b32_e32 v236, 0xffff0000, v170
	s_waitcnt lgkmcnt(2)
	v_pk_add_f32 v[238:239], v[216:217], v[236:237]
	v_and_b32_e32 v241, 0xffff0000, v173
	v_add_f32_e32 v215, v238, v239
	v_lshlrev_b32_e32 v239, 16, v173
	v_lshlrev_b32_e32 v238, 16, v172
	s_waitcnt lgkmcnt(1)
	v_and_b32_e32 v240, 0xffff0000, v172
	s_waitcnt lgkmcnt(0)
	v_pk_add_f32 v[242:243], v[238:239], v[240:241]
	s_waitcnt vmcnt(6)
	v_lshlrev_b32_e32 v194, 16, v174
	v_and_b32_e32 v195, 0xffff0000, v174
	v_lshlrev_b32_e32 v196, 16, v175
	v_and_b32_e32 v197, 0xffff0000, v175
	v_pk_add_f32 v[242:243], v[242:243], v[242:243] op_sel_hi:[0,1]
	v_lshlrev_b32_e32 v214, 16, v176
	v_and_b32_e32 v218, 0xffff0000, v176
	v_lshlrev_b32_e32 v232, 16, v177
	v_and_b32_e32 v234, 0xffff0000, v177
	v_add_f32_e32 v235, 0, v215
	v_add_f32_e32 v215, v194, v195
	v_add_f32_e32 v219, v196, v197
	v_mov_b32_e32 v233, v243
	v_pk_add_f32 v[244:245], v[214:215], v[218:219]
	v_pk_add_f32 v[242:243], v[232:233], v[234:235]
	s_nop 0
	v_pk_add_f32 v[242:243], v[244:245], v[242:243]
	s_nop 0
	v_add_f32_e32 v215, v242, v243
	s_waitcnt lgkmcnt(0)
	s_nop 1
	v_add_f32_dpp v215, v215, v215 quad_perm:[1,0,3,2] row_mask:0xf bank_mask:0xf
	s_nop 1
	v_add_f32_dpp v215, v215, v215 quad_perm:[2,3,0,1] row_mask:0xf bank_mask:0xf
	s_nop 1
	v_add_f32_dpp v215, v215, v215 row_half_mirror row_mask:0xf bank_mask:0xf
	s_nop 1
	v_add_f32_dpp v215, v215, v215 row_mirror row_mask:0xf bank_mask:0xf
	v_mov_b32_e32 v219, v215
	s_nop 1
	v_permlane16_swap_b32_e32 v215, v219
	v_add_f32_e32 v215, v215, v219
	v_mov_b32_e32 v219, v215
	s_nop 1
	v_permlane32_swap_b32_e32 v215, v219
	v_add_f32_e32 v215, v215, v219
	v_fmac_f32_e32 v236, 0xba800000, v215
	v_fmac_f32_e32 v237, 0xba800000, v215
	v_fmac_f32_e32 v217, 0xba800000, v215
	v_fmac_f32_e32 v216, 0xba800000, v215
	v_mov_b32_e32 v242, v217
	v_mov_b32_e32 v243, v237
	v_mov_b32_e32 v217, v236
	v_pk_mul_f32 v[244:245], v[242:243], v[242:243]
	v_pk_mul_f32 v[236:237], v[216:217], v[216:217]
	v_fmac_f32_e32 v240, 0xba800000, v215
	v_pk_mov_b32 v[246:247], v[236:237], v[244:245] op_sel:[1,0]
	v_mov_b32_e32 v237, v245
	v_fmac_f32_e32 v241, 0xba800000, v215
	v_fmac_f32_e32 v239, 0xba800000, v215
	v_pk_add_f32 v[236:237], v[246:247], v[236:237]
	v_fmac_f32_e32 v238, 0xba800000, v215
	v_mov_b32_e32 v244, v239
	v_mov_b32_e32 v245, v241
	v_mov_b32_e32 v239, v240
	v_pk_add_f32 v[236:237], v[236:237], v[236:237] op_sel_hi:[0,1]
	v_pk_mul_f32 v[246:247], v[244:245], v[244:245]
	v_pk_mul_f32 v[240:241], v[238:239], v[238:239]
	v_fmac_f32_e32 v194, 0xba800000, v215
	v_pk_mov_b32 v[248:249], v[240:241], v[246:247] op_sel:[1,0]
	v_mov_b32_e32 v241, v247
	v_fmac_f32_e32 v195, 0xba800000, v215
	v_fmac_f32_e32 v196, 0xba800000, v215
	v_mul_f32_e32 v236, v194, v194
	v_pk_add_f32 v[240:241], v[248:249], v[240:241]
	v_fmac_f32_e32 v197, 0xba800000, v215
	v_pk_fma_f32 v[246:247], v[194:195], v[194:195], v[236:237] op_sel_hi:[1,1,0]
	v_mul_f32_e32 v236, v196, v196
	v_pk_add_f32 v[240:241], v[240:241], v[240:241] op_sel_hi:[0,1]
	v_pk_fma_f32 v[248:249], v[196:197], v[196:197], v[236:237] op_sel_hi:[1,1,0]
	v_fmac_f32_e32 v234, 0xba800000, v215
	v_fmac_f32_e32 v232, 0xba800000, v215
	v_fmac_f32_e32 v218, 0xba800000, v215
	v_fmac_f32_e32 v214, 0xba800000, v215
	v_mul_f32_e32 v246, v214, v214
	v_mul_f32_e32 v248, v218, v218
	v_mul_f32_e32 v236, v232, v232
	v_mul_f32_e32 v240, v234, v234
	v_pk_add_f32 v[246:247], v[246:247], v[248:249]
	v_pk_add_f32 v[236:237], v[236:237], v[240:241]
	s_nop 0
	v_pk_add_f32 v[236:237], v[246:247], v[236:237]
	s_nop 0
	v_add_f32_e32 v215, v236, v237
	s_waitcnt lgkmcnt(0)
	s_nop 1
	v_add_f32_dpp v215, v215, v215 quad_perm:[1,0,3,2] row_mask:0xf bank_mask:0xf
	s_nop 1
	v_add_f32_dpp v215, v215, v215 quad_perm:[2,3,0,1] row_mask:0xf bank_mask:0xf
	s_nop 1
	v_add_f32_dpp v215, v215, v215 row_half_mirror row_mask:0xf bank_mask:0xf
	s_nop 1
	v_add_f32_dpp v215, v215, v215 row_mirror row_mask:0xf bank_mask:0xf
	v_mov_b32_e32 v219, v215
	s_nop 1
	v_permlane16_swap_b32_e32 v215, v219
	v_add_f32_e32 v215, v215, v219
	v_mov_b32_e32 v219, v215
	s_nop 1
	v_permlane32_swap_b32_e32 v215, v219
	v_add_f32_e32 v215, v215, v219
	v_fmamk_f32 v215, v215, 0x3a800000, v228
	v_mul_f32_e32 v219, 0x4f800000, v215
	v_cmp_gt_f32_e32 vcc, s30, v215
	s_nop 1
	v_cndmask_b32_e32 v215, v215, v219, vcc
	v_sqrt_f32_e32 v219, v215
	s_nop 0
	v_add_u32_e32 v233, -1, v219
	v_fma_f32 v235, -v233, v219, v215
	v_cmp_ge_f32_e64 s[0:1], 0, v235
	v_add_u32_e32 v235, 1, v219
	s_nop 0
	v_cndmask_b32_e64 v233, v219, v233, s[0:1]
	v_fma_f32 v219, -v235, v219, v215
	v_cmp_lt_f32_e64 s[0:1], 0, v219
	s_nop 1
	v_cndmask_b32_e64 v219, v233, v235, s[0:1]
	v_mul_f32_e32 v233, 0x37800000, v219
	v_cndmask_b32_e32 v219, v219, v233, vcc
	v_cmp_class_f32_e32 vcc, v215, v229
	s_nop 1
	v_cndmask_b32_e32 v215, v219, v215, vcc
	v_div_scale_f32 v219, s[0:1], v215, v215, 1.0
	v_rcp_f32_e32 v233, v219
	s_nop 0
	v_fma_f32 v235, -v219, v233, 1.0
	v_fmac_f32_e32 v233, v235, v233
	v_div_scale_f32 v235, vcc, 1.0, v215, 1.0
	v_mul_f32_e32 v236, v235, v233
	v_fma_f32 v237, -v219, v236, v235
	v_fmac_f32_e32 v236, v237, v233
	v_fma_f32 v219, -v219, v236, v235
	v_div_fmas_f32 v219, v219, v233, v236
	v_div_fixup_f32 v236, v219, v215, 1.0
	v_pk_mul_f32 v[216:217], v[216:217], v[236:237] op_sel_hi:[1,0]
	v_pk_mul_f32 v[194:195], v[194:195], v[236:237] op_sel_hi:[1,0]
	v_mov_b32_e32 v215, v218
	v_pk_mul_f32 v[240:241], v[242:243], v[236:237] op_sel_hi:[1,0]
	v_pk_fma_f32 v[242:243], v[2:3], v[216:217], v[6:7]
	v_pk_fma_f32 v[246:247], v[18:19], v[194:195], v[30:31]
	v_pk_mul_f32 v[194:195], v[214:215], v[236:237] op_sel_hi:[1,0]
	v_pk_fma_f32 v[240:241], v[4:5], v[240:241], v[8:9]
	v_pk_fma_f32 v[218:219], v[10:11], v[194:195], v[22:23]
	v_bfe_u32 v194, v242, 16, 1
	v_add3_u32 v194, v242, v194, s31
	v_bfe_u32 v195, v243, 16, 1
	v_pk_mul_f32 v[216:217], v[238:239], v[236:237] op_sel_hi:[1,0]
	v_pk_mul_f32 v[196:197], v[196:197], v[236:237] op_sel_hi:[1,0]
	v_mov_b32_e32 v233, v234
	v_lshrrev_b32_e32 v194, 16, v194
	v_add3_u32 v195, v243, v195, s31
	v_pk_mul_f32 v[238:239], v[244:245], v[236:237] op_sel_hi:[1,0]
	v_pk_fma_f32 v[244:245], v[14:15], v[216:217], v[26:27]
	v_pk_fma_f32 v[216:217], v[20:21], v[196:197], v[32:33]
	v_pk_mul_f32 v[196:197], v[232:233], v[236:237] op_sel_hi:[1,0]
	v_and_or_b32 v194, v195, s29, v194
	v_bfe_u32 v195, v240, 16, 1
	v_pk_fma_f32 v[214:215], v[12:13], v[196:197], v[24:25]
	v_add3_u32 v195, v240, v195, s31
	v_bfe_u32 v196, v241, 16, 1
	v_lshrrev_b32_e32 v195, 16, v195
	v_add3_u32 v196, v241, v196, s31
	v_and_or_b32 v195, v196, s29, v195
	v_bfe_u32 v196, v244, 16, 1
	v_add3_u32 v196, v244, v196, s31
	v_bfe_u32 v197, v245, 16, 1
	v_pk_fma_f32 v[238:239], v[16:17], v[238:239], v[28:29]
	v_lshrrev_b32_e32 v196, 16, v196
	v_add3_u32 v197, v245, v197, s31
	v_and_or_b32 v196, v197, s29, v196
	v_bfe_u32 v197, v238, 16, 1
	v_add3_u32 v197, v238, v197, s31
	v_bfe_u32 v232, v239, 16, 1
	v_lshrrev_b32_e32 v197, 16, v197
	v_add3_u32 v232, v239, v232, s31
	v_and_or_b32 v197, v232, s29, v197
	v_fma_f32 v234, v36, v242, 0
	v_fma_f32 v235, v37, v242, 0
	v_fma_f32 v236, v38, v242, 0
	v_fma_f32 v237, v39, v242, 0
	v_fma_f32 v248, v40, v242, 0
	v_fma_f32 v249, v41, v242, 0
	v_pk_fma_f32 v[232:233], v[34:35], v[242:243], 0 op_sel_hi:[1,0,0]
	v_fmac_f32_e32 v234, v44, v243
	v_fmac_f32_e32 v235, v45, v243
	v_fmac_f32_e32 v236, v46, v243
	v_fmac_f32_e32 v237, v47, v243
	v_fmac_f32_e32 v248, v48, v243
	v_fmac_f32_e32 v249, v49, v243
	v_pk_fma_f32 v[232:233], v[42:43], v[242:243], v[232:233] op_sel:[0,1,0]
	v_fmac_f32_e32 v234, v52, v240
	v_fmac_f32_e32 v235, v53, v240
	v_fmac_f32_e32 v236, v54, v240
	v_fmac_f32_e32 v237, v55, v240
	v_fmac_f32_e32 v248, v56, v240
	v_fmac_f32_e32 v249, v57, v240
	v_pk_fma_f32 v[232:233], v[50:51], v[240:241], v[232:233] op_sel_hi:[1,0,1]
	v_fmac_f32_e32 v234, v60, v241
	v_fmac_f32_e32 v235, v61, v241
	v_fmac_f32_e32 v236, v62, v241
	v_fmac_f32_e32 v237, v63, v241
	v_fmac_f32_e32 v248, v64, v241
	v_fmac_f32_e32 v249, v65, v241
	v_pk_fma_f32 v[232:233], v[58:59], v[240:241], v[232:233] op_sel:[0,1,0]
	v_fmac_f32_e32 v234, v68, v244
	v_fmac_f32_e32 v235, v69, v244
	v_fmac_f32_e32 v236, v70, v244
	v_fmac_f32_e32 v237, v71, v244
	v_fmac_f32_e32 v248, v72, v244
	v_fmac_f32_e32 v249, v73, v244
	v_pk_fma_f32 v[232:233], v[66:67], v[244:245], v[232:233] op_sel_hi:[1,0,1]
	v_fmac_f32_e32 v234, v76, v245
	v_fmac_f32_e32 v235, v77, v245
	v_fmac_f32_e32 v236, v78, v245
	v_fmac_f32_e32 v237, v79, v245
	v_fmac_f32_e32 v248, v80, v245
	v_fmac_f32_e32 v249, v81, v245
	v_pk_fma_f32 v[232:233], v[74:75], v[244:245], v[232:233] op_sel:[0,1,0]
	v_fmac_f32_e32 v234, v84, v238
	v_fmac_f32_e32 v235, v85, v238
	v_fmac_f32_e32 v236, v86, v238
	v_fmac_f32_e32 v237, v87, v238
	v_fmac_f32_e32 v248, v88, v238
	v_fmac_f32_e32 v249, v89, v238
	v_pk_fma_f32 v[232:233], v[82:83], v[238:239], v[232:233] op_sel_hi:[1,0,1]
	global_store_dwordx4 v[212:213], v[194:197], off offset:2048
	v_fmac_f32_e32 v234, v92, v239
	v_fmac_f32_e32 v235, v93, v239
	v_bfe_u32 v194, v246, 16, 1
	v_fmac_f32_e32 v236, v94, v239
	v_fmac_f32_e32 v237, v95, v239
	v_fmac_f32_e32 v248, v96, v239
	v_fmac_f32_e32 v249, v97, v239
	v_pk_fma_f32 v[232:233], v[90:91], v[238:239], v[232:233] op_sel:[0,1,0]
	v_add3_u32 v194, v246, v194, s31
	v_bfe_u32 v195, v247, 16, 1
	v_fmac_f32_e32 v234, v108, v246
	v_fmac_f32_e32 v235, v109, v246
	v_fmac_f32_e32 v236, v98, v246
	v_fmac_f32_e32 v237, v99, v246
	v_fmac_f32_e32 v248, v100, v246
	v_fmac_f32_e32 v249, v101, v246
	v_pk_fma_f32 v[232:233], v[106:107], v[246:247], v[232:233] op_sel_hi:[1,0,1]
	v_lshrrev_b32_e32 v194, 16, v194
	v_add3_u32 v195, v247, v195, s31
	v_pk_fma_f32 v[232:233], v[102:103], v[246:247], v[232:233] op_sel:[0,1,0]
	v_fmac_f32_e32 v234, v104, v247
	v_fmac_f32_e32 v235, v105, v247
	v_fmac_f32_e32 v236, v110, v247
	v_fmac_f32_e32 v237, v111, v247
	v_fmac_f32_e32 v248, v112, v247
	v_fmac_f32_e32 v249, v113, v247
	v_and_or_b32 v194, v195, s29, v194
	v_bfe_u32 v195, v216, 16, 1
	v_bfe_u32 v196, v217, 16, 1
	v_fmac_f32_e32 v234, v124, v216
	v_fmac_f32_e32 v235, v125, v216
	v_fmac_f32_e32 v236, v138, v216
	v_fmac_f32_e32 v237, v139, v216
	v_fmac_f32_e32 v248, v140, v216
	v_fmac_f32_e32 v249, v141, v216
	v_pk_fma_f32 v[232:233], v[122:123], v[216:217], v[232:233] op_sel_hi:[1,0,1]
	v_add3_u32 v195, v216, v195, s31
	v_add3_u32 v196, v217, v196, s31
	v_fmac_f32_e32 v234, v116, v217
	v_fmac_f32_e32 v235, v117, v217
	v_fmac_f32_e32 v236, v118, v217
	v_fmac_f32_e32 v237, v119, v217
	v_fmac_f32_e32 v248, v120, v217
	v_fmac_f32_e32 v249, v121, v217
	v_pk_fma_f32 v[216:217], v[114:115], v[216:217], v[232:233] op_sel:[0,1,0]
	v_lshrrev_b32_e32 v195, 16, v195
	v_pk_fma_f32 v[216:217], v[126:127], v[218:219], v[216:217] op_sel_hi:[1,0,1]
	v_and_or_b32 v195, v196, s29, v195
	v_pk_fma_f32 v[216:217], v[134:135], v[218:219], v[216:217] op_sel:[0,1,0]
	v_bfe_u32 v196, v218, 16, 1
	v_pk_fma_f32 v[216:217], v[142:143], v[214:215], v[216:217] op_sel_hi:[1,0,1]
	v_bfe_u32 v197, v219, 16, 1
	v_pk_fma_f32 v[216:217], v[154:155], v[214:215], v[216:217] op_sel:[0,1,0]
	ds_bpermute_b32 v232, v220, v216
	ds_bpermute_b32 v233, v220, v217
	v_fmac_f32_e32 v234, v128, v218
	v_fmac_f32_e32 v235, v129, v218
	v_fmac_f32_e32 v236, v130, v218
	v_fmac_f32_e32 v237, v131, v218
	v_fmac_f32_e32 v248, v132, v218
	v_fmac_f32_e32 v249, v133, v218
	s_waitcnt lgkmcnt(0)
	v_pk_add_f32 v[216:217], v[216:217], v[232:233]
	v_add3_u32 v196, v218, v196, s31
	v_add3_u32 v197, v219, v197, s31
	v_fmac_f32_e32 v234, v136, v219
	v_fmac_f32_e32 v235, v137, v219
	v_fmac_f32_e32 v236, v146, v219
	v_fmac_f32_e32 v237, v147, v219
	v_fmac_f32_e32 v248, v148, v219
	v_fmac_f32_e32 v249, v149, v219
	ds_bpermute_b32 v218, v221, v216
	ds_bpermute_b32 v219, v221, v217
	v_lshrrev_b32_e32 v196, 16, v196
	v_fmac_f32_e32 v234, v144, v214
	v_and_or_b32 v196, v197, s29, v196
	v_bfe_u32 v197, v214, 16, 1
	s_waitcnt lgkmcnt(0)
	v_pk_add_f32 v[216:217], v[216:217], v[218:219]
	v_fmac_f32_e32 v234, v156, v215
	v_add3_u32 v197, v214, v197, s31
	v_fmac_f32_e32 v235, v145, v214
	v_fmac_f32_e32 v236, v150, v214
	v_fmac_f32_e32 v237, v151, v214
	v_fmac_f32_e32 v248, v152, v214
	v_fmac_f32_e32 v249, v153, v214
	ds_bpermute_b32 v218, v222, v216
	ds_bpermute_b32 v219, v222, v217
	ds_bpermute_b32 v214, v220, v234
	v_fmac_f32_e32 v235, v157, v215
	v_fmac_f32_e32 v236, v158, v215
	ds_bpermute_b32 v233, v220, v235
	s_waitcnt lgkmcnt(2)
	v_pk_add_f32 v[216:217], v[216:217], v[218:219]
	s_waitcnt lgkmcnt(1)
	v_add_f32_e32 v214, v234, v214
	ds_bpermute_b32 v218, v223, v216
	ds_bpermute_b32 v219, v223, v217
	ds_bpermute_b32 v232, v221, v214
	ds_bpermute_b32 v234, v220, v236
	v_fmac_f32_e32 v237, v159, v215
	v_fmac_f32_e32 v248, v160, v215
	s_waitcnt lgkmcnt(2)
	v_pk_add_f32 v[216:217], v[216:217], v[218:219]
	s_waitcnt lgkmcnt(1)
	v_add_f32_e32 v214, v214, v232
	ds_bpermute_b32 v218, v224, v216
	ds_bpermute_b32 v219, v224, v217
	ds_bpermute_b32 v232, v222, v214
	v_fmac_f32_e32 v249, v161, v215
	ds_bpermute_b32 v239, v220, v237
	ds_bpermute_b32 v240, v220, v249
	s_waitcnt lgkmcnt(3)
	v_pk_add_f32 v[216:217], v[216:217], v[218:219]
	v_add_f32_e32 v218, v235, v233
	s_waitcnt lgkmcnt(2)
	v_add_f32_e32 v214, v214, v232
	v_add_f32_e32 v232, v236, v234
	ds_bpermute_b32 v219, v221, v218
	ds_bpermute_b32 v233, v221, v232
	ds_bpermute_b32 v234, v223, v214
	s_waitcnt lgkmcnt(4)
	v_add_f32_e32 v237, v237, v239
	s_waitcnt lgkmcnt(3)
	v_add_f32_e32 v240, v249, v240
	s_waitcnt lgkmcnt(2)
	v_add_f32_e32 v219, v218, v219
	s_waitcnt lgkmcnt(1)
	v_add_f32_e32 v232, v232, v233
	ds_bpermute_b32 v235, v222, v219
	ds_bpermute_b32 v233, v222, v232
	s_waitcnt lgkmcnt(2)
	v_add_f32_e32 v214, v214, v234
	ds_bpermute_b32 v236, v224, v214
	ds_bpermute_b32 v239, v221, v237
	s_waitcnt lgkmcnt(3)
	v_add_f32_e32 v234, v219, v235
	s_waitcnt lgkmcnt(2)
	v_add_f32_e32 v232, v232, v233
	ds_bpermute_b32 v235, v223, v234
	ds_bpermute_b32 v233, v223, v232
	s_waitcnt lgkmcnt(3)
	v_add_f32_e32 v214, v214, v236
	ds_bpermute_b32 v242, v221, v240
	s_waitcnt lgkmcnt(3)
	v_add_f32_e32 v237, v237, v239
	s_waitcnt lgkmcnt(2)
	v_add_f32_e32 v234, v234, v235
	s_waitcnt lgkmcnt(1)
	v_add_f32_e32 v236, v232, v233
	ds_bpermute_b32 v235, v224, v234
	ds_bpermute_b32 v238, v224, v236
	s_waitcnt lgkmcnt(2)
	v_add_f32_e32 v240, v240, v242
	ds_bpermute_b32 v239, v222, v237
	ds_bpermute_b32 v242, v222, v240
	s_waitcnt lgkmcnt(3)
	v_add_f32_e32 v233, v234, v235
	s_waitcnt lgkmcnt(2)
	v_add_f32_e32 v235, v236, v238
	ds_bpermute_b32 v238, v220, v248
	s_waitcnt lgkmcnt(2)
	v_add_f32_e32 v237, v237, v239
	s_waitcnt lgkmcnt(1)
	v_add_f32_e32 v240, v240, v242
	ds_bpermute_b32 v239, v223, v237
	ds_bpermute_b32 v242, v223, v240
	s_waitcnt lgkmcnt(2)
	v_add_f32_e32 v238, v248, v238
	ds_bpermute_b32 v241, v221, v238
	ds_bpermute_b32 v218, v225, v216
	s_waitcnt lgkmcnt(3)
	v_add_f32_e32 v237, v237, v239
	s_waitcnt lgkmcnt(2)
	v_add_f32_e32 v242, v240, v242
	ds_bpermute_b32 v239, v224, v237
	s_waitcnt lgkmcnt(2)
	v_add_f32_e32 v238, v238, v241
	ds_bpermute_b32 v241, v222, v238
	ds_bpermute_b32 v244, v224, v242
	ds_bpermute_b32 v219, v225, v217
	s_waitcnt lgkmcnt(3)
	v_add_f32_e32 v237, v237, v239
	ds_bpermute_b32 v232, v225, v214
	s_waitcnt lgkmcnt(3)
	v_add_f32_e32 v238, v238, v241
	ds_bpermute_b32 v241, v223, v238
	ds_bpermute_b32 v234, v225, v233
	ds_bpermute_b32 v236, v225, v235
	v_lshrrev_b32_e32 v197, 16, v197
	s_waitcnt lgkmcnt(2)
	v_add_f32_e32 v241, v238, v241
	ds_bpermute_b32 v243, v224, v241
	ds_bpermute_b32 v238, v225, v237
	s_waitcnt lgkmcnt(1)
	v_add_f32_e32 v239, v241, v243
	v_add_f32_e32 v241, v242, v244
	ds_bpermute_b32 v240, v225, v239
	ds_bpermute_b32 v242, v225, v241
	v_bfe_u32 v243, v215, 16, 1
	v_add3_u32 v215, v215, v243, s31
	v_and_or_b32 v197, v215, s29, v197
	global_store_dwordx4 v[212:213], v[194:197], off offset:3072
	s_and_saveexec_b64 s[24:25], s[2:3]
	s_cbranch_execz .LBB0_1239
	v_pk_add_f32 v[196:197], v[216:217], v[218:219]
	v_add_f32_e32 v214, v214, v232
	v_cmp_gt_f32_e32 vcc, v197, v196
	v_add_f32_e32 v233, v233, v234
	v_add_f32_e32 v215, v235, v236
	v_cndmask_b32_e32 v194, v196, v197, vcc
	v_cmp_gt_f32_e64 s[0:1], v214, v194
	s_waitcnt lgkmcnt(2)
	v_add_f32_e32 v213, v237, v238
	s_waitcnt lgkmcnt(1)
	v_add_f32_e32 v212, v239, v240
	v_cndmask_b32_e64 v194, v194, v214, s[0:1]
	v_cmp_gt_f32_e64 s[4:5], v233, v194
	s_waitcnt lgkmcnt(0)
	v_add_f32_e32 v195, v241, v242
	v_cmp_nlg_f32_e64 s[14:15], s34, v196
	v_cndmask_b32_e64 v194, v194, v233, s[4:5]
	v_cmp_gt_f32_e64 s[6:7], v215, v194
	s_nop 1
	v_cndmask_b32_e64 v194, v194, v215, s[6:7]
	v_cmp_gt_f32_e64 s[8:9], v213, v194
	s_nop 1
	v_cndmask_b32_e64 v194, v194, v213, s[8:9]
	v_cmp_gt_f32_e64 s[10:11], v212, v194
	s_nop 1
	v_cndmask_b32_e64 v216, v194, v212, s[10:11]
	v_cndmask_b32_e64 v194, 0, 1, vcc
	v_cndmask_b32_e64 v194, v194, 2, s[0:1]
	v_cndmask_b32_e64 v194, v194, 3, s[4:5]
	v_cndmask_b32_e64 v194, v194, 4, s[6:7]
	v_cndmask_b32_e64 v194, v194, 5, s[8:9]
	v_cndmask_b32_e64 v194, v194, 6, s[10:11]
	v_cmp_ngt_f32_e32 vcc, v195, v216
	s_and_b64 s[16:17], s[10:11], vcc
	s_nop 0
	v_cndmask_b32_e32 v194, 7, v194, vcc
	v_cmp_eq_u32_e64 s[12:13], 0, v194
	s_or_b64 s[12:13], s[12:13], s[14:15]
	v_cmp_ne_u32_e64 s[10:11], 1, v194
	v_cndmask_b32_e64 v196, v196, v231, s[12:13]
	v_cmp_gt_f32_e64 s[14:15], v197, v196
	s_and_b64 s[10:11], s[10:11], s[14:15]
	v_cndmask_b32_e64 v196, v196, v197, s[10:11]
	v_cmp_ne_u32_e64 s[8:9], 2, v194
	v_cmp_gt_f32_e64 s[14:15], v214, v196
	s_and_b64 s[8:9], s[8:9], s[14:15]
	v_cndmask_b32_e64 v196, v196, v214, s[8:9]
	v_cmp_ne_u32_e64 s[6:7], 3, v194
	v_cmp_gt_f32_e64 s[14:15], v233, v196
	s_and_b64 s[6:7], s[6:7], s[14:15]
	v_cndmask_b32_e64 v196, v196, v233, s[6:7]
	v_cmp_ne_u32_e64 s[4:5], 4, v194
	v_cmp_gt_f32_e64 s[14:15], v215, v196
	s_and_b64 s[4:5], s[4:5], s[14:15]
	v_cndmask_b32_e64 v196, v196, v215, s[4:5]
	v_cmp_ne_u32_e64 s[0:1], 5, v194
	v_cmp_gt_f32_e64 s[14:15], v213, v196
	s_and_b64 s[0:1], s[0:1], s[14:15]
	v_cndmask_b32_e64 v196, v196, v213, s[0:1]
	v_cmp_ngt_f32_e64 s[14:15], v212, v196
	s_or_b64 s[14:15], s[16:17], s[14:15]
	v_cndmask_b32_e64 v197, 0, -1, s[12:13]
	v_cndmask_b32_e64 v196, v212, v196, s[14:15]
	v_cmp_gt_f32_e64 s[16:17], v195, v196
	s_and_b64 s[16:17], vcc, s[16:17]
	v_cndmask_b32_e64 v197, v197, 1, s[10:11]
	v_cndmask_b32_e64 v196, v196, v195, s[16:17]
	v_cndmask_b32_e32 v195, v195, v216, vcc
	v_sub_f32_e32 v195, v196, v195
	v_mul_f32_e32 v195, 0x3fb8aa3b, v195
	v_exp_f32_e32 v213, v195
	v_cndmask_b32_e64 v195, v197, 2, s[8:9]
	v_cndmask_b32_e64 v195, v195, 3, s[6:7]
	v_cndmask_b32_e64 v195, v195, 4, s[4:5]
	v_add_f32_e32 v212, 1.0, v213
	v_div_scale_f32 v196, s[4:5], v212, v212, 1.0
	v_rcp_f32_e32 v214, v196
	v_cndmask_b32_e64 v195, v195, 5, s[0:1]
	v_cndmask_b32_e64 v195, 6, v195, s[14:15]
	v_cndmask_b32_e64 v195, v195, 7, s[16:17]
	v_fma_f32 v197, -v196, v214, 1.0
	v_fmac_f32_e32 v214, v197, v214
	v_div_scale_f32 v197, vcc, 1.0, v212, 1.0
	v_mul_f32_e32 v215, v197, v214
	v_fma_f32 v216, -v196, v215, v197
	v_fmac_f32_e32 v215, v216, v214
	v_fma_f32 v216, -v196, v215, v197
	v_lshl_add_u32 v196, v194, 2, 0
	ds_add_rtn_u32 v196, v196, v230
	v_lshl_add_u32 v197, v195, 2, 0
	ds_add_rtn_u32 v197, v197, v230
	v_div_fmas_f32 v214, v216, v214, v215
	v_div_fixup_f32 v212, v214, v212, 1.0
	v_mul_f32_e32 v213, v213, v212
	s_waitcnt lgkmcnt(0)
	ds_write_b128 v226, v[194:197] offset:16
	v_add_u32_e32 v194, 2, v227
	v_ashrrev_i32_e32 v195, 31, v194
	v_lshl_add_u64 v[194:195], v[194:195], 2, s[36:37]
	global_store_dwordx2 v[194:195], v[212:213], off

.LBB0_1241:
	s_waitcnt vmcnt(7)
	v_lshlrev_b32_e32 v217, 16, v179
	v_lshlrev_b32_e32 v216, 16, v178
	v_and_b32_e32 v235, 0xffff0000, v179
	v_and_b32_e32 v234, 0xffff0000, v178
	v_pk_add_f32 v[236:237], v[216:217], v[234:235]
	v_and_b32_e32 v239, 0xffff0000, v181
	v_add_f32_e32 v213, v236, v237
	v_lshlrev_b32_e32 v237, 16, v181
	v_lshlrev_b32_e32 v236, 16, v180
	s_waitcnt lgkmcnt(2)
	v_and_b32_e32 v238, 0xffff0000, v180
	s_waitcnt lgkmcnt(1)
	v_pk_add_f32 v[240:241], v[236:237], v[238:239]
	s_waitcnt vmcnt(6)
	v_lshlrev_b32_e32 v194, 16, v182
	v_and_b32_e32 v195, 0xffff0000, v182
	v_lshlrev_b32_e32 v196, 16, v183
	v_and_b32_e32 v197, 0xffff0000, v183
	v_pk_add_f32 v[240:241], v[240:241], v[240:241] op_sel_hi:[0,1]
	v_lshlrev_b32_e32 v212, 16, v184
	v_and_b32_e32 v214, 0xffff0000, v184
	v_lshlrev_b32_e32 v218, 16, v185
	v_and_b32_e32 v232, 0xffff0000, v185
	v_add_f32_e32 v233, 0, v213
	v_add_f32_e32 v213, v194, v195
	v_add_f32_e32 v215, v196, v197
	v_mov_b32_e32 v219, v241
	s_waitcnt lgkmcnt(0)
	v_pk_add_f32 v[242:243], v[212:213], v[214:215]
	v_pk_add_f32 v[240:241], v[218:219], v[232:233]
	s_nop 0
	v_pk_add_f32 v[240:241], v[242:243], v[240:241]
	s_nop 0
	v_add_f32_e32 v213, v240, v241
	s_waitcnt lgkmcnt(0)
	s_nop 1
	v_add_f32_dpp v213, v213, v213 quad_perm:[1,0,3,2] row_mask:0xf bank_mask:0xf
	s_nop 1
	v_add_f32_dpp v213, v213, v213 quad_perm:[2,3,0,1] row_mask:0xf bank_mask:0xf
	s_nop 1
	v_add_f32_dpp v213, v213, v213 row_half_mirror row_mask:0xf bank_mask:0xf
	s_nop 1
	v_add_f32_dpp v213, v213, v213 row_mirror row_mask:0xf bank_mask:0xf
	v_mov_b32_e32 v215, v213
	s_nop 1
	v_permlane16_swap_b32_e32 v213, v215
	v_add_f32_e32 v213, v213, v215
	v_mov_b32_e32 v215, v213
	s_nop 1
	v_permlane32_swap_b32_e32 v213, v215
	v_add_f32_e32 v213, v213, v215
	v_fmac_f32_e32 v234, 0xba800000, v213
	v_fmac_f32_e32 v235, 0xba800000, v213
	v_fmac_f32_e32 v217, 0xba800000, v213
	v_fmac_f32_e32 v216, 0xba800000, v213
	v_mov_b32_e32 v240, v217
	v_mov_b32_e32 v241, v235
	v_mov_b32_e32 v217, v234
	v_pk_mul_f32 v[242:243], v[240:241], v[240:241]
	v_pk_mul_f32 v[234:235], v[216:217], v[216:217]
	v_fmac_f32_e32 v238, 0xba800000, v213
	v_pk_mov_b32 v[244:245], v[234:235], v[242:243] op_sel:[1,0]
	v_mov_b32_e32 v235, v243
	v_fmac_f32_e32 v239, 0xba800000, v213
	v_fmac_f32_e32 v237, 0xba800000, v213
	v_pk_add_f32 v[234:235], v[244:245], v[234:235]
	v_fmac_f32_e32 v236, 0xba800000, v213
	v_mov_b32_e32 v242, v237
	v_mov_b32_e32 v243, v239
	v_mov_b32_e32 v237, v238
	v_pk_add_f32 v[234:235], v[234:235], v[234:235] op_sel_hi:[0,1]
	v_pk_mul_f32 v[244:245], v[242:243], v[242:243]
	v_pk_mul_f32 v[238:239], v[236:237], v[236:237]
	v_fmac_f32_e32 v194, 0xba800000, v213
	v_pk_mov_b32 v[246:247], v[238:239], v[244:245] op_sel:[1,0]
	v_mov_b32_e32 v239, v245
	v_fmac_f32_e32 v195, 0xba800000, v213
	v_fmac_f32_e32 v196, 0xba800000, v213
	v_mul_f32_e32 v234, v194, v194
	v_pk_add_f32 v[238:239], v[246:247], v[238:239]
	v_fmac_f32_e32 v197, 0xba800000, v213
	v_pk_fma_f32 v[244:245], v[194:195], v[194:195], v[234:235] op_sel_hi:[1,1,0]
	v_mul_f32_e32 v234, v196, v196
	v_pk_add_f32 v[238:239], v[238:239], v[238:239] op_sel_hi:[0,1]
	v_pk_fma_f32 v[246:247], v[196:197], v[196:197], v[234:235] op_sel_hi:[1,1,0]
	v_fmac_f32_e32 v232, 0xba800000, v213
	v_fmac_f32_e32 v218, 0xba800000, v213
	v_fmac_f32_e32 v214, 0xba800000, v213
	v_fmac_f32_e32 v212, 0xba800000, v213
	v_mul_f32_e32 v244, v212, v212
	v_mul_f32_e32 v246, v214, v214
	v_mul_f32_e32 v234, v218, v218
	v_mul_f32_e32 v238, v232, v232
	v_pk_add_f32 v[244:245], v[244:245], v[246:247]
	v_pk_add_f32 v[234:235], v[234:235], v[238:239]
	s_nop 0
	v_pk_add_f32 v[234:235], v[244:245], v[234:235]
	s_nop 0
	v_add_f32_e32 v213, v234, v235
	s_waitcnt lgkmcnt(0)
	s_nop 1
	v_add_f32_dpp v213, v213, v213 quad_perm:[1,0,3,2] row_mask:0xf bank_mask:0xf
	s_nop 1
	v_add_f32_dpp v213, v213, v213 quad_perm:[2,3,0,1] row_mask:0xf bank_mask:0xf
	s_nop 1
	v_add_f32_dpp v213, v213, v213 row_half_mirror row_mask:0xf bank_mask:0xf
	s_nop 1
	v_add_f32_dpp v213, v213, v213 row_mirror row_mask:0xf bank_mask:0xf
	v_mov_b32_e32 v215, v213
	s_nop 1
	v_permlane16_swap_b32_e32 v213, v215
	v_add_f32_e32 v213, v213, v215
	v_mov_b32_e32 v215, v213
	s_nop 1
	v_permlane32_swap_b32_e32 v213, v215
	v_add_f32_e32 v213, v213, v215
	v_fmamk_f32 v213, v213, 0x3a800000, v228
	v_mul_f32_e32 v215, 0x4f800000, v213
	v_cmp_gt_f32_e32 vcc, s30, v213
	s_nop 1
	v_cndmask_b32_e32 v213, v213, v215, vcc
	v_sqrt_f32_e32 v215, v213
	s_nop 0
	v_add_u32_e32 v219, -1, v215
	v_fma_f32 v233, -v219, v215, v213
	v_cmp_ge_f32_e64 s[0:1], 0, v233
	v_add_u32_e32 v233, 1, v215
	s_nop 0
	v_cndmask_b32_e64 v219, v215, v219, s[0:1]
	v_fma_f32 v215, -v233, v215, v213
	v_cmp_lt_f32_e64 s[0:1], 0, v215
	s_nop 1
	v_cndmask_b32_e64 v215, v219, v233, s[0:1]
	v_mul_f32_e32 v219, 0x37800000, v215
	v_cndmask_b32_e32 v215, v215, v219, vcc
	v_cmp_class_f32_e32 vcc, v213, v229
	s_nop 1
	v_cndmask_b32_e32 v213, v215, v213, vcc
	v_div_scale_f32 v215, s[0:1], v213, v213, 1.0
	v_rcp_f32_e32 v219, v215
	s_nop 0
	v_fma_f32 v233, -v215, v219, 1.0
	v_fmac_f32_e32 v219, v233, v219
	v_div_scale_f32 v233, vcc, 1.0, v213, 1.0
	v_mul_f32_e32 v234, v233, v219
	v_fma_f32 v235, -v215, v234, v233
	v_fmac_f32_e32 v234, v235, v219
	v_fma_f32 v215, -v215, v234, v233
	v_div_fmas_f32 v215, v215, v219, v234
	v_div_fixup_f32 v234, v215, v213, 1.0
	v_pk_mul_f32 v[216:217], v[216:217], v[234:235] op_sel_hi:[1,0]
	v_pk_mul_f32 v[194:195], v[194:195], v[234:235] op_sel_hi:[1,0]
	v_mov_b32_e32 v213, v214
	v_pk_mul_f32 v[238:239], v[240:241], v[234:235] op_sel_hi:[1,0]
	v_pk_fma_f32 v[240:241], v[2:3], v[216:217], v[6:7]
	v_pk_mul_f32 v[216:217], v[236:237], v[234:235] op_sel_hi:[1,0]
	v_pk_mul_f32 v[196:197], v[196:197], v[234:235] op_sel_hi:[1,0]
	v_pk_fma_f32 v[244:245], v[18:19], v[194:195], v[30:31]
	v_pk_mul_f32 v[194:195], v[212:213], v[234:235] op_sel_hi:[1,0]
	v_mov_b32_e32 v219, v232
	v_pk_mul_f32 v[236:237], v[242:243], v[234:235] op_sel_hi:[1,0]
	v_pk_fma_f32 v[242:243], v[14:15], v[216:217], v[26:27]
	v_pk_fma_f32 v[216:217], v[20:21], v[196:197], v[32:33]
	v_pk_mul_f32 v[196:197], v[218:219], v[234:235] op_sel_hi:[1,0]
	v_pk_fma_f32 v[218:219], v[10:11], v[194:195], v[22:23]
	v_bfe_u32 v194, v240, 16, 1
	v_add3_u32 v194, v240, v194, s31
	v_bfe_u32 v195, v241, 16, 1
	v_pk_fma_f32 v[238:239], v[4:5], v[238:239], v[8:9]
	v_lshrrev_b32_e32 v194, 16, v194
	v_add3_u32 v195, v241, v195, s31
	v_and_or_b32 v194, v195, s29, v194
	v_bfe_u32 v195, v238, 16, 1
	v_pk_fma_f32 v[212:213], v[12:13], v[196:197], v[24:25]
	v_add3_u32 v195, v238, v195, s31
	v_bfe_u32 v196, v239, 16, 1
	v_lshrrev_b32_e32 v195, 16, v195
	v_add3_u32 v196, v239, v196, s31
	v_and_or_b32 v195, v196, s29, v195
	v_bfe_u32 v196, v242, 16, 1
	v_add3_u32 v196, v242, v196, s31
	v_bfe_u32 v197, v243, 16, 1
	v_fma_f32 v234, v36, v240, 0
	v_fma_f32 v235, v37, v240, 0
	v_fma_f32 v246, v38, v240, 0
	v_fma_f32 v247, v39, v240, 0
	v_fma_f32 v248, v40, v240, 0
	v_fma_f32 v249, v41, v240, 0
	v_pk_fma_f32 v[232:233], v[34:35], v[240:241], 0 op_sel_hi:[1,0,0]
	v_pk_fma_f32 v[236:237], v[16:17], v[236:237], v[28:29]
	v_lshrrev_b32_e32 v196, 16, v196
	v_add3_u32 v197, v243, v197, s31
	v_fmac_f32_e32 v234, v44, v241
	v_fmac_f32_e32 v235, v45, v241
	v_fmac_f32_e32 v246, v46, v241
	v_fmac_f32_e32 v247, v47, v241
	v_fmac_f32_e32 v248, v48, v241
	v_fmac_f32_e32 v249, v49, v241
	v_pk_fma_f32 v[232:233], v[42:43], v[240:241], v[232:233] op_sel:[0,1,0]
	v_and_or_b32 v196, v197, s29, v196
	v_bfe_u32 v197, v236, 16, 1
	v_fmac_f32_e32 v234, v52, v238
	v_fmac_f32_e32 v235, v53, v238
	v_fmac_f32_e32 v246, v54, v238
	v_fmac_f32_e32 v247, v55, v238
	v_fmac_f32_e32 v248, v56, v238
	v_fmac_f32_e32 v249, v57, v238
	v_pk_fma_f32 v[232:233], v[50:51], v[238:239], v[232:233] op_sel_hi:[1,0,1]
	v_add3_u32 v197, v236, v197, s31
	v_bfe_u32 v214, v237, 16, 1
	v_fmac_f32_e32 v234, v60, v239
	v_fmac_f32_e32 v235, v61, v239
	v_fmac_f32_e32 v246, v62, v239
	v_fmac_f32_e32 v247, v63, v239
	v_fmac_f32_e32 v248, v64, v239
	v_fmac_f32_e32 v249, v65, v239
	v_pk_fma_f32 v[232:233], v[58:59], v[238:239], v[232:233] op_sel:[0,1,0]
	v_lshrrev_b32_e32 v197, 16, v197
	v_add3_u32 v214, v237, v214, s31
	v_fmac_f32_e32 v234, v68, v242
	v_fmac_f32_e32 v235, v69, v242
	v_fmac_f32_e32 v246, v70, v242
	v_fmac_f32_e32 v247, v71, v242
	v_fmac_f32_e32 v248, v72, v242
	v_fmac_f32_e32 v249, v73, v242
	v_pk_fma_f32 v[232:233], v[66:67], v[242:243], v[232:233] op_sel_hi:[1,0,1]
	v_and_or_b32 v197, v214, s29, v197
	v_add_co_u32_e32 v214, vcc, s28, v210
	v_fmac_f32_e32 v234, v76, v243
	v_fmac_f32_e32 v235, v77, v243
	v_fmac_f32_e32 v246, v78, v243
	v_fmac_f32_e32 v247, v79, v243
	v_fmac_f32_e32 v248, v80, v243
	v_fmac_f32_e32 v249, v81, v243
	v_pk_fma_f32 v[232:233], v[74:75], v[242:243], v[232:233] op_sel:[0,1,0]
	v_addc_co_u32_e32 v215, vcc, 0, v211, vcc
	v_fmac_f32_e32 v234, v84, v236
	v_fmac_f32_e32 v235, v85, v236
	v_fmac_f32_e32 v246, v86, v236
	v_fmac_f32_e32 v247, v87, v236
	v_fmac_f32_e32 v248, v88, v236
	v_fmac_f32_e32 v249, v89, v236
	v_pk_fma_f32 v[232:233], v[82:83], v[236:237], v[232:233] op_sel_hi:[1,0,1]
	global_store_dwordx4 v[214:215], v[194:197], off
	v_fmac_f32_e32 v234, v92, v237
	v_fmac_f32_e32 v235, v93, v237
	v_bfe_u32 v194, v244, 16, 1
	v_fmac_f32_e32 v246, v94, v237
	v_fmac_f32_e32 v247, v95, v237
	v_fmac_f32_e32 v248, v96, v237
	v_fmac_f32_e32 v249, v97, v237
	v_pk_fma_f32 v[232:233], v[90:91], v[236:237], v[232:233] op_sel:[0,1,0]
	v_add3_u32 v194, v244, v194, s31
	v_bfe_u32 v195, v245, 16, 1
	v_fmac_f32_e32 v234, v108, v244
	v_fmac_f32_e32 v235, v109, v244
	v_fmac_f32_e32 v246, v98, v244
	v_fmac_f32_e32 v247, v99, v244
	v_fmac_f32_e32 v248, v100, v244
	v_fmac_f32_e32 v249, v101, v244
	v_pk_fma_f32 v[232:233], v[106:107], v[244:245], v[232:233] op_sel_hi:[1,0,1]
	v_lshrrev_b32_e32 v194, 16, v194
	v_add3_u32 v195, v245, v195, s31
	v_pk_fma_f32 v[232:233], v[102:103], v[244:245], v[232:233] op_sel:[0,1,0]
	v_fmac_f32_e32 v234, v104, v245
	v_fmac_f32_e32 v235, v105, v245
	v_fmac_f32_e32 v246, v110, v245
	v_fmac_f32_e32 v247, v111, v245
	v_fmac_f32_e32 v248, v112, v245
	v_fmac_f32_e32 v249, v113, v245
	v_and_or_b32 v194, v195, s29, v194
	v_bfe_u32 v195, v216, 16, 1
	v_bfe_u32 v196, v217, 16, 1
	v_fmac_f32_e32 v234, v124, v216
	v_fmac_f32_e32 v235, v125, v216
	v_fmac_f32_e32 v246, v138, v216
	v_fmac_f32_e32 v247, v139, v216
	v_fmac_f32_e32 v248, v140, v216
	v_fmac_f32_e32 v249, v141, v216
	v_pk_fma_f32 v[232:233], v[122:123], v[216:217], v[232:233] op_sel_hi:[1,0,1]
	v_add3_u32 v195, v216, v195, s31
	v_add3_u32 v196, v217, v196, s31
	v_fmac_f32_e32 v234, v116, v217
	v_fmac_f32_e32 v235, v117, v217
	v_fmac_f32_e32 v246, v118, v217
	v_fmac_f32_e32 v247, v119, v217
	v_fmac_f32_e32 v248, v120, v217
	v_fmac_f32_e32 v249, v121, v217
	v_pk_fma_f32 v[216:217], v[114:115], v[216:217], v[232:233] op_sel:[0,1,0]
	v_lshrrev_b32_e32 v195, 16, v195
	v_pk_fma_f32 v[216:217], v[126:127], v[218:219], v[216:217] op_sel_hi:[1,0,1]
	v_and_or_b32 v195, v196, s29, v195
	v_pk_fma_f32 v[216:217], v[134:135], v[218:219], v[216:217] op_sel:[0,1,0]
	v_bfe_u32 v196, v218, 16, 1
	v_pk_fma_f32 v[216:217], v[142:143], v[212:213], v[216:217] op_sel_hi:[1,0,1]
	v_bfe_u32 v197, v219, 16, 1
	v_pk_fma_f32 v[216:217], v[154:155], v[212:213], v[216:217] op_sel:[0,1,0]
	ds_bpermute_b32 v232, v220, v216
	ds_bpermute_b32 v233, v220, v217
	v_fmac_f32_e32 v234, v128, v218
	v_fmac_f32_e32 v235, v129, v218
	v_fmac_f32_e32 v246, v130, v218
	v_fmac_f32_e32 v247, v131, v218
	v_fmac_f32_e32 v248, v132, v218
	v_fmac_f32_e32 v249, v133, v218
	s_waitcnt lgkmcnt(0)
	v_pk_add_f32 v[216:217], v[216:217], v[232:233]
	v_add3_u32 v196, v218, v196, s31
	v_add3_u32 v197, v219, v197, s31
	v_fmac_f32_e32 v234, v136, v219
	v_fmac_f32_e32 v235, v137, v219
	v_fmac_f32_e32 v246, v146, v219
	v_fmac_f32_e32 v247, v147, v219
	v_fmac_f32_e32 v248, v148, v219
	v_fmac_f32_e32 v249, v149, v219
	ds_bpermute_b32 v218, v221, v216
	ds_bpermute_b32 v219, v221, v217
	v_lshrrev_b32_e32 v196, 16, v196
	v_fmac_f32_e32 v234, v144, v212
	v_and_or_b32 v196, v197, s29, v196
	v_bfe_u32 v197, v212, 16, 1
	s_waitcnt lgkmcnt(0)
	v_pk_add_f32 v[216:217], v[216:217], v[218:219]
	v_fmac_f32_e32 v234, v156, v213
	v_add3_u32 v197, v212, v197, s31
	v_fmac_f32_e32 v235, v145, v212
	v_fmac_f32_e32 v246, v150, v212
	v_fmac_f32_e32 v247, v151, v212
	v_fmac_f32_e32 v248, v152, v212
	v_fmac_f32_e32 v249, v153, v212
	ds_bpermute_b32 v218, v222, v216
	ds_bpermute_b32 v219, v222, v217
	ds_bpermute_b32 v212, v220, v234
	v_fmac_f32_e32 v235, v157, v213
	v_fmac_f32_e32 v246, v158, v213
	ds_bpermute_b32 v233, v220, v235
	s_waitcnt lgkmcnt(2)
	v_pk_add_f32 v[216:217], v[216:217], v[218:219]
	s_waitcnt lgkmcnt(1)
	v_add_f32_e32 v212, v234, v212
	ds_bpermute_b32 v218, v223, v216
	ds_bpermute_b32 v219, v223, v217
	ds_bpermute_b32 v232, v221, v212
	ds_bpermute_b32 v234, v220, v246
	v_fmac_f32_e32 v247, v159, v213
	v_fmac_f32_e32 v248, v160, v213
	s_waitcnt lgkmcnt(2)
	v_pk_add_f32 v[216:217], v[216:217], v[218:219]
	s_waitcnt lgkmcnt(1)
	v_add_f32_e32 v212, v212, v232
	ds_bpermute_b32 v218, v224, v216
	ds_bpermute_b32 v219, v224, v217
	ds_bpermute_b32 v232, v222, v212
	v_fmac_f32_e32 v249, v161, v213
	ds_bpermute_b32 v238, v220, v247
	ds_bpermute_b32 v239, v220, v249
	s_waitcnt lgkmcnt(3)
	v_pk_add_f32 v[216:217], v[216:217], v[218:219]
	v_add_f32_e32 v218, v235, v233
	s_waitcnt lgkmcnt(2)
	v_add_f32_e32 v212, v212, v232
	v_add_f32_e32 v232, v246, v234
	ds_bpermute_b32 v219, v221, v218
	ds_bpermute_b32 v233, v221, v232
	ds_bpermute_b32 v234, v223, v212
	s_waitcnt lgkmcnt(4)
	v_add_f32_e32 v238, v247, v238
	s_waitcnt lgkmcnt(3)
	v_add_f32_e32 v239, v249, v239
	s_waitcnt lgkmcnt(2)
	v_add_f32_e32 v219, v218, v219
	s_waitcnt lgkmcnt(1)
	v_add_f32_e32 v232, v232, v233
	ds_bpermute_b32 v235, v222, v219
	ds_bpermute_b32 v233, v222, v232
	s_waitcnt lgkmcnt(2)
	v_add_f32_e32 v212, v212, v234
	ds_bpermute_b32 v236, v224, v212
	ds_bpermute_b32 v240, v221, v238
	s_waitcnt lgkmcnt(3)
	v_add_f32_e32 v234, v219, v235
	s_waitcnt lgkmcnt(2)
	v_add_f32_e32 v232, v232, v233
	ds_bpermute_b32 v235, v223, v234
	ds_bpermute_b32 v233, v223, v232
	s_waitcnt lgkmcnt(3)
	v_add_f32_e32 v212, v212, v236
	ds_bpermute_b32 v242, v221, v239
	s_waitcnt lgkmcnt(3)
	v_add_f32_e32 v238, v238, v240
	s_waitcnt lgkmcnt(2)
	v_add_f32_e32 v234, v234, v235
	s_waitcnt lgkmcnt(1)
	v_add_f32_e32 v236, v232, v233
	ds_bpermute_b32 v235, v224, v234
	ds_bpermute_b32 v237, v224, v236
	s_waitcnt lgkmcnt(2)
	v_add_f32_e32 v239, v239, v242
	ds_bpermute_b32 v240, v222, v238
	ds_bpermute_b32 v242, v222, v239
	s_waitcnt lgkmcnt(3)
	v_add_f32_e32 v233, v234, v235
	s_waitcnt lgkmcnt(2)
	v_add_f32_e32 v235, v236, v237
	ds_bpermute_b32 v237, v220, v248
	s_waitcnt lgkmcnt(2)
	v_add_f32_e32 v238, v238, v240
	s_waitcnt lgkmcnt(1)
	v_add_f32_e32 v239, v239, v242
	ds_bpermute_b32 v240, v223, v238
	ds_bpermute_b32 v242, v223, v239
	s_waitcnt lgkmcnt(2)
	v_add_f32_e32 v237, v248, v237
	ds_bpermute_b32 v241, v221, v237
	ds_bpermute_b32 v218, v225, v216
	s_waitcnt lgkmcnt(3)
	v_add_f32_e32 v238, v238, v240
	s_waitcnt lgkmcnt(2)
	v_add_f32_e32 v242, v239, v242
	ds_bpermute_b32 v240, v224, v238
	s_waitcnt lgkmcnt(2)
	v_add_f32_e32 v237, v237, v241
	ds_bpermute_b32 v241, v222, v237
	ds_bpermute_b32 v244, v224, v242
	ds_bpermute_b32 v219, v225, v217
	ds_bpermute_b32 v232, v225, v212
	ds_bpermute_b32 v234, v225, v233
	s_waitcnt lgkmcnt(4)
	v_add_f32_e32 v237, v237, v241
	ds_bpermute_b32 v241, v223, v237
	ds_bpermute_b32 v236, v225, v235
	v_lshrrev_b32_e32 v197, 16, v197
	s_waitcnt lgkmcnt(1)
	v_add_f32_e32 v241, v237, v241
	ds_bpermute_b32 v243, v224, v241
	v_add_f32_e32 v237, v238, v240
	ds_bpermute_b32 v238, v225, v237
	s_waitcnt lgkmcnt(1)
	v_add_f32_e32 v239, v241, v243
	v_add_f32_e32 v241, v242, v244
	ds_bpermute_b32 v240, v225, v239
	ds_bpermute_b32 v242, v225, v241
	v_bfe_u32 v243, v213, 16, 1
	v_add3_u32 v213, v213, v243, s31
	v_and_or_b32 v197, v213, s29, v197
	global_store_dwordx4 v[214:215], v[194:197], off offset:1024
	s_and_saveexec_b64 s[24:25], s[2:3]
	s_cbranch_execz .LBB0_1243
	v_pk_add_f32 v[196:197], v[216:217], v[218:219]
	v_add_f32_e32 v212, v212, v232
	v_cmp_gt_f32_e32 vcc, v197, v196
	v_add_f32_e32 v233, v233, v234
	v_add_f32_e32 v215, v235, v236
	v_cndmask_b32_e32 v194, v196, v197, vcc
	v_cmp_gt_f32_e64 s[0:1], v212, v194
	s_waitcnt lgkmcnt(2)
	v_add_f32_e32 v214, v237, v238
	s_waitcnt lgkmcnt(1)
	v_add_f32_e32 v213, v239, v240
	v_cndmask_b32_e64 v194, v194, v212, s[0:1]
	v_cmp_gt_f32_e64 s[4:5], v233, v194
	s_waitcnt lgkmcnt(0)
	v_add_f32_e32 v195, v241, v242
	v_cmp_nlg_f32_e64 s[14:15], s34, v196
	v_cndmask_b32_e64 v194, v194, v233, s[4:5]
	v_cmp_gt_f32_e64 s[6:7], v215, v194
	s_nop 1
	v_cndmask_b32_e64 v194, v194, v215, s[6:7]
	v_cmp_gt_f32_e64 s[8:9], v214, v194
	s_nop 1
	v_cndmask_b32_e64 v194, v194, v214, s[8:9]
	v_cmp_gt_f32_e64 s[10:11], v213, v194
	s_nop 1
	v_cndmask_b32_e64 v216, v194, v213, s[10:11]
	v_cndmask_b32_e64 v194, 0, 1, vcc
	v_cndmask_b32_e64 v194, v194, 2, s[0:1]
	v_cndmask_b32_e64 v194, v194, 3, s[4:5]
	v_cndmask_b32_e64 v194, v194, 4, s[6:7]
	v_cndmask_b32_e64 v194, v194, 5, s[8:9]
	v_cndmask_b32_e64 v194, v194, 6, s[10:11]
	v_cmp_ngt_f32_e32 vcc, v195, v216
	s_and_b64 s[16:17], s[10:11], vcc
	s_nop 0
	v_cndmask_b32_e32 v194, 7, v194, vcc
	v_cmp_eq_u32_e64 s[12:13], 0, v194
	s_or_b64 s[12:13], s[12:13], s[14:15]
	v_cmp_ne_u32_e64 s[10:11], 1, v194
	v_cndmask_b32_e64 v196, v196, v231, s[12:13]
	v_cmp_gt_f32_e64 s[14:15], v197, v196
	s_and_b64 s[10:11], s[10:11], s[14:15]
	v_cndmask_b32_e64 v196, v196, v197, s[10:11]
	v_cmp_ne_u32_e64 s[8:9], 2, v194
	v_cmp_gt_f32_e64 s[14:15], v212, v196
	s_and_b64 s[8:9], s[8:9], s[14:15]
	v_cndmask_b32_e64 v196, v196, v212, s[8:9]
	v_cmp_ne_u32_e64 s[6:7], 3, v194
	v_cmp_gt_f32_e64 s[14:15], v233, v196
	s_and_b64 s[6:7], s[6:7], s[14:15]
	v_cndmask_b32_e64 v196, v196, v233, s[6:7]
	v_cmp_ne_u32_e64 s[4:5], 4, v194
	v_cmp_gt_f32_e64 s[14:15], v215, v196
	s_and_b64 s[4:5], s[4:5], s[14:15]
	v_cndmask_b32_e64 v196, v196, v215, s[4:5]
	v_cmp_ne_u32_e64 s[0:1], 5, v194
	v_cmp_gt_f32_e64 s[14:15], v214, v196
	s_and_b64 s[0:1], s[0:1], s[14:15]
	v_cndmask_b32_e64 v196, v196, v214, s[0:1]
	v_cmp_ngt_f32_e64 s[14:15], v213, v196
	s_or_b64 s[14:15], s[16:17], s[14:15]
	v_cndmask_b32_e64 v197, 0, -1, s[12:13]
	v_cndmask_b32_e64 v196, v213, v196, s[14:15]
	v_cmp_gt_f32_e64 s[16:17], v195, v196
	s_and_b64 s[16:17], vcc, s[16:17]
	v_cndmask_b32_e64 v197, v197, 1, s[10:11]
	v_cndmask_b32_e64 v196, v196, v195, s[16:17]
	v_cndmask_b32_e32 v195, v195, v216, vcc
	v_sub_f32_e32 v195, v196, v195
	v_mul_f32_e32 v195, 0x3fb8aa3b, v195
	v_exp_f32_e32 v213, v195
	v_cndmask_b32_e64 v195, v197, 2, s[8:9]
	v_cndmask_b32_e64 v195, v195, 3, s[6:7]
	v_cndmask_b32_e64 v195, v195, 4, s[4:5]
	v_add_f32_e32 v212, 1.0, v213
	v_div_scale_f32 v196, s[4:5], v212, v212, 1.0
	v_rcp_f32_e32 v214, v196
	v_cndmask_b32_e64 v195, v195, 5, s[0:1]
	v_cndmask_b32_e64 v195, 6, v195, s[14:15]
	v_cndmask_b32_e64 v195, v195, 7, s[16:17]
	v_fma_f32 v197, -v196, v214, 1.0
	v_fmac_f32_e32 v214, v197, v214
	v_div_scale_f32 v197, vcc, 1.0, v212, 1.0
	v_mul_f32_e32 v215, v197, v214
	v_fma_f32 v216, -v196, v215, v197
	v_fmac_f32_e32 v215, v216, v214
	v_fma_f32 v216, -v196, v215, v197
	v_lshl_add_u32 v196, v194, 2, 0
	ds_add_rtn_u32 v196, v196, v230
	v_lshl_add_u32 v197, v195, 2, 0
	ds_add_rtn_u32 v197, v197, v230
	v_div_fmas_f32 v214, v216, v214, v215
	v_div_fixup_f32 v212, v214, v212, 1.0
	v_mul_f32_e32 v213, v213, v212
	s_waitcnt lgkmcnt(0)
	ds_write_b128 v226, v[194:197] offset:32
	v_add_u32_e32 v194, 4, v227
	v_ashrrev_i32_e32 v195, 31, v194
	v_lshl_add_u64 v[194:195], v[194:195], 2, s[36:37]
	global_store_dwordx2 v[194:195], v[212:213], off

.LBB0_1245:
	s_waitcnt vmcnt(7)
	v_lshlrev_b32_e32 v219, 16, v187
	v_lshlrev_b32_e32 v218, 16, v186
	v_and_b32_e32 v187, 0xffff0000, v187
	v_and_b32_e32 v186, 0xffff0000, v186
	s_waitcnt vmcnt(6)
	v_lshlrev_b32_e32 v194, 16, v190
	v_and_b32_e32 v195, 0xffff0000, v190
	v_lshlrev_b32_e32 v196, 16, v191
	v_and_b32_e32 v197, 0xffff0000, v191
	v_pk_add_f32 v[190:191], v[218:219], v[186:187]
	v_lshlrev_b32_e32 v233, 16, v189
	v_add_f32_e32 v190, v190, v191
	v_lshlrev_b32_e32 v232, 16, v188
	v_and_b32_e32 v189, 0xffff0000, v189
	v_and_b32_e32 v188, 0xffff0000, v188
	v_add_f32_e32 v217, 0, v190
	v_pk_add_f32 v[190:191], v[232:233], v[188:189]
	v_lshlrev_b32_e32 v212, 16, v192
	v_pk_add_f32 v[190:191], v[190:191], v[190:191] op_sel_hi:[0,1]
	v_and_b32_e32 v192, 0xffff0000, v192
	v_lshlrev_b32_e32 v214, 16, v193
	v_and_b32_e32 v216, 0xffff0000, v193
	v_add_f32_e32 v213, v194, v195
	v_add_f32_e32 v193, v196, v197
	v_mov_b32_e32 v215, v191
	v_pk_add_f32 v[234:235], v[212:213], v[192:193]
	v_pk_add_f32 v[190:191], v[214:215], v[216:217]
	s_nop 0
	v_pk_add_f32 v[190:191], v[234:235], v[190:191]
	s_nop 0
	v_add_f32_e32 v190, v190, v191
	s_waitcnt lgkmcnt(0)
	s_nop 1
	v_add_f32_dpp v190, v190, v190 quad_perm:[1,0,3,2] row_mask:0xf bank_mask:0xf
	s_nop 1
	v_add_f32_dpp v190, v190, v190 quad_perm:[2,3,0,1] row_mask:0xf bank_mask:0xf
	s_nop 1
	v_add_f32_dpp v190, v190, v190 row_half_mirror row_mask:0xf bank_mask:0xf
	s_nop 1
	v_add_f32_dpp v190, v190, v190 row_mirror row_mask:0xf bank_mask:0xf
	v_mov_b32_e32 v191, v190
	s_nop 1
	v_permlane16_swap_b32_e32 v190, v191
	v_add_f32_e32 v190, v190, v191
	v_mov_b32_e32 v191, v190
	s_nop 1
	v_permlane32_swap_b32_e32 v190, v191
	v_add_f32_e32 v193, v190, v191
	v_fmac_f32_e32 v186, 0xba800000, v193
	v_fmac_f32_e32 v187, 0xba800000, v193
	v_fmac_f32_e32 v219, 0xba800000, v193
	v_fmac_f32_e32 v218, 0xba800000, v193
	v_mov_b32_e32 v234, v219
	v_mov_b32_e32 v235, v187
	v_mov_b32_e32 v219, v186
	v_pk_mul_f32 v[190:191], v[234:235], v[234:235]
	v_pk_mul_f32 v[186:187], v[218:219], v[218:219]
	v_fmac_f32_e32 v188, 0xba800000, v193
	v_pk_mov_b32 v[236:237], v[186:187], v[190:191] op_sel:[1,0]
	v_mov_b32_e32 v187, v191
	v_fmac_f32_e32 v189, 0xba800000, v193
	v_fmac_f32_e32 v233, 0xba800000, v193
	v_pk_add_f32 v[186:187], v[236:237], v[186:187]
	v_fmac_f32_e32 v232, 0xba800000, v193
	v_mov_b32_e32 v236, v233
	v_mov_b32_e32 v237, v189
	v_mov_b32_e32 v233, v188
	v_pk_add_f32 v[186:187], v[186:187], v[186:187] op_sel_hi:[0,1]
	v_pk_mul_f32 v[190:191], v[236:237], v[236:237]
	v_pk_mul_f32 v[188:189], v[232:233], v[232:233]
	v_fmac_f32_e32 v194, 0xba800000, v193
	v_pk_mov_b32 v[238:239], v[188:189], v[190:191] op_sel:[1,0]
	v_mov_b32_e32 v189, v191
	v_fmac_f32_e32 v195, 0xba800000, v193
	v_fmac_f32_e32 v196, 0xba800000, v193
	v_mul_f32_e32 v186, v194, v194
	v_pk_add_f32 v[188:189], v[238:239], v[188:189]
	v_fmac_f32_e32 v197, 0xba800000, v193
	v_pk_fma_f32 v[190:191], v[194:195], v[194:195], v[186:187] op_sel_hi:[1,1,0]
	v_mul_f32_e32 v186, v196, v196
	v_pk_add_f32 v[188:189], v[188:189], v[188:189] op_sel_hi:[0,1]
	v_pk_fma_f32 v[238:239], v[196:197], v[196:197], v[186:187] op_sel_hi:[1,1,0]
	v_fmac_f32_e32 v216, 0xba800000, v193
	v_fmac_f32_e32 v214, 0xba800000, v193
	v_fmac_f32_e32 v192, 0xba800000, v193
	v_fmac_f32_e32 v212, 0xba800000, v193
	v_mul_f32_e32 v190, v212, v212
	v_mul_f32_e32 v238, v192, v192
	v_mul_f32_e32 v186, v214, v214
	v_mul_f32_e32 v188, v216, v216
	v_pk_add_f32 v[190:191], v[190:191], v[238:239]
	v_pk_add_f32 v[186:187], v[186:187], v[188:189]
	v_lshl_add_u64 v[238:239], v[210:211], 0, s[18:19]
	v_pk_add_f32 v[186:187], v[190:191], v[186:187]
	v_lshl_add_u64 v[190:191], v[210:211], 0, s[20:21]
	v_add_f32_e32 v186, v186, v187
	ds_bpermute_b32 v187, v220, v186
	v_mov_b32_e32 v213, v192
	v_mov_b32_e32 v215, v216
	s_waitcnt lgkmcnt(0)
	v_add_f32_e32 v186, v186, v187
	ds_bpermute_b32 v187, v221, v186
	s_waitcnt lgkmcnt(0)
	v_add_f32_e32 v186, v186, v187
	ds_bpermute_b32 v187, v222, v186
	s_waitcnt lgkmcnt(0)
	v_add_f32_e32 v186, v186, v187
	ds_bpermute_b32 v187, v223, v186
	s_waitcnt lgkmcnt(0)
	v_add_f32_e32 v186, v186, v187
	ds_bpermute_b32 v187, v224, v186
	s_waitcnt lgkmcnt(0)
	v_add_f32_e32 v186, v186, v187
	ds_bpermute_b32 v187, v225, v186
	s_waitcnt lgkmcnt(0)
	v_add_f32_e32 v186, v186, v187
	v_fmamk_f32 v186, v186, 0x3a800000, v228
	v_mul_f32_e32 v187, 0x4f800000, v186
	v_cmp_gt_f32_e32 vcc, s30, v186
	s_nop 1
	v_cndmask_b32_e32 v186, v186, v187, vcc
	v_sqrt_f32_e32 v187, v186
	s_nop 0
	v_add_u32_e32 v188, -1, v187
	v_fma_f32 v189, -v188, v187, v186
	v_cmp_ge_f32_e64 s[0:1], 0, v189
	v_add_u32_e32 v189, 1, v187
	s_nop 0
	v_cndmask_b32_e64 v188, v187, v188, s[0:1]
	v_fma_f32 v187, -v189, v187, v186
	v_cmp_lt_f32_e64 s[0:1], 0, v187
	s_nop 1
	v_cndmask_b32_e64 v187, v188, v189, s[0:1]
	v_mul_f32_e32 v188, 0x37800000, v187
	v_cndmask_b32_e32 v187, v187, v188, vcc
	v_cmp_class_f32_e32 vcc, v186, v229
	s_nop 1
	v_cndmask_b32_e32 v186, v187, v186, vcc
	v_div_scale_f32 v187, s[0:1], v186, v186, 1.0
	v_rcp_f32_e32 v188, v187
	s_nop 0
	v_fma_f32 v189, -v187, v188, 1.0
	v_fmac_f32_e32 v188, v189, v188
	v_div_scale_f32 v189, vcc, 1.0, v186, 1.0
	v_mul_f32_e32 v193, v189, v188
	v_fma_f32 v210, -v187, v193, v189
	v_fmac_f32_e32 v193, v210, v188
	v_fma_f32 v187, -v187, v193, v189
	v_div_fmas_f32 v187, v187, v188, v193
	v_div_fixup_f32 v186, v187, v186, 1.0
	v_pk_mul_f32 v[188:189], v[218:219], v[186:187] op_sel_hi:[1,0]
	v_pk_mul_f32 v[210:211], v[234:235], v[186:187] op_sel_hi:[1,0]
	v_pk_fma_f32 v[218:219], v[2:3], v[188:189], v[6:7]
	v_pk_mul_f32 v[188:189], v[232:233], v[186:187] op_sel_hi:[1,0]
	v_pk_mul_f32 v[232:233], v[236:237], v[186:187] op_sel_hi:[1,0]
	v_pk_fma_f32 v[234:235], v[14:15], v[188:189], v[26:27]
	v_pk_mul_f32 v[188:189], v[194:195], v[186:187] op_sel_hi:[1,0]
	v_pk_mul_f32 v[194:195], v[196:197], v[186:187] op_sel_hi:[1,0]
	v_pk_fma_f32 v[236:237], v[18:19], v[188:189], v[30:31]
	v_pk_mul_f32 v[188:189], v[212:213], v[186:187] op_sel_hi:[1,0]
	v_pk_mul_f32 v[186:187], v[214:215], v[186:187] op_sel_hi:[1,0]
	v_pk_fma_f32 v[210:211], v[4:5], v[210:211], v[8:9]
	v_pk_fma_f32 v[192:193], v[12:13], v[186:187], v[24:25]
	v_bfe_u32 v186, v218, 16, 1
	v_add3_u32 v186, v218, v186, s31
	v_bfe_u32 v187, v219, 16, 1
	v_lshrrev_b32_e32 v186, 16, v186
	v_add3_u32 v187, v219, v187, s31
	v_and_or_b32 v186, v187, s29, v186
	v_bfe_u32 v187, v210, 16, 1
	v_pk_fma_f32 v[196:197], v[10:11], v[188:189], v[22:23]
	v_add3_u32 v187, v210, v187, s31
	v_bfe_u32 v188, v211, 16, 1
	v_lshrrev_b32_e32 v187, 16, v187
	v_add3_u32 v188, v211, v188, s31
	v_and_or_b32 v187, v188, s29, v187
	v_bfe_u32 v188, v234, 16, 1
	v_add3_u32 v188, v234, v188, s31
	v_bfe_u32 v189, v235, 16, 1
	v_pk_fma_f32 v[232:233], v[16:17], v[232:233], v[28:29]
	v_lshrrev_b32_e32 v188, 16, v188
	v_add3_u32 v189, v235, v189, s31
	v_and_or_b32 v188, v189, s29, v188
	v_bfe_u32 v189, v232, 16, 1
	v_add3_u32 v189, v232, v189, s31
	v_bfe_u32 v212, v233, 16, 1
	v_lshrrev_b32_e32 v189, 16, v189
	v_add3_u32 v212, v233, v212, s31
	v_and_or_b32 v189, v212, s29, v189
	global_store_dwordx4 v[238:239], v[186:189], off
	v_fma_f32 v214, v36, v218, 0
	v_fma_f32 v215, v37, v218, 0
	v_fma_f32 v216, v38, v218, 0
	v_fma_f32 v217, v39, v218, 0
	v_fma_f32 v238, v40, v218, 0
	v_fma_f32 v239, v41, v218, 0
	v_pk_fma_f32 v[212:213], v[34:35], v[218:219], 0 op_sel_hi:[1,0,0]
	v_fmac_f32_e32 v214, v44, v219
	v_fmac_f32_e32 v215, v45, v219
	v_fmac_f32_e32 v216, v46, v219
	v_fmac_f32_e32 v217, v47, v219
	v_fmac_f32_e32 v238, v48, v219
	v_fmac_f32_e32 v239, v49, v219
	v_pk_fma_f32 v[212:213], v[42:43], v[218:219], v[212:213] op_sel:[0,1,0]
	v_fmac_f32_e32 v214, v52, v210
	v_fmac_f32_e32 v215, v53, v210
	v_fmac_f32_e32 v216, v54, v210
	v_fmac_f32_e32 v217, v55, v210
	v_fmac_f32_e32 v238, v56, v210
	v_fmac_f32_e32 v239, v57, v210
	v_pk_fma_f32 v[212:213], v[50:51], v[210:211], v[212:213] op_sel_hi:[1,0,1]
	v_fmac_f32_e32 v214, v60, v211
	v_fmac_f32_e32 v215, v61, v211
	v_fmac_f32_e32 v216, v62, v211
	v_fmac_f32_e32 v217, v63, v211
	v_fmac_f32_e32 v238, v64, v211
	v_fmac_f32_e32 v239, v65, v211
	v_pk_fma_f32 v[210:211], v[58:59], v[210:211], v[212:213] op_sel:[0,1,0]
	v_fmac_f32_e32 v214, v68, v234
	v_fmac_f32_e32 v215, v69, v234
	v_fmac_f32_e32 v216, v70, v234
	v_fmac_f32_e32 v217, v71, v234
	v_fmac_f32_e32 v238, v72, v234
	v_fmac_f32_e32 v239, v73, v234
	v_pk_fma_f32 v[210:211], v[66:67], v[234:235], v[210:211] op_sel_hi:[1,0,1]
	v_fmac_f32_e32 v214, v76, v235
	v_fmac_f32_e32 v215, v77, v235
	v_fmac_f32_e32 v216, v78, v235
	v_fmac_f32_e32 v217, v79, v235
	v_fmac_f32_e32 v238, v80, v235
	v_fmac_f32_e32 v239, v81, v235
	v_pk_fma_f32 v[210:211], v[74:75], v[234:235], v[210:211] op_sel:[0,1,0]
	v_fmac_f32_e32 v214, v84, v232
	v_fmac_f32_e32 v215, v85, v232
	v_fmac_f32_e32 v216, v86, v232
	v_fmac_f32_e32 v217, v87, v232
	v_fmac_f32_e32 v238, v88, v232
	v_fmac_f32_e32 v239, v89, v232
	v_pk_fma_f32 v[210:211], v[82:83], v[232:233], v[210:211] op_sel_hi:[1,0,1]
	v_bfe_u32 v186, v236, 16, 1
	v_fmac_f32_e32 v214, v92, v233
	v_fmac_f32_e32 v215, v93, v233
	v_fmac_f32_e32 v216, v94, v233
	v_fmac_f32_e32 v217, v95, v233
	v_fmac_f32_e32 v238, v96, v233
	v_fmac_f32_e32 v239, v97, v233
	v_pk_fma_f32 v[210:211], v[90:91], v[232:233], v[210:211] op_sel:[0,1,0]
	v_add3_u32 v186, v236, v186, s31
	v_bfe_u32 v187, v237, 16, 1
	v_fmac_f32_e32 v214, v108, v236
	v_fmac_f32_e32 v215, v109, v236
	v_fmac_f32_e32 v216, v98, v236
	v_fmac_f32_e32 v217, v99, v236
	v_fmac_f32_e32 v238, v100, v236
	v_fmac_f32_e32 v239, v101, v236
	v_pk_fma_f32 v[210:211], v[106:107], v[236:237], v[210:211] op_sel_hi:[1,0,1]
	v_pk_fma_f32 v[194:195], v[20:21], v[194:195], v[32:33]
	v_lshrrev_b32_e32 v186, 16, v186
	v_add3_u32 v187, v237, v187, s31
	v_pk_fma_f32 v[210:211], v[102:103], v[236:237], v[210:211] op_sel:[0,1,0]
	v_fmac_f32_e32 v214, v104, v237
	v_fmac_f32_e32 v215, v105, v237
	v_fmac_f32_e32 v216, v110, v237
	v_fmac_f32_e32 v217, v111, v237
	v_fmac_f32_e32 v238, v112, v237
	v_fmac_f32_e32 v239, v113, v237
	v_and_or_b32 v186, v187, s29, v186
	v_bfe_u32 v187, v194, 16, 1
	v_bfe_u32 v188, v195, 16, 1
	v_fmac_f32_e32 v214, v124, v194
	v_fmac_f32_e32 v215, v125, v194
	v_fmac_f32_e32 v216, v138, v194
	v_fmac_f32_e32 v217, v139, v194
	v_fmac_f32_e32 v238, v140, v194
	v_fmac_f32_e32 v239, v141, v194
	v_pk_fma_f32 v[210:211], v[122:123], v[194:195], v[210:211] op_sel_hi:[1,0,1]
	v_add3_u32 v187, v194, v187, s31
	v_add3_u32 v188, v195, v188, s31
	v_fmac_f32_e32 v214, v116, v195
	v_fmac_f32_e32 v215, v117, v195
	v_fmac_f32_e32 v216, v118, v195
	v_fmac_f32_e32 v217, v119, v195
	v_fmac_f32_e32 v238, v120, v195
	v_fmac_f32_e32 v239, v121, v195
	v_pk_fma_f32 v[194:195], v[114:115], v[194:195], v[210:211] op_sel:[0,1,0]
	v_lshrrev_b32_e32 v187, 16, v187
	v_pk_fma_f32 v[194:195], v[126:127], v[196:197], v[194:195] op_sel_hi:[1,0,1]
	v_and_or_b32 v187, v188, s29, v187
	v_pk_fma_f32 v[194:195], v[134:135], v[196:197], v[194:195] op_sel:[0,1,0]
	v_bfe_u32 v188, v196, 16, 1
	v_pk_fma_f32 v[194:195], v[142:143], v[192:193], v[194:195] op_sel_hi:[1,0,1]
	v_bfe_u32 v189, v197, 16, 1
	v_pk_fma_f32 v[194:195], v[154:155], v[192:193], v[194:195] op_sel:[0,1,0]
	ds_bpermute_b32 v210, v220, v194
	ds_bpermute_b32 v211, v220, v195
	v_fmac_f32_e32 v214, v128, v196
	v_fmac_f32_e32 v215, v129, v196
	v_fmac_f32_e32 v216, v130, v196
	v_fmac_f32_e32 v217, v131, v196
	v_fmac_f32_e32 v238, v132, v196
	v_fmac_f32_e32 v239, v133, v196
	s_waitcnt lgkmcnt(0)
	v_pk_add_f32 v[194:195], v[194:195], v[210:211]
	v_add3_u32 v188, v196, v188, s31
	v_add3_u32 v189, v197, v189, s31
	v_fmac_f32_e32 v214, v136, v197
	v_fmac_f32_e32 v215, v137, v197
	v_fmac_f32_e32 v216, v146, v197
	v_fmac_f32_e32 v217, v147, v197
	v_fmac_f32_e32 v238, v148, v197
	v_fmac_f32_e32 v239, v149, v197
	ds_bpermute_b32 v196, v221, v194
	ds_bpermute_b32 v197, v221, v195
	v_lshrrev_b32_e32 v188, 16, v188
	v_fmac_f32_e32 v214, v144, v192
	v_and_or_b32 v188, v189, s29, v188
	v_bfe_u32 v189, v192, 16, 1
	s_waitcnt lgkmcnt(0)
	v_pk_add_f32 v[194:195], v[194:195], v[196:197]
	v_fmac_f32_e32 v214, v156, v193
	v_add3_u32 v189, v192, v189, s31
	v_fmac_f32_e32 v215, v145, v192
	v_fmac_f32_e32 v216, v150, v192
	v_fmac_f32_e32 v217, v151, v192
	v_fmac_f32_e32 v238, v152, v192
	v_fmac_f32_e32 v239, v153, v192
	ds_bpermute_b32 v196, v222, v194
	ds_bpermute_b32 v197, v222, v195
	ds_bpermute_b32 v192, v220, v214
	v_fmac_f32_e32 v215, v157, v193
	v_fmac_f32_e32 v216, v158, v193
	ds_bpermute_b32 v211, v220, v215
	s_waitcnt lgkmcnt(2)
	v_pk_add_f32 v[194:195], v[194:195], v[196:197]
	s_waitcnt lgkmcnt(1)
	v_add_f32_e32 v192, v214, v192
	ds_bpermute_b32 v196, v223, v194
	ds_bpermute_b32 v197, v223, v195
	ds_bpermute_b32 v210, v221, v192
	ds_bpermute_b32 v212, v220, v216
	v_fmac_f32_e32 v217, v159, v193
	v_fmac_f32_e32 v238, v160, v193
	s_waitcnt lgkmcnt(2)
	v_pk_add_f32 v[194:195], v[194:195], v[196:197]
	s_waitcnt lgkmcnt(1)
	v_add_f32_e32 v192, v192, v210
	ds_bpermute_b32 v196, v224, v194
	ds_bpermute_b32 v197, v224, v195
	ds_bpermute_b32 v210, v222, v192
	v_fmac_f32_e32 v239, v161, v193
	ds_bpermute_b32 v218, v220, v239
	v_lshrrev_b32_e32 v189, 16, v189
	s_waitcnt lgkmcnt(2)
	v_pk_add_f32 v[194:195], v[194:195], v[196:197]
	v_add_f32_e32 v196, v215, v211
	s_waitcnt lgkmcnt(1)
	v_add_f32_e32 v192, v192, v210
	v_add_f32_e32 v210, v216, v212
	ds_bpermute_b32 v197, v221, v196
	ds_bpermute_b32 v211, v221, v210
	ds_bpermute_b32 v212, v223, v192
	ds_bpermute_b32 v216, v220, v217
	s_waitcnt lgkmcnt(4)
	v_add_f32_e32 v218, v239, v218
	s_waitcnt lgkmcnt(3)
	v_add_f32_e32 v197, v196, v197
	s_waitcnt lgkmcnt(2)
	v_add_f32_e32 v210, v210, v211
	ds_bpermute_b32 v213, v222, v197
	ds_bpermute_b32 v211, v222, v210
	s_waitcnt lgkmcnt(3)
	v_add_f32_e32 v192, v192, v212
	ds_bpermute_b32 v214, v224, v192
	s_waitcnt lgkmcnt(3)
	v_add_f32_e32 v216, v217, v216
	s_waitcnt lgkmcnt(2)
	v_add_f32_e32 v212, v197, v213
	s_waitcnt lgkmcnt(1)
	v_add_f32_e32 v210, v210, v211
	ds_bpermute_b32 v213, v223, v212
	ds_bpermute_b32 v211, v223, v210
	s_waitcnt lgkmcnt(2)
	v_add_f32_e32 v192, v192, v214
	ds_bpermute_b32 v217, v221, v216
	ds_bpermute_b32 v232, v221, v218
	s_waitcnt lgkmcnt(3)
	v_add_f32_e32 v212, v212, v213
	s_waitcnt lgkmcnt(2)
	v_add_f32_e32 v214, v210, v211
	ds_bpermute_b32 v213, v224, v212
	ds_bpermute_b32 v215, v224, v214
	s_waitcnt lgkmcnt(3)
	v_add_f32_e32 v216, v216, v217
	s_waitcnt lgkmcnt(2)
	v_add_f32_e32 v218, v218, v232
	ds_bpermute_b32 v217, v222, v216
	s_waitcnt lgkmcnt(2)
	v_add_f32_e32 v211, v212, v213
	s_waitcnt lgkmcnt(1)
	v_add_f32_e32 v213, v214, v215
	ds_bpermute_b32 v215, v220, v238
	ds_bpermute_b32 v232, v222, v218
	s_waitcnt lgkmcnt(2)
	v_add_f32_e32 v216, v216, v217
	ds_bpermute_b32 v217, v223, v216
	ds_bpermute_b32 v196, v225, v194
	s_waitcnt lgkmcnt(3)
	v_add_f32_e32 v215, v238, v215
	ds_bpermute_b32 v219, v221, v215
	s_waitcnt lgkmcnt(3)
	v_add_f32_e32 v218, v218, v232
	ds_bpermute_b32 v232, v223, v218
	s_waitcnt lgkmcnt(3)
	v_add_f32_e32 v216, v216, v217
	ds_bpermute_b32 v217, v224, v216
	s_waitcnt lgkmcnt(2)
	v_add_f32_e32 v215, v215, v219
	ds_bpermute_b32 v219, v222, v215
	s_waitcnt lgkmcnt(2)
	v_add_f32_e32 v232, v218, v232
	ds_bpermute_b32 v234, v224, v232
	ds_bpermute_b32 v197, v225, v195
	ds_bpermute_b32 v210, v225, v192
	s_waitcnt lgkmcnt(3)
	v_add_f32_e32 v215, v215, v219
	ds_bpermute_b32 v219, v223, v215
	ds_bpermute_b32 v212, v225, v211
	ds_bpermute_b32 v214, v225, v213
	s_waitcnt lgkmcnt(2)
	v_add_f32_e32 v219, v215, v219
	ds_bpermute_b32 v233, v224, v219
	v_add_f32_e32 v215, v216, v217
	ds_bpermute_b32 v216, v225, v215
	s_waitcnt lgkmcnt(1)
	v_add_f32_e32 v217, v219, v233
	v_add_f32_e32 v219, v232, v234
	ds_bpermute_b32 v218, v225, v217
	ds_bpermute_b32 v232, v225, v219
	v_bfe_u32 v233, v193, 16, 1
	v_add3_u32 v193, v193, v233, s31
	v_and_or_b32 v189, v193, s29, v189
	global_store_dwordx4 v[190:191], v[186:189], off
	s_and_saveexec_b64 s[24:25], s[2:3]
	s_cbranch_execz .LBB0_1232
	v_pk_add_f32 v[188:189], v[194:195], v[196:197]
	v_add_f32_e32 v192, v192, v210
	v_cmp_gt_f32_e32 vcc, v189, v188
	v_add_f32_e32 v211, v211, v212
	v_add_f32_e32 v193, v213, v214
	v_cndmask_b32_e32 v186, v188, v189, vcc
	v_cmp_gt_f32_e64 s[0:1], v192, v186
	s_waitcnt lgkmcnt(2)
	v_add_f32_e32 v191, v215, v216
	s_waitcnt lgkmcnt(1)
	v_add_f32_e32 v190, v217, v218
	v_cndmask_b32_e64 v186, v186, v192, s[0:1]
	v_cmp_gt_f32_e64 s[4:5], v211, v186
	s_waitcnt lgkmcnt(0)
	v_add_f32_e32 v187, v219, v232
	v_cmp_nlg_f32_e64 s[14:15], s34, v188
	v_cndmask_b32_e64 v186, v186, v211, s[4:5]
	v_cmp_gt_f32_e64 s[6:7], v193, v186
	s_nop 1
	v_cndmask_b32_e64 v186, v186, v193, s[6:7]
	v_cmp_gt_f32_e64 s[8:9], v191, v186
	s_nop 1
	v_cndmask_b32_e64 v186, v186, v191, s[8:9]
	v_cmp_gt_f32_e64 s[10:11], v190, v186
	s_nop 1
	v_cndmask_b32_e64 v194, v186, v190, s[10:11]
	v_cndmask_b32_e64 v186, 0, 1, vcc
	v_cndmask_b32_e64 v186, v186, 2, s[0:1]
	v_cndmask_b32_e64 v186, v186, 3, s[4:5]
	v_cndmask_b32_e64 v186, v186, 4, s[6:7]
	v_cndmask_b32_e64 v186, v186, 5, s[8:9]
	v_cndmask_b32_e64 v186, v186, 6, s[10:11]
	v_cmp_ngt_f32_e32 vcc, v187, v194
	s_and_b64 s[16:17], s[10:11], vcc
	s_nop 0
	v_cndmask_b32_e32 v186, 7, v186, vcc
	v_cmp_eq_u32_e64 s[12:13], 0, v186
	s_or_b64 s[12:13], s[12:13], s[14:15]
	v_cmp_ne_u32_e64 s[10:11], 1, v186
	v_cndmask_b32_e64 v188, v188, v231, s[12:13]
	v_cmp_gt_f32_e64 s[14:15], v189, v188
	s_and_b64 s[10:11], s[10:11], s[14:15]
	v_cndmask_b32_e64 v188, v188, v189, s[10:11]
	v_cmp_ne_u32_e64 s[8:9], 2, v186
	v_cmp_gt_f32_e64 s[14:15], v192, v188
	s_and_b64 s[8:9], s[8:9], s[14:15]
	v_cndmask_b32_e64 v188, v188, v192, s[8:9]
	v_cmp_ne_u32_e64 s[6:7], 3, v186
	v_cmp_gt_f32_e64 s[14:15], v211, v188
	s_and_b64 s[6:7], s[6:7], s[14:15]
	v_cndmask_b32_e64 v188, v188, v211, s[6:7]
	v_cmp_ne_u32_e64 s[4:5], 4, v186
	v_cmp_gt_f32_e64 s[14:15], v193, v188
	s_and_b64 s[4:5], s[4:5], s[14:15]
	v_cndmask_b32_e64 v188, v188, v193, s[4:5]
	v_cmp_ne_u32_e64 s[0:1], 5, v186
	v_cmp_gt_f32_e64 s[14:15], v191, v188
	s_and_b64 s[0:1], s[0:1], s[14:15]
	v_cndmask_b32_e64 v188, v188, v191, s[0:1]
	v_cmp_ngt_f32_e64 s[14:15], v190, v188
	s_or_b64 s[14:15], s[16:17], s[14:15]
	v_cndmask_b32_e64 v189, 0, -1, s[12:13]
	v_cndmask_b32_e64 v188, v190, v188, s[14:15]
	v_cmp_gt_f32_e64 s[16:17], v187, v188
	s_and_b64 s[16:17], vcc, s[16:17]
	v_cndmask_b32_e64 v189, v189, 1, s[10:11]
	v_cndmask_b32_e64 v188, v188, v187, s[16:17]
	v_cndmask_b32_e32 v187, v187, v194, vcc
	v_sub_f32_e32 v187, v188, v187
	v_mul_f32_e32 v187, 0x3fb8aa3b, v187
	v_exp_f32_e32 v191, v187
	v_cndmask_b32_e64 v187, v189, 2, s[8:9]
	v_cndmask_b32_e64 v187, v187, 3, s[6:7]
	v_cndmask_b32_e64 v187, v187, 4, s[4:5]
	v_add_f32_e32 v190, 1.0, v191
	v_div_scale_f32 v188, s[4:5], v190, v190, 1.0
	v_rcp_f32_e32 v192, v188
	v_cndmask_b32_e64 v187, v187, 5, s[0:1]
	v_cndmask_b32_e64 v187, 6, v187, s[14:15]
	v_cndmask_b32_e64 v187, v187, 7, s[16:17]
	v_fma_f32 v189, -v188, v192, 1.0
	v_fmac_f32_e32 v192, v189, v192
	v_div_scale_f32 v189, vcc, 1.0, v190, 1.0
	v_mul_f32_e32 v193, v189, v192
	v_fma_f32 v194, -v188, v193, v189
	v_fmac_f32_e32 v193, v194, v192
	v_fma_f32 v194, -v188, v193, v189
	v_lshl_add_u32 v188, v186, 2, 0
	ds_add_rtn_u32 v188, v188, v230
	v_lshl_add_u32 v189, v187, 2, 0
	ds_add_rtn_u32 v189, v189, v230
	v_div_fmas_f32 v192, v194, v192, v193
	v_div_fixup_f32 v190, v192, v190, 1.0
	v_mul_f32_e32 v191, v191, v190
	s_waitcnt lgkmcnt(0)
	ds_write_b128 v226, v[186:189] offset:48
	v_add_u32_e32 v186, 6, v227
	v_ashrrev_i32_e32 v187, 31, v186
	v_lshl_add_u64 v[186:187], v[186:187], 2, s[36:37]
	global_store_dwordx2 v[186:187], v[190:191], off
	s_branch .LBB0_1232

.LBB0_1450:
	s_waitcnt vmcnt(15)
	v_lshlrev_b32_e32 v156, 16, v118
	v_and_b32_e32 v157, 0xffff0000, v118
	v_lshlrev_b32_e32 v118, 16, v119
	v_and_b32_e32 v119, 0xffff0000, v119
	v_lshlrev_b32_e32 v138, 16, v126
	v_and_b32_e32 v139, 0xffff0000, v126
	v_lshlrev_b32_e32 v126, 16, v127
	v_and_b32_e32 v127, 0xffff0000, v127
	v_pk_mul_f32 v[118:119], s[16:17], v[118:119] op_sel_hi:[0,1]
	v_pk_mul_f32 v[156:157], s[16:17], v[156:157] op_sel_hi:[0,1]
	v_pk_fma_f32 v[138:139], v[138:139], s[6:7], v[156:157] op_sel_hi:[1,0,1]
	v_pk_fma_f32 v[118:119], v[126:127], s[6:7], v[118:119] op_sel_hi:[1,0,1]
	s_waitcnt vmcnt(13)
	v_lshlrev_b32_e32 v126, 16, v114
	v_and_b32_e32 v127, 0xffff0000, v114
	v_lshlrev_b32_e32 v114, 16, v115
	v_and_b32_e32 v115, 0xffff0000, v115
	v_pk_fma_f32 v[114:115], s[14:15], v[114:115], v[118:119] op_sel_hi:[0,1,1]
	v_pk_fma_f32 v[118:119], s[14:15], v[126:127], v[138:139] op_sel_hi:[0,1,1]
	v_lshlrev_b32_e32 v126, 16, v120
	v_and_b32_e32 v127, 0xffff0000, v120
	v_lshlrev_b32_e32 v120, 16, v121
	v_and_b32_e32 v121, 0xffff0000, v121
	v_lshlrev_b32_e32 v150, 16, v128
	v_and_b32_e32 v151, 0xffff0000, v128
	v_lshlrev_b32_e32 v128, 16, v129
	v_and_b32_e32 v129, 0xffff0000, v129
	v_pk_mul_f32 v[120:121], s[16:17], v[120:121] op_sel_hi:[0,1]
	v_pk_mul_f32 v[126:127], s[16:17], v[126:127] op_sel_hi:[0,1]
	v_pk_fma_f32 v[126:127], v[150:151], s[6:7], v[126:127] op_sel_hi:[1,0,1]
	v_pk_fma_f32 v[120:121], v[128:129], s[6:7], v[120:121] op_sel_hi:[1,0,1]
	v_lshlrev_b32_e32 v128, 16, v116
	v_and_b32_e32 v129, 0xffff0000, v116
	v_lshlrev_b32_e32 v116, 16, v117
	v_and_b32_e32 v117, 0xffff0000, v117
	v_pk_fma_f32 v[116:117], s[14:15], v[116:117], v[120:121] op_sel_hi:[0,1,1]
	v_pk_fma_f32 v[120:121], s[14:15], v[128:129], v[126:127] op_sel_hi:[0,1,1]
	v_lshlrev_b32_e32 v126, 16, v110
	v_and_b32_e32 v127, 0xffff0000, v110
	v_lshlrev_b32_e32 v110, 16, v111
	v_and_b32_e32 v111, 0xffff0000, v111
	v_lshlrev_b32_e32 v152, 16, v122
	v_and_b32_e32 v153, 0xffff0000, v122
	v_lshlrev_b32_e32 v122, 16, v123
	v_and_b32_e32 v123, 0xffff0000, v123
	v_pk_mul_f32 v[110:111], s[16:17], v[110:111] op_sel_hi:[0,1]
	v_pk_fma_f32 v[110:111], v[122:123], s[6:7], v[110:111] op_sel_hi:[1,0,1]
	s_waitcnt vmcnt(12)
	v_lshlrev_b32_e32 v122, 16, v106
	v_and_b32_e32 v123, 0xffff0000, v106
	v_lshlrev_b32_e32 v106, 16, v107
	v_and_b32_e32 v107, 0xffff0000, v107
	v_pk_fma_f32 v[128:129], s[14:15], v[106:107], v[110:111] op_sel_hi:[0,1,1]
	v_lshlrev_b32_e32 v106, 16, v112
	v_and_b32_e32 v107, 0xffff0000, v112
	v_lshlrev_b32_e32 v110, 16, v113
	v_and_b32_e32 v111, 0xffff0000, v113
	v_lshlrev_b32_e32 v154, 16, v124
	v_and_b32_e32 v155, 0xffff0000, v124
	v_lshlrev_b32_e32 v124, 16, v125
	v_and_b32_e32 v125, 0xffff0000, v125
	v_pk_mul_f32 v[126:127], s[16:17], v[126:127] op_sel_hi:[0,1]
	v_pk_mul_f32 v[110:111], s[16:17], v[110:111] op_sel_hi:[0,1]
	v_pk_mul_f32 v[106:107], s[16:17], v[106:107] op_sel_hi:[0,1]
	v_pk_fma_f32 v[126:127], v[152:153], s[6:7], v[126:127] op_sel_hi:[1,0,1]
	v_pk_fma_f32 v[106:107], v[154:155], s[6:7], v[106:107] op_sel_hi:[1,0,1]
	v_pk_fma_f32 v[110:111], v[124:125], s[6:7], v[110:111] op_sel_hi:[1,0,1]
	v_lshlrev_b32_e32 v112, 16, v108
	v_and_b32_e32 v113, 0xffff0000, v108
	v_lshlrev_b32_e32 v108, 16, v109
	v_and_b32_e32 v109, 0xffff0000, v109
	v_pk_fma_f32 v[122:123], s[14:15], v[122:123], v[126:127] op_sel_hi:[0,1,1]
	v_pk_fma_f32 v[124:125], s[14:15], v[108:109], v[110:111] op_sel_hi:[0,1,1]
	v_pk_fma_f32 v[126:127], s[14:15], v[112:113], v[106:107] op_sel_hi:[0,1,1]
	v_pk_mov_b32 v[106:107], v[118:119], v[114:115] op_sel:[1,0]
	v_mov_b32_e32 v108, v118
	v_mov_b32_e32 v109, v115
	v_pk_add_f32 v[106:107], v[106:107], v[108:109]
	v_pk_mov_b32 v[108:109], v[120:121], v[116:117] op_sel:[1,0]
	v_mov_b32_e32 v110, v120
	v_mov_b32_e32 v111, v117
	v_pk_add_f32 v[108:109], v[108:109], v[110:111]
	v_add_f32_e32 v106, v106, v107
	v_pk_add_f32 v[108:109], v[108:109], v[108:109] op_sel_hi:[0,1]
	v_add_f32_e32 v107, 0, v106
	v_add_f32_e32 v111, v122, v123
	v_add_f32_e32 v113, v128, v129
	v_mov_b32_e32 v110, v126
	v_mov_b32_e32 v112, v127
	v_mov_b32_e32 v108, v124
	v_mov_b32_e32 v106, v125
	v_pk_add_f32 v[110:111], v[110:111], v[112:113]
	v_pk_add_f32 v[106:107], v[108:109], v[106:107]
	s_add_i32 s17, s17, 8
	v_pk_add_f32 v[106:107], v[110:111], v[106:107]
	v_lshl_add_u64 v[136:137], v[136:137], 0, s[2:3]
	v_add_f32_e32 v106, v106, v107
	s_waitcnt lgkmcnt(0)
	s_nop 1
	v_add_f32_dpp v106, v106, v106 quad_perm:[1,0,3,2] row_mask:0xf bank_mask:0xf
	s_nop 1
	v_add_f32_dpp v106, v106, v106 quad_perm:[2,3,0,1] row_mask:0xf bank_mask:0xf
	s_nop 1
	v_add_f32_dpp v106, v106, v106 row_half_mirror row_mask:0xf bank_mask:0xf
	s_nop 1
	v_add_f32_dpp v106, v106, v106 row_mirror row_mask:0xf bank_mask:0xf
	v_mov_b32_e32 v107, v106
	s_nop 1
	v_permlane16_swap_b32_e32 v106, v107
	v_add_f32_e32 v106, v106, v107
	v_mov_b32_e32 v107, v106
	s_nop 1
	v_permlane32_swap_b32_e32 v106, v107
	v_add_f32_e32 v138, v106, v107
	v_fmamk_f32 v119, v138, 0xba800000, v119
	v_fmac_f32_e32 v118, 0xba800000, v138
	v_fmamk_f32 v115, v138, 0xba800000, v115
	v_fmac_f32_e32 v114, 0xba800000, v138
	v_pk_mul_f32 v[106:107], v[114:115], v[114:115]
	v_pk_mul_f32 v[108:109], v[118:119], v[118:119]
	v_fmamk_f32 v121, v138, 0xba800000, v121
	v_pk_mov_b32 v[110:111], v[108:109], v[106:107] op_sel:[1,0]
	v_mov_b32_e32 v109, v107
	v_pk_add_f32 v[106:107], v[110:111], v[108:109]
	v_fmac_f32_e32 v120, 0xba800000, v138
	v_fmamk_f32 v117, v138, 0xba800000, v117
	v_fmac_f32_e32 v116, 0xba800000, v138
	v_pk_add_f32 v[106:107], v[106:107], v[106:107] op_sel_hi:[0,1]
	v_pk_mul_f32 v[108:109], v[116:117], v[116:117]
	v_pk_mul_f32 v[110:111], v[120:121], v[120:121]
	v_fmac_f32_e32 v122, 0xba800000, v138
	v_pk_mov_b32 v[112:113], v[110:111], v[108:109] op_sel:[1,0]
	v_mov_b32_e32 v111, v109
	v_fmamk_f32 v123, v138, 0xba800000, v123
	v_fmac_f32_e32 v128, 0xba800000, v138
	v_mul_f32_e32 v106, v122, v122
	v_pk_add_f32 v[108:109], v[112:113], v[110:111]
	v_fmamk_f32 v129, v138, 0xba800000, v129
	v_pk_fma_f32 v[110:111], v[122:123], v[122:123], v[106:107] op_sel_hi:[1,1,0]
	v_mul_f32_e32 v106, v128, v128
	v_pk_add_f32 v[108:109], v[108:109], v[108:109] op_sel_hi:[0,1]
	v_pk_fma_f32 v[112:113], v[128:129], v[128:129], v[106:107] op_sel_hi:[1,1,0]
	v_fmamk_f32 v125, v138, 0xba800000, v125
	v_fmac_f32_e32 v124, 0xba800000, v138
	v_fmamk_f32 v127, v138, 0xba800000, v127
	v_fmac_f32_e32 v126, 0xba800000, v138
	v_mul_f32_e32 v110, v126, v126
	v_mul_f32_e32 v112, v127, v127
	v_mul_f32_e32 v106, v124, v124
	v_mul_f32_e32 v108, v125, v125
	v_pk_add_f32 v[110:111], v[110:111], v[112:113]
	v_pk_add_f32 v[106:107], v[106:107], v[108:109]
	s_nop 0
	v_pk_add_f32 v[106:107], v[110:111], v[106:107]
	s_nop 0
	v_add_f32_e32 v106, v106, v107
	s_waitcnt lgkmcnt(0)
	s_nop 1
	v_add_f32_dpp v106, v106, v106 quad_perm:[1,0,3,2] row_mask:0xf bank_mask:0xf
	s_nop 1
	v_add_f32_dpp v106, v106, v106 quad_perm:[2,3,0,1] row_mask:0xf bank_mask:0xf
	s_nop 1
	v_add_f32_dpp v106, v106, v106 row_half_mirror row_mask:0xf bank_mask:0xf
	s_nop 1
	v_add_f32_dpp v106, v106, v106 row_mirror row_mask:0xf bank_mask:0xf
	v_mov_b32_e32 v107, v106
	s_nop 1
	v_permlane16_swap_b32_e32 v106, v107
	v_add_f32_e32 v106, v106, v107
	v_mov_b32_e32 v107, v106
	s_nop 1
	v_permlane32_swap_b32_e32 v106, v107
	v_add_f32_e32 v106, v106, v107
	v_fmamk_f32 v106, v106, 0x3a800000, v131
	v_mul_f32_e32 v107, 0x4f800000, v106
	v_cmp_gt_f32_e32 vcc, s18, v106
	s_nop 1
	v_cndmask_b32_e32 v106, v106, v107, vcc
	v_sqrt_f32_e32 v107, v106
	s_nop 0
	v_add_u32_e32 v108, -1, v107
	v_fma_f32 v109, -v108, v107, v106
	v_cmp_ge_f32_e64 s[0:1], 0, v109
	v_add_u32_e32 v109, 1, v107
	s_nop 0
	v_cndmask_b32_e64 v108, v107, v108, s[0:1]
	v_fma_f32 v107, -v109, v107, v106
	v_cmp_lt_f32_e64 s[0:1], 0, v107
	s_nop 1
	v_cndmask_b32_e64 v107, v108, v109, s[0:1]
	v_mul_f32_e32 v108, 0x37800000, v107
	v_cndmask_b32_e32 v107, v107, v108, vcc
	v_cmp_class_f32_e32 vcc, v106, v148
	s_nop 1
	v_cndmask_b32_e32 v106, v107, v106, vcc
	v_div_scale_f32 v107, s[0:1], v106, v106, 1.0
	v_rcp_f32_e32 v108, v107
	s_add_i32 s0, s15, 4
	s_add_i32 s1, s15, -3
	s_cmp_gt_u32 s1, 11
	v_fma_f32 v109, -v107, v108, 1.0
	v_fmac_f32_e32 v108, v109, v108
	v_div_scale_f32 v109, vcc, 1.0, v106, 1.0
	v_mul_f32_e32 v110, v109, v108
	v_fma_f32 v111, -v107, v110, v109
	v_fmac_f32_e32 v110, v111, v108
	v_fma_f32 v107, -v107, v110, v109
	v_div_fmas_f32 v107, v107, v108, v110
	v_div_fixup_f32 v138, v107, v106, 1.0
	v_pk_mul_f32 v[106:107], v[118:119], v[138:139] op_sel_hi:[1,0]
	v_pk_mul_f32 v[108:109], v[114:115], v[138:139] op_sel_hi:[1,0]
	v_pk_mul_f32 v[114:115], v[122:123], v[138:139] op_sel_hi:[1,0]
	v_add_co_u32_e32 v122, vcc, s7, v134
	v_pk_fma_f32 v[108:109], v[4:5], v[108:109], v[8:9]
	v_pk_fma_f32 v[106:107], v[2:3], v[106:107], v[6:7]
	v_pk_mul_f32 v[110:111], v[120:121], v[138:139] op_sel_hi:[1,0]
	v_pk_mul_f32 v[112:113], v[116:117], v[138:139] op_sel_hi:[1,0]
	v_pk_mul_f32 v[116:117], v[128:129], v[138:139] op_sel_hi:[1,0]
	v_pk_mul_f32 v[118:119], v[126:127], v[138:139] op_sel_hi:[1,0]
	v_pk_mul_f32 v[120:121], v[124:125], v[138:139] op_sel_hi:[1,0]
	v_addc_co_u32_e32 v123, vcc, 0, v135, vcc
	v_lshl_add_u64 v[134:135], v[134:135], 0, s[12:13]
	s_mov_b32 s15, s0
	v_pk_fma_f32 v[112:113], v[16:17], v[112:113], v[28:29]
	v_pk_fma_f32 v[110:111], v[14:15], v[110:111], v[26:27]
	v_pk_fma_f32 v[116:117], v[20:21], v[116:117], v[32:33]
	v_pk_fma_f32 v[114:115], v[18:19], v[114:115], v[30:31]
	v_pk_fma_f32 v[120:121], v[12:13], v[120:121], v[24:25]
	v_pk_fma_f32 v[118:119], v[10:11], v[118:119], v[22:23]
	global_store_dwordx4 v[122:123], v[106:109], off nt
	global_store_dwordx4 v[122:123], v[110:113], off offset:16 nt
	global_store_dwordx4 v[122:123], v[114:117], off offset:2048 nt
	global_store_dwordx4 v[122:123], v[118:121], off offset:2064 nt
	s_cbranch_scc1 .LBB0_1457
.LBB0_1451:
	s_waitcnt vmcnt(15)
	v_lshlrev_b32_e32 v122, 16, v50
	v_and_b32_e32 v123, 0xffff0000, v50
	v_lshlrev_b32_e32 v124, 16, v51
	v_and_b32_e32 v125, 0xffff0000, v51
	v_lshlrev_b32_e32 v106, 16, v34
	v_and_b32_e32 v107, 0xffff0000, v34
	v_lshlrev_b32_e32 v108, 16, v35
	v_and_b32_e32 v109, 0xffff0000, v35
	v_pk_mul_f32 v[124:125], s[4:5], v[124:125] op_sel_hi:[0,1]
	v_pk_mul_f32 v[122:123], s[4:5], v[122:123] op_sel_hi:[0,1]
	v_pk_fma_f32 v[106:107], v[106:107], s[6:7], v[122:123] op_sel_hi:[1,0,1]
	v_pk_fma_f32 v[108:109], v[108:109], s[6:7], v[124:125] op_sel_hi:[1,0,1]
	s_waitcnt vmcnt(13)
	v_lshlrev_b32_e32 v122, 16, v58
	v_and_b32_e32 v123, 0xffff0000, v58
	v_lshlrev_b32_e32 v124, 16, v59
	v_and_b32_e32 v125, 0xffff0000, v59
	v_pk_fma_f32 v[138:139], s[4:5], v[124:125], v[108:109] op_sel:[1,0,0]
	v_pk_fma_f32 v[150:151], s[4:5], v[122:123], v[106:107] op_sel:[1,0,0]
	v_lshlrev_b32_e32 v106, 16, v52
	v_and_b32_e32 v107, 0xffff0000, v52
	v_lshlrev_b32_e32 v108, 16, v53
	v_and_b32_e32 v109, 0xffff0000, v53
	v_lshlrev_b32_e32 v110, 16, v36
	v_and_b32_e32 v111, 0xffff0000, v36
	v_lshlrev_b32_e32 v112, 16, v37
	v_and_b32_e32 v113, 0xffff0000, v37
	v_pk_mul_f32 v[108:109], s[4:5], v[108:109] op_sel_hi:[0,1]
	v_pk_mul_f32 v[106:107], s[4:5], v[106:107] op_sel_hi:[0,1]
	v_pk_fma_f32 v[106:107], v[110:111], s[6:7], v[106:107] op_sel_hi:[1,0,1]
	v_pk_fma_f32 v[108:109], v[112:113], s[6:7], v[108:109] op_sel_hi:[1,0,1]
	v_lshlrev_b32_e32 v110, 16, v60
	v_and_b32_e32 v111, 0xffff0000, v60
	v_lshlrev_b32_e32 v112, 16, v61
	v_and_b32_e32 v113, 0xffff0000, v61
	v_pk_fma_f32 v[154:155], s[4:5], v[112:113], v[108:109] op_sel:[1,0,0]
	v_pk_fma_f32 v[156:157], s[4:5], v[110:111], v[106:107] op_sel:[1,0,0]
	v_lshlrev_b32_e32 v106, 16, v54
	v_and_b32_e32 v107, 0xffff0000, v54
	v_lshlrev_b32_e32 v108, 16, v55
	v_and_b32_e32 v109, 0xffff0000, v55
	v_lshlrev_b32_e32 v114, 16, v38
	v_and_b32_e32 v115, 0xffff0000, v38
	v_lshlrev_b32_e32 v116, 16, v39
	v_and_b32_e32 v117, 0xffff0000, v39
	v_pk_mul_f32 v[108:109], s[4:5], v[108:109] op_sel_hi:[0,1]
	v_pk_mul_f32 v[106:107], s[4:5], v[106:107] op_sel_hi:[0,1]
	v_pk_fma_f32 v[106:107], v[114:115], s[6:7], v[106:107] op_sel_hi:[1,0,1]
	v_pk_fma_f32 v[108:109], v[116:117], s[6:7], v[108:109] op_sel_hi:[1,0,1]
	s_waitcnt vmcnt(12)
	v_lshlrev_b32_e32 v110, 16, v62
	v_and_b32_e32 v111, 0xffff0000, v62
	v_lshlrev_b32_e32 v112, 16, v63
	v_and_b32_e32 v113, 0xffff0000, v63
	v_pk_fma_f32 v[158:159], s[4:5], v[112:113], v[108:109] op_sel:[1,0,0]
	v_pk_fma_f32 v[160:161], s[4:5], v[110:111], v[106:107] op_sel:[1,0,0]
	v_lshlrev_b32_e32 v106, 16, v56
	v_and_b32_e32 v107, 0xffff0000, v56
	v_lshlrev_b32_e32 v108, 16, v57
	v_and_b32_e32 v109, 0xffff0000, v57
	v_lshlrev_b32_e32 v118, 16, v40
	v_and_b32_e32 v119, 0xffff0000, v40
	v_lshlrev_b32_e32 v120, 16, v41
	v_and_b32_e32 v121, 0xffff0000, v41
	v_pk_mul_f32 v[108:109], s[4:5], v[108:109] op_sel_hi:[0,1]
	v_pk_mul_f32 v[106:107], s[4:5], v[106:107] op_sel_hi:[0,1]
	v_pk_fma_f32 v[106:107], v[118:119], s[6:7], v[106:107] op_sel_hi:[1,0,1]
	v_pk_fma_f32 v[108:109], v[120:121], s[6:7], v[108:109] op_sel_hi:[1,0,1]
	v_lshlrev_b32_e32 v110, 16, v64
	v_and_b32_e32 v111, 0xffff0000, v64
	v_lshlrev_b32_e32 v112, 16, v65
	v_and_b32_e32 v113, 0xffff0000, v65
	v_pk_fma_f32 v[162:163], s[4:5], v[112:113], v[108:109] op_sel:[1,0,0]
	v_pk_fma_f32 v[164:165], s[4:5], v[110:111], v[106:107] op_sel:[1,0,0]
	v_pk_mov_b32 v[106:107], v[150:151], v[138:139] op_sel:[1,0]
	v_mov_b32_e32 v108, v150
	v_mov_b32_e32 v109, v139
	v_pk_add_f32 v[106:107], v[106:107], v[108:109]
	v_pk_mov_b32 v[108:109], v[156:157], v[154:155] op_sel:[1,0]
	v_mov_b32_e32 v110, v156
	v_mov_b32_e32 v111, v155
	v_pk_add_f32 v[108:109], v[108:109], v[110:111]
	v_add_f32_e32 v106, v106, v107
	v_pk_add_f32 v[108:109], v[108:109], v[108:109] op_sel_hi:[0,1]
	v_add_f32_e32 v107, 0, v106
	v_add_f32_e32 v111, v160, v161
	v_add_f32_e32 v113, v158, v159
	v_mov_b32_e32 v110, v164
	v_mov_b32_e32 v112, v165
	v_mov_b32_e32 v108, v162
	v_mov_b32_e32 v106, v163
	v_pk_add_f32 v[110:111], v[110:111], v[112:113]
	v_pk_add_f32 v[106:107], v[108:109], v[106:107]
	s_add_i32 s14, s17, -7
	v_pk_add_f32 v[106:107], v[110:111], v[106:107]
	v_readlane_b32 s0, v141, s14
	v_add_f32_e32 v106, v106, v107
	ds_bpermute_b32 v107, v142, v106
	s_add_i32 s22, s17, -6
	v_readlane_b32 s20, v141, s22
	s_ashr_i32 s1, s0, 31
	s_lshl_b64 s[0:1], s[0:1], 11
	s_waitcnt lgkmcnt(0)
	v_add_f32_e32 v106, v106, v107
	ds_bpermute_b32 v107, v143, v106
	s_ashr_i32 s21, s20, 31
	global_load_dwordx4 v[126:129], v[136:137], off nt
	global_load_dwordx4 v[122:125], v[136:137], off offset:1024 nt
	v_readlane_b32 s16, v140, s14
	v_readlane_b32 s14, v140, s22
	s_waitcnt lgkmcnt(0)
	v_add_f32_e32 v106, v106, v107
	ds_bpermute_b32 v107, v144, v106
	s_waitcnt lgkmcnt(0)
	v_add_f32_e32 v106, v106, v107
	ds_bpermute_b32 v107, v145, v106
	s_waitcnt lgkmcnt(0)
	v_add_f32_e32 v106, v106, v107
	ds_bpermute_b32 v107, v146, v106
	s_waitcnt lgkmcnt(0)
	v_add_f32_e32 v106, v106, v107
	ds_bpermute_b32 v107, v147, v106
	s_waitcnt lgkmcnt(0)
	v_add_f32_e32 v114, v106, v107
	v_fmamk_f32 v151, v114, 0xba800000, v151
	v_fmac_f32_e32 v150, 0xba800000, v114
	v_fmamk_f32 v139, v114, 0xba800000, v139
	v_fmac_f32_e32 v138, 0xba800000, v114
	v_pk_mul_f32 v[106:107], v[138:139], v[138:139]
	v_pk_mul_f32 v[108:109], v[150:151], v[150:151]
	v_fmamk_f32 v157, v114, 0xba800000, v157
	v_pk_mov_b32 v[110:111], v[108:109], v[106:107] op_sel:[1,0]
	v_mov_b32_e32 v109, v107
	v_pk_add_f32 v[106:107], v[110:111], v[108:109]
	v_fmac_f32_e32 v156, 0xba800000, v114
	v_fmamk_f32 v155, v114, 0xba800000, v155
	v_fmac_f32_e32 v154, 0xba800000, v114
	v_pk_add_f32 v[106:107], v[106:107], v[106:107] op_sel_hi:[0,1]
	v_pk_mul_f32 v[108:109], v[154:155], v[154:155]
	v_pk_mul_f32 v[110:111], v[156:157], v[156:157]
	v_fmac_f32_e32 v160, 0xba800000, v114
	v_pk_mov_b32 v[112:113], v[110:111], v[108:109] op_sel:[1,0]
	v_mov_b32_e32 v111, v109
	v_fmamk_f32 v161, v114, 0xba800000, v161
	v_fmac_f32_e32 v158, 0xba800000, v114
	v_mul_f32_e32 v106, v160, v160
	v_pk_add_f32 v[108:109], v[112:113], v[110:111]
	v_fmamk_f32 v159, v114, 0xba800000, v159
	v_pk_fma_f32 v[110:111], v[160:161], v[160:161], v[106:107] op_sel_hi:[1,1,0]
	v_mul_f32_e32 v106, v158, v158
	v_pk_add_f32 v[108:109], v[108:109], v[108:109] op_sel_hi:[0,1]
	v_pk_fma_f32 v[112:113], v[158:159], v[158:159], v[106:107] op_sel_hi:[1,1,0]
	v_fmamk_f32 v163, v114, 0xba800000, v163
	v_fmac_f32_e32 v162, 0xba800000, v114
	v_fmamk_f32 v165, v114, 0xba800000, v165
	v_fmac_f32_e32 v164, 0xba800000, v114
	v_mul_f32_e32 v110, v164, v164
	v_mul_f32_e32 v112, v165, v165
	v_mul_f32_e32 v106, v162, v162
	v_mul_f32_e32 v108, v163, v163
	v_pk_add_f32 v[110:111], v[110:111], v[112:113]
	v_pk_add_f32 v[106:107], v[106:107], v[108:109]
	s_nop 0
	v_pk_add_f32 v[106:107], v[110:111], v[106:107]
	s_nop 0
	v_add_f32_e32 v106, v106, v107
	s_waitcnt lgkmcnt(0)
	s_nop 1
	v_add_f32_dpp v106, v106, v106 quad_perm:[1,0,3,2] row_mask:0xf bank_mask:0xf
	s_nop 1
	v_add_f32_dpp v108, v106, v106 quad_perm:[2,3,0,1] row_mask:0xf bank_mask:0xf
	ds_bpermute_b32 v109, v144, v108
	v_lshl_add_u64 v[106:107], v[132:133], 0, s[0:1]
	s_lshl_b64 s[0:1], s[20:21], 11
	global_load_dwordx4 v[118:121], v[106:107], off nt
	global_load_dwordx4 v[110:113], v[106:107], off offset:1024 nt
	s_waitcnt lgkmcnt(0)
	v_add_f32_e32 v114, v108, v109
	ds_bpermute_b32 v115, v145, v114
	v_lshl_add_u64 v[108:109], v[132:133], 0, s[0:1]
	s_waitcnt lgkmcnt(0)
	v_add_f32_e32 v149, v114, v115
	global_load_dwordx4 v[114:117], v[108:109], off nt
	s_nop 0
	global_load_dwordx4 v[106:109], v[108:109], off offset:1024 nt
	ds_bpermute_b32 v152, v146, v149
	s_waitcnt lgkmcnt(0)
	v_add_f32_e32 v149, v149, v152
	ds_bpermute_b32 v152, v147, v149
	s_waitcnt lgkmcnt(0)
	v_add_f32_e32 v149, v149, v152
	v_fmamk_f32 v149, v149, 0x3a800000, v131
	v_mul_f32_e32 v152, 0x4f800000, v149
	v_cmp_gt_f32_e32 vcc, s18, v149
	s_nop 1
	v_cndmask_b32_e32 v149, v149, v152, vcc
	v_sqrt_f32_e32 v152, v149
	s_nop 0
	v_add_u32_e32 v153, -1, v152
	v_fma_f32 v166, -v153, v152, v149
	v_cmp_ge_f32_e64 s[0:1], 0, v166
	v_add_u32_e32 v166, 1, v152
	s_nop 0
	v_cndmask_b32_e64 v153, v152, v153, s[0:1]
	v_fma_f32 v152, -v166, v152, v149
	v_cmp_lt_f32_e64 s[0:1], 0, v152
	s_nop 1
	v_cndmask_b32_e64 v152, v153, v166, s[0:1]
	v_mul_f32_e32 v153, 0x37800000, v152
	v_cndmask_b32_e32 v152, v152, v153, vcc
	v_cmp_class_f32_e32 vcc, v149, v148
	s_nop 1
	v_cndmask_b32_e32 v149, v152, v149, vcc
	v_div_scale_f32 v152, s[0:1], v149, v149, 1.0
	v_rcp_f32_e32 v153, v152
	s_add_i32 s0, s15, -2
	s_cmp_gt_u32 s0, 12
	v_fma_f32 v166, -v152, v153, 1.0
	v_fmac_f32_e32 v153, v166, v153
	v_div_scale_f32 v166, vcc, 1.0, v149, 1.0
	v_mul_f32_e32 v167, v166, v153
	v_fma_f32 v168, -v152, v167, v166
	v_fmac_f32_e32 v167, v168, v153
	v_fma_f32 v152, -v152, v167, v166
	v_div_fmas_f32 v152, v152, v153, v167
	v_div_fixup_f32 v166, v152, v149, 1.0
	v_pk_mul_f32 v[138:139], v[138:139], v[166:167] op_sel_hi:[1,0]
	v_pk_mul_f32 v[154:155], v[154:155], v[166:167] op_sel_hi:[1,0]
	v_pk_fma_f32 v[152:153], v[4:5], v[138:139], v[8:9]
	v_pk_mul_f32 v[138:139], v[156:157], v[166:167] op_sel_hi:[1,0]
	v_pk_fma_f32 v[156:157], v[16:17], v[154:155], v[28:29]
	v_pk_fma_f32 v[154:155], v[14:15], v[138:139], v[26:27]
	v_pk_mul_f32 v[138:139], v[160:161], v[166:167] op_sel_hi:[1,0]
	v_pk_mul_f32 v[158:159], v[158:159], v[166:167] op_sel_hi:[1,0]
	v_pk_mul_f32 v[162:163], v[162:163], v[166:167] op_sel_hi:[1,0]
	v_pk_fma_f32 v[160:161], v[20:21], v[158:159], v[32:33]
	v_pk_fma_f32 v[158:159], v[18:19], v[138:139], v[30:31]
	v_pk_mul_f32 v[138:139], v[164:165], v[166:167] op_sel_hi:[1,0]
	v_pk_mul_f32 v[150:151], v[150:151], v[166:167] op_sel_hi:[1,0]
	v_pk_fma_f32 v[164:165], v[12:13], v[162:163], v[24:25]
	v_pk_fma_f32 v[162:163], v[10:11], v[138:139], v[22:23]
	v_add_co_u32_e32 v138, vcc, s19, v134
	v_pk_fma_f32 v[150:151], v[2:3], v[150:151], v[6:7]
	s_nop 0
	v_addc_co_u32_e32 v139, vcc, -1, v135, vcc
	global_store_dwordx4 v[138:139], v[150:153], off nt
	v_add_co_u32_e32 v138, vcc, 0xfffff000, v134
	s_nop 1
	v_addc_co_u32_e32 v139, vcc, -1, v135, vcc
	global_store_dwordx4 v[138:139], v[154:157], off offset:-4080 nt
	global_store_dwordx4 v[138:139], v[158:161], off offset:-2048 nt
	global_store_dwordx4 v[138:139], v[162:165], off offset:-2032 nt
	s_cbranch_scc1 .LBB0_1453
	s_add_i32 s20, s17, -5
	v_readlane_b32 s0, v141, s20
	s_add_i32 s21, s17, -4
	v_add3_u32 v34, v130, s15, 1
	v_readlane_b32 s4, v141, s21
	s_ashr_i32 s1, s0, 31
	v_ashrrev_i32_e32 v35, 31, v34
	s_lshl_b64 s[0:1], s[0:1], 11
	s_ashr_i32 s5, s4, 31
	v_lshlrev_b64 v[34:35], 11, v[34:35]
	v_lshl_add_u64 v[54:55], v[132:133], 0, s[0:1]
	s_lshl_b64 s[0:1], s[4:5], 11
	v_lshl_add_u64 v[38:39], v[0:1], 0, v[34:35]
	v_lshl_add_u64 v[62:63], v[132:133], 0, s[0:1]
	global_load_dwordx4 v[34:37], v[38:39], off nt
	s_nop 0
	global_load_dwordx4 v[38:41], v[38:39], off offset:1024 nt
	s_nop 0
	global_load_dwordx4 v[50:53], v[54:55], off nt
	s_nop 0
	global_load_dwordx4 v[54:57], v[54:55], off offset:1024 nt
	s_nop 0
	global_load_dwordx4 v[58:61], v[62:63], off nt
	s_nop 0
	global_load_dwordx4 v[62:65], v[62:63], off offset:1024 nt
	v_readlane_b32 s4, v140, s20
	v_readlane_b32 s5, v140, s21
.LBB0_1453:
	s_waitcnt vmcnt(19)
	v_lshlrev_b32_e32 v164, 16, v74
	v_and_b32_e32 v165, 0xffff0000, v74
	v_lshlrev_b32_e32 v166, 16, v75
	v_and_b32_e32 v167, 0xffff0000, v75
	v_lshlrev_b32_e32 v138, 16, v42
	v_and_b32_e32 v139, 0xffff0000, v42
	v_lshlrev_b32_e32 v150, 16, v43
	v_and_b32_e32 v151, 0xffff0000, v43
	v_pk_mul_f32 v[166:167], s[8:9], v[166:167] op_sel_hi:[0,1]
	v_pk_mul_f32 v[164:165], s[8:9], v[164:165] op_sel_hi:[0,1]
	v_pk_fma_f32 v[138:139], v[138:139], s[6:7], v[164:165] op_sel_hi:[1,0,1]
	v_pk_fma_f32 v[150:151], v[150:151], s[6:7], v[166:167] op_sel_hi:[1,0,1]
	s_waitcnt vmcnt(17)
	v_lshlrev_b32_e32 v164, 16, v82
	v_and_b32_e32 v165, 0xffff0000, v82
	v_lshlrev_b32_e32 v166, 16, v83
	v_and_b32_e32 v167, 0xffff0000, v83
	v_pk_fma_f32 v[150:151], s[8:9], v[166:167], v[150:151] op_sel:[1,0,0]
	v_pk_fma_f32 v[138:139], s[8:9], v[164:165], v[138:139] op_sel:[1,0,0]
	v_lshlrev_b32_e32 v164, 16, v76
	v_and_b32_e32 v165, 0xffff0000, v76
	v_lshlrev_b32_e32 v166, 16, v77
	v_and_b32_e32 v167, 0xffff0000, v77
	v_lshlrev_b32_e32 v152, 16, v44
	v_and_b32_e32 v153, 0xffff0000, v44
	v_lshlrev_b32_e32 v154, 16, v45
	v_and_b32_e32 v155, 0xffff0000, v45
	v_pk_mul_f32 v[166:167], s[8:9], v[166:167] op_sel_hi:[0,1]
	v_pk_mul_f32 v[164:165], s[8:9], v[164:165] op_sel_hi:[0,1]
	v_pk_fma_f32 v[152:153], v[152:153], s[6:7], v[164:165] op_sel_hi:[1,0,1]
	v_pk_fma_f32 v[154:155], v[154:155], s[6:7], v[166:167] op_sel_hi:[1,0,1]
	v_lshlrev_b32_e32 v164, 16, v84
	v_and_b32_e32 v165, 0xffff0000, v84
	v_lshlrev_b32_e32 v166, 16, v85
	v_and_b32_e32 v167, 0xffff0000, v85
	v_pk_fma_f32 v[154:155], s[8:9], v[166:167], v[154:155] op_sel:[1,0,0]
	v_pk_fma_f32 v[164:165], s[8:9], v[164:165], v[152:153] op_sel:[1,0,0]
	v_lshlrev_b32_e32 v152, 16, v78
	v_and_b32_e32 v153, 0xffff0000, v78
	v_lshlrev_b32_e32 v166, 16, v79
	v_and_b32_e32 v167, 0xffff0000, v79
	v_lshlrev_b32_e32 v156, 16, v46
	v_and_b32_e32 v157, 0xffff0000, v46
	v_lshlrev_b32_e32 v158, 16, v47
	v_and_b32_e32 v159, 0xffff0000, v47
	v_pk_mul_f32 v[166:167], s[8:9], v[166:167] op_sel_hi:[0,1]
	v_pk_mul_f32 v[152:153], s[8:9], v[152:153] op_sel_hi:[0,1]
	v_pk_fma_f32 v[152:153], v[156:157], s[6:7], v[152:153] op_sel_hi:[1,0,1]
	v_pk_fma_f32 v[156:157], v[158:159], s[6:7], v[166:167] op_sel_hi:[1,0,1]
	s_waitcnt vmcnt(16)
	v_lshlrev_b32_e32 v158, 16, v86
	v_and_b32_e32 v159, 0xffff0000, v86
	v_lshlrev_b32_e32 v166, 16, v87
	v_and_b32_e32 v167, 0xffff0000, v87
	v_pk_fma_f32 v[166:167], s[8:9], v[166:167], v[156:157] op_sel:[1,0,0]
	v_pk_fma_f32 v[158:159], s[8:9], v[158:159], v[152:153] op_sel:[1,0,0]
	v_lshlrev_b32_e32 v152, 16, v80
	v_and_b32_e32 v153, 0xffff0000, v80
	v_lshlrev_b32_e32 v156, 16, v81
	v_and_b32_e32 v157, 0xffff0000, v81
	v_lshlrev_b32_e32 v160, 16, v48
	v_and_b32_e32 v161, 0xffff0000, v48
	v_lshlrev_b32_e32 v162, 16, v49
	v_and_b32_e32 v163, 0xffff0000, v49
	v_pk_mul_f32 v[156:157], s[8:9], v[156:157] op_sel_hi:[0,1]
	v_pk_mul_f32 v[152:153], s[8:9], v[152:153] op_sel_hi:[0,1]
	v_pk_fma_f32 v[152:153], v[160:161], s[6:7], v[152:153] op_sel_hi:[1,0,1]
	v_pk_fma_f32 v[156:157], v[162:163], s[6:7], v[156:157] op_sel_hi:[1,0,1]
	v_lshlrev_b32_e32 v160, 16, v88
	v_and_b32_e32 v161, 0xffff0000, v88
	v_lshlrev_b32_e32 v162, 16, v89
	v_and_b32_e32 v163, 0xffff0000, v89
	v_pk_fma_f32 v[162:163], s[8:9], v[162:163], v[156:157] op_sel:[1,0,0]
	v_pk_fma_f32 v[168:169], s[8:9], v[160:161], v[152:153] op_sel:[1,0,0]
	v_pk_mov_b32 v[152:153], v[138:139], v[150:151] op_sel:[1,0]
	v_mov_b32_e32 v156, v138
	v_mov_b32_e32 v157, v151
	v_pk_add_f32 v[152:153], v[152:153], v[156:157]
	v_pk_mov_b32 v[156:157], v[164:165], v[154:155] op_sel:[1,0]
	v_mov_b32_e32 v160, v164
	v_mov_b32_e32 v161, v155
	v_pk_add_f32 v[156:157], v[156:157], v[160:161]
	v_add_f32_e32 v149, v152, v153
	v_pk_add_f32 v[156:157], v[156:157], v[156:157] op_sel_hi:[0,1]
	v_add_f32_e32 v153, 0, v149
	v_add_f32_e32 v161, v158, v159
	v_add_f32_e32 v171, v166, v167
	v_mov_b32_e32 v160, v168
	v_mov_b32_e32 v170, v169
	v_mov_b32_e32 v156, v162
	v_mov_b32_e32 v152, v163
	v_pk_add_f32 v[160:161], v[160:161], v[170:171]
	v_pk_add_f32 v[152:153], v[156:157], v[152:153]
	s_nop 0
	v_pk_add_f32 v[152:153], v[160:161], v[152:153]
	s_nop 0
	v_add_f32_e32 v149, v152, v153
	s_waitcnt lgkmcnt(0)
	s_nop 1
	v_add_f32_dpp v149, v149, v149 quad_perm:[1,0,3,2] row_mask:0xf bank_mask:0xf
	s_nop 1
	v_add_f32_dpp v149, v149, v149 quad_perm:[2,3,0,1] row_mask:0xf bank_mask:0xf
	s_nop 1
	v_add_f32_dpp v149, v149, v149 row_half_mirror row_mask:0xf bank_mask:0xf
	s_nop 1
	v_add_f32_dpp v149, v149, v149 row_mirror row_mask:0xf bank_mask:0xf
	v_mov_b32_e32 v152, v149
	s_nop 1
	v_permlane16_swap_b32_e32 v149, v152
	v_add_f32_e32 v149, v149, v152
	v_mov_b32_e32 v152, v149
	s_nop 1
	v_permlane32_swap_b32_e32 v149, v152
	v_add_f32_e32 v149, v149, v152
	v_fmamk_f32 v139, v149, 0xba800000, v139
	v_fmac_f32_e32 v138, 0xba800000, v149
	v_fmamk_f32 v151, v149, 0xba800000, v151
	v_fmac_f32_e32 v150, 0xba800000, v149
	v_pk_mul_f32 v[152:153], v[150:151], v[150:151]
	v_pk_mul_f32 v[156:157], v[138:139], v[138:139]
	v_fmamk_f32 v165, v149, 0xba800000, v165
	v_pk_mov_b32 v[160:161], v[156:157], v[152:153] op_sel:[1,0]
	v_mov_b32_e32 v157, v153
	v_pk_add_f32 v[152:153], v[160:161], v[156:157]
	v_fmac_f32_e32 v164, 0xba800000, v149
	v_fmamk_f32 v155, v149, 0xba800000, v155
	v_fmac_f32_e32 v154, 0xba800000, v149
	v_pk_add_f32 v[152:153], v[152:153], v[152:153] op_sel_hi:[0,1]
	v_pk_mul_f32 v[156:157], v[154:155], v[154:155]
	v_pk_mul_f32 v[160:161], v[164:165], v[164:165]
	v_fmac_f32_e32 v158, 0xba800000, v149
	v_pk_mov_b32 v[170:171], v[160:161], v[156:157] op_sel:[1,0]
	v_mov_b32_e32 v161, v157
	v_fmamk_f32 v159, v149, 0xba800000, v159
	v_fmac_f32_e32 v166, 0xba800000, v149
	v_mul_f32_e32 v152, v158, v158
	v_pk_add_f32 v[156:157], v[170:171], v[160:161]
	v_fmamk_f32 v167, v149, 0xba800000, v167
	v_pk_fma_f32 v[160:161], v[158:159], v[158:159], v[152:153] op_sel_hi:[1,1,0]
	v_mul_f32_e32 v152, v166, v166
	v_pk_add_f32 v[156:157], v[156:157], v[156:157] op_sel_hi:[0,1]
	v_pk_fma_f32 v[170:171], v[166:167], v[166:167], v[152:153] op_sel_hi:[1,1,0]
	v_fmamk_f32 v163, v149, 0xba800000, v163
	v_fmac_f32_e32 v162, 0xba800000, v149
	v_fmamk_f32 v169, v149, 0xba800000, v169
	v_fmac_f32_e32 v168, 0xba800000, v149
	v_mul_f32_e32 v160, v168, v168
	v_mul_f32_e32 v170, v169, v169
	v_mul_f32_e32 v152, v162, v162
	v_mul_f32_e32 v156, v163, v163
	v_pk_add_f32 v[160:161], v[160:161], v[170:171]
	v_pk_add_f32 v[152:153], v[152:153], v[156:157]
	s_nop 0
	v_pk_add_f32 v[152:153], v[160:161], v[152:153]
	s_nop 0
	v_add_f32_e32 v149, v152, v153
	s_waitcnt lgkmcnt(0)
	s_nop 1
	v_add_f32_dpp v149, v149, v149 quad_perm:[1,0,3,2] row_mask:0xf bank_mask:0xf
	s_nop 1
	v_add_f32_dpp v149, v149, v149 quad_perm:[2,3,0,1] row_mask:0xf bank_mask:0xf
	s_nop 1
	v_add_f32_dpp v149, v149, v149 row_half_mirror row_mask:0xf bank_mask:0xf
	s_nop 1
	v_add_f32_dpp v149, v149, v149 row_mirror row_mask:0xf bank_mask:0xf
	v_mov_b32_e32 v152, v149
	s_nop 1
	v_permlane16_swap_b32_e32 v149, v152
	v_add_f32_e32 v149, v149, v152
	v_mov_b32_e32 v152, v149
	s_nop 1
	v_permlane32_swap_b32_e32 v149, v152
	v_add_f32_e32 v149, v149, v152
	v_fmamk_f32 v149, v149, 0x3a800000, v131
	v_mul_f32_e32 v152, 0x4f800000, v149
	v_cmp_gt_f32_e32 vcc, s18, v149
	s_nop 1
	v_cndmask_b32_e32 v149, v149, v152, vcc
	v_sqrt_f32_e32 v152, v149
	s_nop 0
	v_add_u32_e32 v153, -1, v152
	v_fma_f32 v156, -v153, v152, v149
	v_cmp_ge_f32_e64 s[0:1], 0, v156
	v_add_u32_e32 v156, 1, v152
	s_nop 0
	v_cndmask_b32_e64 v153, v152, v153, s[0:1]
	v_fma_f32 v152, -v156, v152, v149
	v_cmp_lt_f32_e64 s[0:1], 0, v152
	s_nop 1
	v_cndmask_b32_e64 v152, v153, v156, s[0:1]
	v_mul_f32_e32 v153, 0x37800000, v152
	v_cndmask_b32_e32 v152, v152, v153, vcc
	v_cmp_class_f32_e32 vcc, v149, v148
	s_nop 1
	v_cndmask_b32_e32 v149, v152, v149, vcc
	v_div_scale_f32 v152, s[0:1], v149, v149, 1.0
	v_rcp_f32_e32 v153, v152
	s_add_i32 s0, s15, -1
	s_cmp_gt_u32 s0, 12
	v_fma_f32 v156, -v152, v153, 1.0
	v_fmac_f32_e32 v153, v156, v153
	v_div_scale_f32 v156, vcc, 1.0, v149, 1.0
	v_mul_f32_e32 v157, v156, v153
	v_fma_f32 v160, -v152, v157, v156
	v_fmac_f32_e32 v157, v160, v153
	v_fma_f32 v152, -v152, v157, v156
	v_div_fmas_f32 v152, v152, v153, v157
	v_div_fixup_f32 v170, v152, v149, 1.0
	v_pk_mul_f32 v[138:139], v[138:139], v[170:171] op_sel_hi:[1,0]
	v_pk_mul_f32 v[150:151], v[150:151], v[170:171] op_sel_hi:[1,0]
	v_pk_mul_f32 v[154:155], v[154:155], v[170:171] op_sel_hi:[1,0]
	v_pk_fma_f32 v[152:153], v[4:5], v[150:151], v[8:9]
	v_pk_fma_f32 v[150:151], v[2:3], v[138:139], v[6:7]
	v_pk_mul_f32 v[138:139], v[164:165], v[170:171] op_sel_hi:[1,0]
	v_pk_fma_f32 v[156:157], v[16:17], v[154:155], v[28:29]
	v_pk_fma_f32 v[154:155], v[14:15], v[138:139], v[26:27]
	v_pk_mul_f32 v[138:139], v[158:159], v[170:171] op_sel_hi:[1,0]
	v_pk_mul_f32 v[158:159], v[166:167], v[170:171] op_sel_hi:[1,0]
	v_pk_mul_f32 v[162:163], v[162:163], v[170:171] op_sel_hi:[1,0]
	v_pk_fma_f32 v[160:161], v[20:21], v[158:159], v[32:33]
	v_pk_fma_f32 v[158:159], v[18:19], v[138:139], v[30:31]
	v_pk_mul_f32 v[138:139], v[168:169], v[170:171] op_sel_hi:[1,0]
	v_pk_fma_f32 v[164:165], v[12:13], v[162:163], v[24:25]
	v_pk_fma_f32 v[162:163], v[10:11], v[138:139], v[22:23]
	global_store_dwordx4 v[134:135], v[150:153], off offset:-4096 nt
	global_store_dwordx4 v[134:135], v[154:157], off offset:-4080 nt
	global_store_dwordx4 v[134:135], v[158:161], off offset:-2048 nt
	global_store_dwordx4 v[134:135], v[162:165], off offset:-2032 nt
	s_cbranch_scc1 .LBB0_1455
	s_add_i32 s20, s17, -3
	v_readlane_b32 s0, v141, s20
	s_add_i32 s21, s17, -2
	v_add3_u32 v42, v130, s15, 2
	v_readlane_b32 s8, v141, s21
	s_ashr_i32 s1, s0, 31
	v_ashrrev_i32_e32 v43, 31, v42
	s_lshl_b64 s[0:1], s[0:1], 11
	s_ashr_i32 s9, s8, 31
	v_lshlrev_b64 v[42:43], 11, v[42:43]
	v_lshl_add_u64 v[78:79], v[132:133], 0, s[0:1]
	s_lshl_b64 s[0:1], s[8:9], 11
	v_lshl_add_u64 v[46:47], v[0:1], 0, v[42:43]
	v_lshl_add_u64 v[86:87], v[132:133], 0, s[0:1]
	global_load_dwordx4 v[42:45], v[46:47], off nt
	s_nop 0
	global_load_dwordx4 v[46:49], v[46:47], off offset:1024 nt
	s_nop 0
	global_load_dwordx4 v[74:77], v[78:79], off nt
	s_nop 0
	global_load_dwordx4 v[78:81], v[78:79], off offset:1024 nt
	s_nop 0
	global_load_dwordx4 v[82:85], v[86:87], off nt
	s_nop 0
	global_load_dwordx4 v[86:89], v[86:87], off offset:1024 nt
	v_readlane_b32 s8, v140, s20
	v_readlane_b32 s9, v140, s21
.LBB0_1455:
	s_waitcnt vmcnt(17)
	v_lshlrev_b32_e32 v164, 16, v90
	v_and_b32_e32 v165, 0xffff0000, v90
	v_lshlrev_b32_e32 v166, 16, v91
	v_and_b32_e32 v167, 0xffff0000, v91
	v_lshlrev_b32_e32 v138, 16, v66
	v_and_b32_e32 v139, 0xffff0000, v66
	v_lshlrev_b32_e32 v150, 16, v67
	v_and_b32_e32 v151, 0xffff0000, v67
	v_pk_mul_f32 v[166:167], s[10:11], v[166:167] op_sel_hi:[0,1]
	v_pk_mul_f32 v[164:165], s[10:11], v[164:165] op_sel_hi:[0,1]
	v_pk_fma_f32 v[138:139], v[138:139], s[6:7], v[164:165] op_sel_hi:[1,0,1]
	v_pk_fma_f32 v[150:151], v[150:151], s[6:7], v[166:167] op_sel_hi:[1,0,1]
	s_waitcnt vmcnt(15)
	v_lshlrev_b32_e32 v164, 16, v98
	v_and_b32_e32 v165, 0xffff0000, v98
	v_lshlrev_b32_e32 v166, 16, v99
	v_and_b32_e32 v167, 0xffff0000, v99
	v_pk_fma_f32 v[150:151], s[10:11], v[166:167], v[150:151] op_sel:[1,0,0]
	v_pk_fma_f32 v[138:139], s[10:11], v[164:165], v[138:139] op_sel:[1,0,0]
	v_lshlrev_b32_e32 v164, 16, v92
	v_and_b32_e32 v165, 0xffff0000, v92
	v_lshlrev_b32_e32 v166, 16, v93
	v_and_b32_e32 v167, 0xffff0000, v93
	v_lshlrev_b32_e32 v152, 16, v68
	v_and_b32_e32 v153, 0xffff0000, v68
	v_lshlrev_b32_e32 v154, 16, v69
	v_and_b32_e32 v155, 0xffff0000, v69
	v_pk_mul_f32 v[166:167], s[10:11], v[166:167] op_sel_hi:[0,1]
	v_pk_mul_f32 v[164:165], s[10:11], v[164:165] op_sel_hi:[0,1]
	v_pk_fma_f32 v[152:153], v[152:153], s[6:7], v[164:165] op_sel_hi:[1,0,1]
	v_pk_fma_f32 v[154:155], v[154:155], s[6:7], v[166:167] op_sel_hi:[1,0,1]
	v_lshlrev_b32_e32 v164, 16, v100
	v_and_b32_e32 v165, 0xffff0000, v100
	v_lshlrev_b32_e32 v166, 16, v101
	v_and_b32_e32 v167, 0xffff0000, v101
	v_pk_fma_f32 v[154:155], s[10:11], v[166:167], v[154:155] op_sel:[1,0,0]
	v_pk_fma_f32 v[164:165], s[10:11], v[164:165], v[152:153] op_sel:[1,0,0]
	v_lshlrev_b32_e32 v152, 16, v94
	v_and_b32_e32 v153, 0xffff0000, v94
	v_lshlrev_b32_e32 v166, 16, v95
	v_and_b32_e32 v167, 0xffff0000, v95
	v_lshlrev_b32_e32 v156, 16, v70
	v_and_b32_e32 v157, 0xffff0000, v70
	v_lshlrev_b32_e32 v158, 16, v71
	v_and_b32_e32 v159, 0xffff0000, v71
	v_pk_mul_f32 v[166:167], s[10:11], v[166:167] op_sel_hi:[0,1]
	v_pk_mul_f32 v[152:153], s[10:11], v[152:153] op_sel_hi:[0,1]
	v_pk_fma_f32 v[152:153], v[156:157], s[6:7], v[152:153] op_sel_hi:[1,0,1]
	v_pk_fma_f32 v[156:157], v[158:159], s[6:7], v[166:167] op_sel_hi:[1,0,1]
	s_waitcnt vmcnt(14)
	v_lshlrev_b32_e32 v158, 16, v102
	v_and_b32_e32 v159, 0xffff0000, v102
	v_lshlrev_b32_e32 v166, 16, v103
	v_and_b32_e32 v167, 0xffff0000, v103
	v_pk_fma_f32 v[166:167], s[10:11], v[166:167], v[156:157] op_sel:[1,0,0]
	v_pk_fma_f32 v[158:159], s[10:11], v[158:159], v[152:153] op_sel:[1,0,0]
	v_lshlrev_b32_e32 v152, 16, v96
	v_and_b32_e32 v153, 0xffff0000, v96
	v_lshlrev_b32_e32 v156, 16, v97
	v_and_b32_e32 v157, 0xffff0000, v97
	v_lshlrev_b32_e32 v160, 16, v72
	v_and_b32_e32 v161, 0xffff0000, v72
	v_lshlrev_b32_e32 v162, 16, v73
	v_and_b32_e32 v163, 0xffff0000, v73
	v_pk_mul_f32 v[156:157], s[10:11], v[156:157] op_sel_hi:[0,1]
	v_pk_mul_f32 v[152:153], s[10:11], v[152:153] op_sel_hi:[0,1]
	v_pk_fma_f32 v[152:153], v[160:161], s[6:7], v[152:153] op_sel_hi:[1,0,1]
	v_pk_fma_f32 v[156:157], v[162:163], s[6:7], v[156:157] op_sel_hi:[1,0,1]
	v_lshlrev_b32_e32 v160, 16, v104
	v_and_b32_e32 v161, 0xffff0000, v104
	v_lshlrev_b32_e32 v162, 16, v105
	v_and_b32_e32 v163, 0xffff0000, v105
	v_pk_fma_f32 v[162:163], s[10:11], v[162:163], v[156:157] op_sel:[1,0,0]
	v_pk_fma_f32 v[168:169], s[10:11], v[160:161], v[152:153] op_sel:[1,0,0]
	v_pk_mov_b32 v[152:153], v[138:139], v[150:151] op_sel:[1,0]
	v_mov_b32_e32 v156, v138
	v_mov_b32_e32 v157, v151
	v_pk_add_f32 v[152:153], v[152:153], v[156:157]
	v_pk_mov_b32 v[156:157], v[164:165], v[154:155] op_sel:[1,0]
	v_mov_b32_e32 v160, v164
	v_mov_b32_e32 v161, v155
	v_pk_add_f32 v[156:157], v[156:157], v[160:161]
	v_add_f32_e32 v149, v152, v153
	v_pk_add_f32 v[156:157], v[156:157], v[156:157] op_sel_hi:[0,1]
	v_add_f32_e32 v153, 0, v149
	v_add_f32_e32 v161, v158, v159
	v_add_f32_e32 v171, v166, v167
	v_mov_b32_e32 v160, v168
	v_mov_b32_e32 v170, v169
	v_mov_b32_e32 v156, v162
	v_mov_b32_e32 v152, v163
	v_pk_add_f32 v[160:161], v[160:161], v[170:171]
	v_pk_add_f32 v[152:153], v[156:157], v[152:153]
	s_cmp_gt_u32 s15, 12
	v_pk_add_f32 v[152:153], v[160:161], v[152:153]
	s_nop 0
	v_add_f32_e32 v149, v152, v153
	s_waitcnt lgkmcnt(0)
	s_nop 1
	v_add_f32_dpp v149, v149, v149 quad_perm:[1,0,3,2] row_mask:0xf bank_mask:0xf
	s_nop 1
	v_add_f32_dpp v149, v149, v149 quad_perm:[2,3,0,1] row_mask:0xf bank_mask:0xf
	s_nop 1
	v_add_f32_dpp v149, v149, v149 row_half_mirror row_mask:0xf bank_mask:0xf
	s_nop 1
	v_add_f32_dpp v149, v149, v149 row_mirror row_mask:0xf bank_mask:0xf
	v_mov_b32_e32 v152, v149
	s_nop 1
	v_permlane16_swap_b32_e32 v149, v152
	v_add_f32_e32 v149, v149, v152
	v_mov_b32_e32 v152, v149
	s_nop 1
	v_permlane32_swap_b32_e32 v149, v152
	v_add_f32_e32 v149, v149, v152
	v_fmamk_f32 v139, v149, 0xba800000, v139
	v_fmac_f32_e32 v138, 0xba800000, v149
	v_fmamk_f32 v151, v149, 0xba800000, v151
	v_fmac_f32_e32 v150, 0xba800000, v149
	v_pk_mul_f32 v[152:153], v[150:151], v[150:151]
	v_pk_mul_f32 v[156:157], v[138:139], v[138:139]
	v_fmamk_f32 v165, v149, 0xba800000, v165
	v_pk_mov_b32 v[160:161], v[156:157], v[152:153] op_sel:[1,0]
	v_mov_b32_e32 v157, v153
	v_pk_add_f32 v[152:153], v[160:161], v[156:157]
	v_fmac_f32_e32 v164, 0xba800000, v149
	v_fmamk_f32 v155, v149, 0xba800000, v155
	v_fmac_f32_e32 v154, 0xba800000, v149
	v_pk_add_f32 v[152:153], v[152:153], v[152:153] op_sel_hi:[0,1]
	v_pk_mul_f32 v[156:157], v[154:155], v[154:155]
	v_pk_mul_f32 v[160:161], v[164:165], v[164:165]
	v_fmac_f32_e32 v158, 0xba800000, v149
	v_pk_mov_b32 v[170:171], v[160:161], v[156:157] op_sel:[1,0]
	v_mov_b32_e32 v161, v157
	v_fmamk_f32 v159, v149, 0xba800000, v159
	v_fmac_f32_e32 v166, 0xba800000, v149
	v_mul_f32_e32 v152, v158, v158
	v_pk_add_f32 v[156:157], v[170:171], v[160:161]
	v_fmamk_f32 v167, v149, 0xba800000, v167
	v_pk_fma_f32 v[160:161], v[158:159], v[158:159], v[152:153] op_sel_hi:[1,1,0]
	v_mul_f32_e32 v152, v166, v166
	v_pk_add_f32 v[156:157], v[156:157], v[156:157] op_sel_hi:[0,1]
	v_pk_fma_f32 v[170:171], v[166:167], v[166:167], v[152:153] op_sel_hi:[1,1,0]
	v_fmamk_f32 v163, v149, 0xba800000, v163
	v_fmac_f32_e32 v162, 0xba800000, v149
	v_fmamk_f32 v169, v149, 0xba800000, v169
	v_fmac_f32_e32 v168, 0xba800000, v149
	v_mul_f32_e32 v160, v168, v168
	v_mul_f32_e32 v170, v169, v169
	v_mul_f32_e32 v152, v162, v162
	v_mul_f32_e32 v156, v163, v163
	v_pk_add_f32 v[160:161], v[160:161], v[170:171]
	v_pk_add_f32 v[152:153], v[152:153], v[156:157]
	s_nop 0
	v_pk_add_f32 v[152:153], v[160:161], v[152:153]
	s_nop 0
	v_add_f32_e32 v149, v152, v153
	s_waitcnt lgkmcnt(0)
	s_nop 1
	v_add_f32_dpp v149, v149, v149 quad_perm:[1,0,3,2] row_mask:0xf bank_mask:0xf
	s_nop 1
	v_add_f32_dpp v149, v149, v149 quad_perm:[2,3,0,1] row_mask:0xf bank_mask:0xf
	s_nop 1
	v_add_f32_dpp v149, v149, v149 row_half_mirror row_mask:0xf bank_mask:0xf
	s_nop 1
	v_add_f32_dpp v149, v149, v149 row_mirror row_mask:0xf bank_mask:0xf
	v_mov_b32_e32 v152, v149
	s_nop 1
	v_permlane16_swap_b32_e32 v149, v152
	v_add_f32_e32 v149, v149, v152
	v_mov_b32_e32 v152, v149
	s_nop 1
	v_permlane32_swap_b32_e32 v149, v152
	v_add_f32_e32 v149, v149, v152
	v_fmamk_f32 v149, v149, 0x3a800000, v131
	v_mul_f32_e32 v152, 0x4f800000, v149
	v_cmp_gt_f32_e32 vcc, s18, v149
	s_nop 1
	v_cndmask_b32_e32 v149, v149, v152, vcc
	v_sqrt_f32_e32 v152, v149
	s_nop 0
	v_add_u32_e32 v153, -1, v152
	v_fma_f32 v156, -v153, v152, v149
	v_cmp_ge_f32_e64 s[0:1], 0, v156
	v_add_u32_e32 v156, 1, v152
	s_nop 0
	v_cndmask_b32_e64 v153, v152, v153, s[0:1]
	v_fma_f32 v152, -v156, v152, v149
	v_cmp_lt_f32_e64 s[0:1], 0, v152
	s_nop 1
	v_cndmask_b32_e64 v152, v153, v156, s[0:1]
	v_mul_f32_e32 v153, 0x37800000, v152
	v_cndmask_b32_e32 v152, v152, v153, vcc
	v_cmp_class_f32_e32 vcc, v149, v148
	s_nop 1
	v_cndmask_b32_e32 v149, v152, v149, vcc
	v_div_scale_f32 v152, s[0:1], v149, v149, 1.0
	v_rcp_f32_e32 v153, v152
	s_nop 0
	v_fma_f32 v156, -v152, v153, 1.0
	v_fmac_f32_e32 v153, v156, v153
	v_div_scale_f32 v156, vcc, 1.0, v149, 1.0
	v_mul_f32_e32 v157, v156, v153
	v_fma_f32 v160, -v152, v157, v156
	v_fmac_f32_e32 v157, v160, v153
	v_fma_f32 v152, -v152, v157, v156
	v_div_fmas_f32 v152, v152, v153, v157
	v_div_fixup_f32 v170, v152, v149, 1.0
	v_pk_mul_f32 v[138:139], v[138:139], v[170:171] op_sel_hi:[1,0]
	v_pk_mul_f32 v[150:151], v[150:151], v[170:171] op_sel_hi:[1,0]
	v_pk_mul_f32 v[154:155], v[154:155], v[170:171] op_sel_hi:[1,0]
	v_pk_fma_f32 v[152:153], v[4:5], v[150:151], v[8:9]
	v_pk_fma_f32 v[150:151], v[2:3], v[138:139], v[6:7]
	v_pk_mul_f32 v[138:139], v[164:165], v[170:171] op_sel_hi:[1,0]
	v_pk_fma_f32 v[156:157], v[16:17], v[154:155], v[28:29]
	v_pk_fma_f32 v[154:155], v[14:15], v[138:139], v[26:27]
	v_pk_mul_f32 v[138:139], v[158:159], v[170:171] op_sel_hi:[1,0]
	v_pk_mul_f32 v[158:159], v[166:167], v[170:171] op_sel_hi:[1,0]
	v_pk_mul_f32 v[162:163], v[162:163], v[170:171] op_sel_hi:[1,0]
	v_pk_fma_f32 v[160:161], v[20:21], v[158:159], v[32:33]
	v_pk_fma_f32 v[158:159], v[18:19], v[138:139], v[30:31]
	v_pk_mul_f32 v[138:139], v[168:169], v[170:171] op_sel_hi:[1,0]
	v_pk_fma_f32 v[164:165], v[12:13], v[162:163], v[24:25]
	v_pk_fma_f32 v[162:163], v[10:11], v[138:139], v[22:23]
	global_store_dwordx4 v[134:135], v[150:153], off nt
	global_store_dwordx4 v[134:135], v[154:157], off offset:16 nt
	global_store_dwordx4 v[134:135], v[158:161], off offset:2048 nt
	global_store_dwordx4 v[134:135], v[162:165], off offset:2064 nt
	s_cbranch_scc1 .LBB0_1450
	s_add_i32 s20, s17, -1
	v_readlane_b32 s0, v141, s20
	v_add3_u32 v66, v130, s15, 3
	v_readlane_b32 s10, v141, s17
	s_ashr_i32 s1, s0, 31
	v_ashrrev_i32_e32 v67, 31, v66
	s_lshl_b64 s[0:1], s[0:1], 11
	s_ashr_i32 s11, s10, 31
	v_lshlrev_b64 v[66:67], 11, v[66:67]
	v_lshl_add_u64 v[94:95], v[132:133], 0, s[0:1]
	s_lshl_b64 s[0:1], s[10:11], 11
	v_lshl_add_u64 v[70:71], v[0:1], 0, v[66:67]
	v_lshl_add_u64 v[102:103], v[132:133], 0, s[0:1]
	global_load_dwordx4 v[66:69], v[70:71], off nt
	s_nop 0
	global_load_dwordx4 v[70:73], v[70:71], off offset:1024 nt
	s_nop 0
	global_load_dwordx4 v[90:93], v[94:95], off nt
	s_nop 0
	global_load_dwordx4 v[94:97], v[94:95], off offset:1024 nt
	s_nop 0
	global_load_dwordx4 v[98:101], v[102:103], off nt
	s_nop 0
	global_load_dwordx4 v[102:105], v[102:103], off offset:1024 nt
	v_readlane_b32 s10, v140, s20
	v_readlane_b32 s11, v140, s17
	s_branch .LBB0_1450
